# as previous but GEMM trailing barrier moved up by 8 (f16) / 4 (fp8) MFMAs
# baseline (speedup 1.0000x reference)
.LBB0_410:
	ds_read_b128 v[152:155], v148
	ds_read_b128 v[156:159], v148 offset:1024
	ds_read_b128 v[160:163], v148 offset:2048
	ds_read_b128 v[164:167], v148 offset:3072
	ds_read_b128 v[168:171], v149
	ds_read_b128 v[172:175], v149 offset:1024
	ds_read_b128 v[176:179], v149 offset:2048
	ds_read_b128 v[180:183], v149 offset:3072
	s_add_u32 s28, s26, 0xfff80080
	s_addc_u32 s29, s27, -1
	s_cmp_eq_u32 s64, 28
	s_cselect_b32 s31, s21, s29
	s_cselect_b32 s30, s60, s28
	s_cselect_b32 s29, s19, s63
	s_cselect_b32 s28, s61, s62
	v_lshl_add_u64 v[184:185], s[26:27], 0, v[138:139]
	s_add_i32 m0, s17, 0xc000
	ds_read_b128 v[188:191], v150
	ds_read_b128 v[192:195], v150 offset:1024
	ds_read_b128 v[196:199], v150 offset:2048
	ds_read_b128 v[200:203], v150 offset:3072
	ds_read_b128 v[204:207], v150 offset:4096
	ds_read_b128 v[208:211], v150 offset:5120
	ds_read_b128 v[212:215], v150 offset:6144
	ds_read_b128 v[216:219], v150 offset:7168
	global_load_lds_dwordx4 v[184:185], off
	v_lshl_add_u64 v[184:185], s[26:27], 0, v[140:141]
	s_add_i32 m0, s17, 0xe000
	s_nop 0
	global_load_lds_dwordx4 v[184:185], off
	s_waitcnt vmcnt(8)
	s_waitcnt lgkmcnt(0)
	s_barrier
	s_setprio 1
	s_waitcnt lgkmcnt(0)
	v_mfma_f32_16x16x32_f16 v[126:129], v[152:155], v[188:191], v[126:129]
	v_mfma_f32_16x16x32_f16 v[122:125], v[160:163], v[188:191], v[122:125]
	v_mfma_f32_16x16x32_f16 v[118:121], v[152:155], v[196:199], v[118:121]
	v_mfma_f32_16x16x32_f16 v[114:117], v[160:163], v[196:199], v[114:117]
	v_mfma_f32_16x16x32_f16 v[102:105], v[152:155], v[204:207], v[102:105]
	v_mfma_f32_16x16x32_f16 v[98:101], v[160:163], v[204:207], v[98:101]
	v_mfma_f32_16x16x32_f16 v[86:89], v[152:155], v[212:215], v[86:89]
	v_mfma_f32_16x16x32_f16 v[82:85], v[160:163], v[212:215], v[82:85]
	v_mfma_f32_16x16x32_f16 v[126:129], v[156:159], v[192:195], v[126:129]
	v_mfma_f32_16x16x32_f16 v[122:125], v[164:167], v[192:195], v[122:125]
	v_mfma_f32_16x16x32_f16 v[118:121], v[156:159], v[200:203], v[118:121]
	v_mfma_f32_16x16x32_f16 v[114:117], v[164:167], v[200:203], v[114:117]
	v_mfma_f32_16x16x32_f16 v[102:105], v[156:159], v[208:211], v[102:105]
	v_mfma_f32_16x16x32_f16 v[98:101], v[164:167], v[208:211], v[98:101]
	v_mfma_f32_16x16x32_f16 v[86:89], v[156:159], v[216:219], v[86:89]
	v_mfma_f32_16x16x32_f16 v[82:85], v[164:167], v[216:219], v[82:85]
	s_setprio 0
	s_setprio 1
	v_mfma_f32_16x16x32_f16 v[110:113], v[168:171], v[188:191], v[110:113]
	v_mfma_f32_16x16x32_f16 v[106:109], v[176:179], v[188:191], v[106:109]
	v_mfma_f32_16x16x32_f16 v[94:97], v[168:171], v[196:199], v[94:97]
	v_mfma_f32_16x16x32_f16 v[90:93], v[176:179], v[196:199], v[90:93]
	v_mfma_f32_16x16x32_f16 v[78:81], v[168:171], v[204:207], v[78:81]
	v_mfma_f32_16x16x32_f16 v[74:77], v[176:179], v[204:207], v[74:77]
	v_mfma_f32_16x16x32_f16 v[70:73], v[168:171], v[212:215], v[70:73]
	v_mfma_f32_16x16x32_f16 v[66:69], v[176:179], v[212:215], v[66:69]
	s_setprio 2
	s_barrier
	v_mfma_f32_16x16x32_f16 v[110:113], v[172:175], v[192:195], v[110:113]
	v_mfma_f32_16x16x32_f16 v[106:109], v[180:183], v[192:195], v[106:109]
	v_mfma_f32_16x16x32_f16 v[94:97], v[172:175], v[200:203], v[94:97]
	v_mfma_f32_16x16x32_f16 v[90:93], v[180:183], v[200:203], v[90:93]
	v_mfma_f32_16x16x32_f16 v[78:81], v[172:175], v[208:211], v[78:81]
	v_mfma_f32_16x16x32_f16 v[74:77], v[180:183], v[208:211], v[74:77]
	v_mfma_f32_16x16x32_f16 v[70:73], v[172:175], v[216:219], v[70:73]
	v_mfma_f32_16x16x32_f16 v[66:69], v[180:183], v[216:219], v[66:69]
	s_setprio 0
	s_nop 0
	s_add_i32 s65, s48, s34
	v_lshl_add_u64 v[184:185], s[28:29], 0, v[134:135]
	s_mov_b32 m0, s65
	ds_read_b128 v[188:191], v150 offset:16384
	ds_read_b128 v[192:195], v150 offset:17408
	ds_read_b128 v[196:199], v150 offset:18432
	ds_read_b128 v[200:203], v150 offset:19456
	ds_read_b128 v[204:207], v150 offset:20480
	ds_read_b128 v[208:211], v150 offset:21504
	ds_read_b128 v[212:215], v150 offset:22528
	ds_read_b128 v[216:219], v150 offset:23552
	global_load_lds_dwordx4 v[184:185], off
	s_add_i32 m0, s65, 0x2000
	s_add_u32 s66, s28, 0x80000
	v_lshl_add_u64 v[220:221], s[28:29], 0, v[130:131]
	s_addc_u32 s67, s29, 0
	s_add_i32 s65, s49, s34
	global_load_lds_dwordx4 v[220:221], off
	v_lshl_add_u64 v[222:223], s[66:67], 0, v[134:135]
	s_mov_b32 m0, s65
	v_lshl_add_u64 v[224:225], s[30:31], 0, v[132:133]
	global_load_lds_dwordx4 v[222:223], off
	v_lshl_add_u64 v[222:223], s[66:67], 0, v[130:131]
	s_add_i32 m0, s65, 0x2000
	s_nop 0
	global_load_lds_dwordx4 v[222:223], off
	v_lshl_add_u64 v[222:223], s[30:31], 0, v[136:137]
	s_mov_b32 m0, s17
	s_nop 0
	global_load_lds_dwordx4 v[222:223], off
	s_mov_b32 m0, s37
	s_nop 0
	global_load_lds_dwordx4 v[224:225], off
	s_waitcnt vmcnt(8)
	s_waitcnt lgkmcnt(0)
	s_barrier
	s_setprio 1
	s_waitcnt lgkmcnt(0)
	v_mfma_f32_16x16x32_f16 v[62:65], v[152:155], v[188:191], v[62:65]
	v_mfma_f32_16x16x32_f16 v[58:61], v[160:163], v[188:191], v[58:61]
	v_mfma_f32_16x16x32_f16 v[54:57], v[152:155], v[196:199], v[54:57]
	v_mfma_f32_16x16x32_f16 v[50:53], v[160:163], v[196:199], v[50:53]
	v_mfma_f32_16x16x32_f16 v[38:41], v[152:155], v[204:207], v[38:41]
	v_mfma_f32_16x16x32_f16 v[34:37], v[160:163], v[204:207], v[34:37]
	v_mfma_f32_16x16x32_f16 v[22:25], v[152:155], v[212:215], v[22:25]
	v_mfma_f32_16x16x32_f16 v[18:21], v[160:163], v[212:215], v[18:21]
	v_mfma_f32_16x16x32_f16 v[62:65], v[156:159], v[192:195], v[62:65]
	v_mfma_f32_16x16x32_f16 v[58:61], v[164:167], v[192:195], v[58:61]
	v_mfma_f32_16x16x32_f16 v[54:57], v[156:159], v[200:203], v[54:57]
	v_mfma_f32_16x16x32_f16 v[50:53], v[164:167], v[200:203], v[50:53]
	v_mfma_f32_16x16x32_f16 v[38:41], v[156:159], v[208:211], v[38:41]
	v_mfma_f32_16x16x32_f16 v[34:37], v[164:167], v[208:211], v[34:37]
	v_mfma_f32_16x16x32_f16 v[22:25], v[156:159], v[216:219], v[22:25]
	v_mfma_f32_16x16x32_f16 v[18:21], v[164:167], v[216:219], v[18:21]
	s_setprio 0
	s_setprio 1
	v_mfma_f32_16x16x32_f16 v[46:49], v[168:171], v[188:191], v[46:49]
	v_mfma_f32_16x16x32_f16 v[42:45], v[176:179], v[188:191], v[42:45]
	v_mfma_f32_16x16x32_f16 v[30:33], v[168:171], v[196:199], v[30:33]
	v_mfma_f32_16x16x32_f16 v[26:29], v[176:179], v[196:199], v[26:29]
	v_mfma_f32_16x16x32_f16 v[14:17], v[168:171], v[204:207], v[14:17]
	v_mfma_f32_16x16x32_f16 v[10:13], v[176:179], v[204:207], v[10:13]
	v_mfma_f32_16x16x32_f16 v[6:9], v[168:171], v[212:215], v[6:9]
	v_mfma_f32_16x16x32_f16 v[2:5], v[176:179], v[212:215], v[2:5]
	s_setprio 2
	s_barrier
	v_mfma_f32_16x16x32_f16 v[46:49], v[172:175], v[192:195], v[46:49]
	v_mfma_f32_16x16x32_f16 v[42:45], v[180:183], v[192:195], v[42:45]
	v_mfma_f32_16x16x32_f16 v[30:33], v[172:175], v[200:203], v[30:33]
	v_mfma_f32_16x16x32_f16 v[26:29], v[180:183], v[200:203], v[26:29]
	v_mfma_f32_16x16x32_f16 v[14:17], v[172:175], v[208:211], v[14:17]
	v_mfma_f32_16x16x32_f16 v[10:13], v[180:183], v[208:211], v[10:13]
	v_mfma_f32_16x16x32_f16 v[6:9], v[172:175], v[216:219], v[6:9]
	v_mfma_f32_16x16x32_f16 v[2:5], v[180:183], v[216:219], v[2:5]
	s_setprio 0
	s_nop 0
	s_add_i32 s65, 0, 0x18000
	v_add_u32_e32 v151, s65, v146
	s_add_i32 s66, 0, 0x1c000
	ds_read_b128 v[152:155], v151
	ds_read_b128 v[156:159], v151 offset:1024
	ds_read_b128 v[160:163], v151 offset:2048
	ds_read_b128 v[164:167], v151 offset:3072
	v_add_u32_e32 v151, s66, v146
	ds_read_b128 v[168:171], v151
	ds_read_b128 v[172:175], v151 offset:1024
	ds_read_b128 v[176:179], v151 offset:2048
	ds_read_b128 v[180:183], v151 offset:3072
	s_add_u32 s30, s30, 0x80000
	s_addc_u32 s31, s31, 0
	s_mov_b32 m0, s38
	v_lshl_add_u64 v[226:227], s[30:31], 0, v[136:137]
	ds_read_b128 v[188:191], v150 offset:32768
	ds_read_b128 v[192:195], v150 offset:33792
	ds_read_b128 v[196:199], v150 offset:34816
	ds_read_b128 v[200:203], v150 offset:35840
	ds_read_b128 v[204:207], v150 offset:36864
	ds_read_b128 v[208:211], v150 offset:37888
	ds_read_b128 v[212:215], v150 offset:38912
	ds_read_b128 v[216:219], v150 offset:39936
	global_load_lds_dwordx4 v[226:227], off
	v_lshl_add_u64 v[226:227], s[30:31], 0, v[132:133]
	s_mov_b32 m0, s39
	s_nop 0
	global_load_lds_dwordx4 v[226:227], off
	s_waitcnt vmcnt(8)
	s_waitcnt lgkmcnt(0)
	s_barrier
	s_setprio 1
	s_waitcnt lgkmcnt(0)
	v_mfma_f32_16x16x32_f16 v[126:129], v[152:155], v[188:191], v[126:129]
	v_mfma_f32_16x16x32_f16 v[122:125], v[160:163], v[188:191], v[122:125]
	v_mfma_f32_16x16x32_f16 v[118:121], v[152:155], v[196:199], v[118:121]
	v_mfma_f32_16x16x32_f16 v[114:117], v[160:163], v[196:199], v[114:117]
	v_mfma_f32_16x16x32_f16 v[102:105], v[152:155], v[204:207], v[102:105]
	v_mfma_f32_16x16x32_f16 v[98:101], v[160:163], v[204:207], v[98:101]
	v_mfma_f32_16x16x32_f16 v[86:89], v[152:155], v[212:215], v[86:89]
	v_mfma_f32_16x16x32_f16 v[82:85], v[160:163], v[212:215], v[82:85]
	v_mfma_f32_16x16x32_f16 v[126:129], v[156:159], v[192:195], v[126:129]
	v_mfma_f32_16x16x32_f16 v[122:125], v[164:167], v[192:195], v[122:125]
	v_mfma_f32_16x16x32_f16 v[118:121], v[156:159], v[200:203], v[118:121]
	v_mfma_f32_16x16x32_f16 v[114:117], v[164:167], v[200:203], v[114:117]
	v_mfma_f32_16x16x32_f16 v[102:105], v[156:159], v[208:211], v[102:105]
	v_mfma_f32_16x16x32_f16 v[98:101], v[164:167], v[208:211], v[98:101]
	v_mfma_f32_16x16x32_f16 v[86:89], v[156:159], v[216:219], v[86:89]
	v_mfma_f32_16x16x32_f16 v[82:85], v[164:167], v[216:219], v[82:85]
	s_setprio 0
	s_setprio 1
	v_mfma_f32_16x16x32_f16 v[110:113], v[168:171], v[188:191], v[110:113]
	v_mfma_f32_16x16x32_f16 v[106:109], v[176:179], v[188:191], v[106:109]
	v_mfma_f32_16x16x32_f16 v[94:97], v[168:171], v[196:199], v[94:97]
	v_mfma_f32_16x16x32_f16 v[90:93], v[176:179], v[196:199], v[90:93]
	v_mfma_f32_16x16x32_f16 v[78:81], v[168:171], v[204:207], v[78:81]
	v_mfma_f32_16x16x32_f16 v[74:77], v[176:179], v[204:207], v[74:77]
	v_mfma_f32_16x16x32_f16 v[70:73], v[168:171], v[212:215], v[70:73]
	v_mfma_f32_16x16x32_f16 v[66:69], v[176:179], v[212:215], v[66:69]
	s_setprio 2
	s_barrier
	v_mfma_f32_16x16x32_f16 v[110:113], v[172:175], v[192:195], v[110:113]
	v_mfma_f32_16x16x32_f16 v[106:109], v[180:183], v[192:195], v[106:109]
	v_mfma_f32_16x16x32_f16 v[94:97], v[172:175], v[200:203], v[94:97]
	v_mfma_f32_16x16x32_f16 v[90:93], v[180:183], v[200:203], v[90:93]
	v_mfma_f32_16x16x32_f16 v[78:81], v[172:175], v[208:211], v[78:81]
	v_mfma_f32_16x16x32_f16 v[74:77], v[180:183], v[208:211], v[74:77]
	v_mfma_f32_16x16x32_f16 v[70:73], v[172:175], v[216:219], v[70:73]
	v_mfma_f32_16x16x32_f16 v[66:69], v[180:183], v[216:219], v[66:69]
	s_setprio 0
	s_nop 0
	s_add_i32 s30, s65, s34
	v_lshl_add_u64 v[184:185], v[184:185], 0, s[12:13]
	s_mov_b32 m0, s30
	ds_read_b128 v[188:191], v150 offset:49152
	ds_read_b128 v[192:195], v150 offset:50176
	ds_read_b128 v[196:199], v150 offset:51200
	ds_read_b128 v[200:203], v150 offset:52224
	ds_read_b128 v[204:207], v150 offset:53248
	ds_read_b128 v[208:211], v150 offset:54272
	ds_read_b128 v[212:215], v150 offset:55296
	ds_read_b128 v[216:219], v150 offset:56320
	global_load_lds_dwordx4 v[184:185], off
	s_add_i32 m0, s30, 0x2000
	s_add_u32 s28, s28, 0x80080
	v_lshl_add_u64 v[184:185], v[220:221], 0, s[12:13]
	s_addc_u32 s29, s29, 0
	s_add_i32 s30, s66, s34
	global_load_lds_dwordx4 v[184:185], off
	v_lshl_add_u64 v[184:185], s[28:29], 0, v[134:135]
	s_mov_b32 m0, s30
	s_nop 0
	global_load_lds_dwordx4 v[184:185], off
	v_lshl_add_u64 v[184:185], s[28:29], 0, v[130:131]
	s_add_i32 m0, s30, 0x2000
	s_nop 0
	global_load_lds_dwordx4 v[184:185], off
	v_lshl_add_u64 v[184:185], v[222:223], 0, s[12:13]
	s_mov_b32 m0, s41
	s_nop 0
	global_load_lds_dwordx4 v[184:185], off
	v_lshl_add_u64 v[184:185], v[224:225], 0, s[12:13]
	s_mov_b32 m0, s46
	s_nop 0
	global_load_lds_dwordx4 v[184:185], off
	s_waitcnt vmcnt(8)
	s_waitcnt lgkmcnt(0)
	s_barrier
	s_setprio 1
	s_waitcnt lgkmcnt(0)
	v_mfma_f32_16x16x32_f16 v[62:65], v[152:155], v[188:191], v[62:65]
	v_mfma_f32_16x16x32_f16 v[58:61], v[160:163], v[188:191], v[58:61]
	v_mfma_f32_16x16x32_f16 v[54:57], v[152:155], v[196:199], v[54:57]
	v_mfma_f32_16x16x32_f16 v[50:53], v[160:163], v[196:199], v[50:53]
	v_mfma_f32_16x16x32_f16 v[38:41], v[152:155], v[204:207], v[38:41]
	v_mfma_f32_16x16x32_f16 v[34:37], v[160:163], v[204:207], v[34:37]
	v_mfma_f32_16x16x32_f16 v[22:25], v[152:155], v[212:215], v[22:25]
	v_mfma_f32_16x16x32_f16 v[18:21], v[160:163], v[212:215], v[18:21]
	v_mfma_f32_16x16x32_f16 v[62:65], v[156:159], v[192:195], v[62:65]
	v_mfma_f32_16x16x32_f16 v[58:61], v[164:167], v[192:195], v[58:61]
	v_mfma_f32_16x16x32_f16 v[54:57], v[156:159], v[200:203], v[54:57]
	v_mfma_f32_16x16x32_f16 v[50:53], v[164:167], v[200:203], v[50:53]
	v_mfma_f32_16x16x32_f16 v[38:41], v[156:159], v[208:211], v[38:41]
	v_mfma_f32_16x16x32_f16 v[34:37], v[164:167], v[208:211], v[34:37]
	v_mfma_f32_16x16x32_f16 v[22:25], v[156:159], v[216:219], v[22:25]
	v_mfma_f32_16x16x32_f16 v[18:21], v[164:167], v[216:219], v[18:21]
	s_setprio 0
	s_setprio 1
	v_mfma_f32_16x16x32_f16 v[46:49], v[168:171], v[188:191], v[46:49]
	v_mfma_f32_16x16x32_f16 v[42:45], v[176:179], v[188:191], v[42:45]
	v_mfma_f32_16x16x32_f16 v[30:33], v[168:171], v[196:199], v[30:33]
	v_mfma_f32_16x16x32_f16 v[26:29], v[176:179], v[196:199], v[26:29]
	v_mfma_f32_16x16x32_f16 v[14:17], v[168:171], v[204:207], v[14:17]
	v_mfma_f32_16x16x32_f16 v[10:13], v[176:179], v[204:207], v[10:13]
	v_mfma_f32_16x16x32_f16 v[6:9], v[168:171], v[212:215], v[6:9]
	v_mfma_f32_16x16x32_f16 v[2:5], v[176:179], v[212:215], v[2:5]
	s_setprio 2
	s_barrier
	v_mfma_f32_16x16x32_f16 v[46:49], v[172:175], v[192:195], v[46:49]
	v_mfma_f32_16x16x32_f16 v[42:45], v[180:183], v[192:195], v[42:45]
	v_mfma_f32_16x16x32_f16 v[30:33], v[172:175], v[200:203], v[30:33]
	v_mfma_f32_16x16x32_f16 v[26:29], v[180:183], v[200:203], v[26:29]
	v_mfma_f32_16x16x32_f16 v[14:17], v[172:175], v[208:211], v[14:17]
	v_mfma_f32_16x16x32_f16 v[10:13], v[180:183], v[208:211], v[10:13]
	v_mfma_f32_16x16x32_f16 v[6:9], v[172:175], v[216:219], v[6:9]
	v_mfma_f32_16x16x32_f16 v[2:5], v[180:183], v[216:219], v[2:5]
	s_setprio 0
	s_nop 0
	s_add_i32 s64, s64, 2
	s_add_u32 s26, s26, 0x100
	s_addc_u32 s27, s27, 0
	s_add_u32 s62, s62, 0x100
	s_addc_u32 s63, s63, 0
	s_cmp_gt_u32 s64, 29
	s_cbranch_scc0 .LBB0_410
	s_and_b64 vcc, exec, s[14:15]
	s_cbranch_vccz .LBB0_413
	s_barrier

.LBB0_628:
	ds_read_b128 v[146:149], v154
	ds_read_b128 v[158:161], v154 offset:1024
	ds_read_b128 v[162:165], v154 offset:2048
	ds_read_b128 v[166:169], v154 offset:3072
	ds_read_b128 v[170:173], v155
	ds_read_b128 v[174:177], v155 offset:1024
	ds_read_b128 v[178:181], v155 offset:2048
	ds_read_b128 v[182:185], v155 offset:3072
	s_add_u32 s28, s26, 0xfff80080
	s_addc_u32 s29, s27, -1
	s_cmp_eq_u32 s63, 28
	s_cselect_b32 s31, s19, s29
	s_cselect_b32 s30, s51, s28
	s_cselect_b32 s29, s17, s62
	s_cselect_b32 s28, s60, s61
	v_lshl_add_u64 v[150:151], s[26:27], 0, v[138:139]
	s_add_i32 m0, s25, 0xc000
	ds_read_b128 v[188:191], v156
	ds_read_b128 v[192:195], v156 offset:1024
	ds_read_b128 v[196:199], v156 offset:2048
	ds_read_b128 v[200:203], v156 offset:3072
	ds_read_b128 v[204:207], v156 offset:4096
	ds_read_b128 v[208:211], v156 offset:5120
	ds_read_b128 v[212:215], v156 offset:6144
	ds_read_b128 v[216:219], v156 offset:7168
	global_load_lds_dwordx4 v[150:151], off
	v_lshl_add_u64 v[150:151], s[26:27], 0, v[140:141]
	s_add_i32 m0, s25, 0xe000
	s_nop 0
	global_load_lds_dwordx4 v[150:151], off
	s_waitcnt vmcnt(8)
	s_waitcnt lgkmcnt(0)
	s_barrier
	s_setprio 1
	s_waitcnt lgkmcnt(0)
	v_mfma_f32_16x16x32_f16 v[126:129], v[146:149], v[188:191], v[126:129]
	v_mfma_f32_16x16x32_f16 v[122:125], v[162:165], v[188:191], v[122:125]
	v_mfma_f32_16x16x32_f16 v[110:113], v[146:149], v[196:199], v[110:113]
	v_mfma_f32_16x16x32_f16 v[106:109], v[162:165], v[196:199], v[106:109]
	v_mfma_f32_16x16x32_f16 v[94:97], v[146:149], v[204:207], v[94:97]
	v_mfma_f32_16x16x32_f16 v[90:93], v[162:165], v[204:207], v[90:93]
	v_mfma_f32_16x16x32_f16 v[78:81], v[146:149], v[212:215], v[78:81]
	v_mfma_f32_16x16x32_f16 v[74:77], v[162:165], v[212:215], v[74:77]
	v_mfma_f32_16x16x32_f16 v[126:129], v[158:161], v[192:195], v[126:129]
	v_mfma_f32_16x16x32_f16 v[122:125], v[166:169], v[192:195], v[122:125]
	v_mfma_f32_16x16x32_f16 v[110:113], v[158:161], v[200:203], v[110:113]
	v_mfma_f32_16x16x32_f16 v[106:109], v[166:169], v[200:203], v[106:109]
	v_mfma_f32_16x16x32_f16 v[94:97], v[158:161], v[208:211], v[94:97]
	v_mfma_f32_16x16x32_f16 v[90:93], v[166:169], v[208:211], v[90:93]
	v_mfma_f32_16x16x32_f16 v[78:81], v[158:161], v[216:219], v[78:81]
	v_mfma_f32_16x16x32_f16 v[74:77], v[166:169], v[216:219], v[74:77]
	s_setprio 0
	s_setprio 1
	v_mfma_f32_16x16x32_f16 v[118:121], v[170:173], v[188:191], v[118:121]
	v_mfma_f32_16x16x32_f16 v[114:117], v[178:181], v[188:191], v[114:117]
	v_mfma_f32_16x16x32_f16 v[102:105], v[170:173], v[196:199], v[102:105]
	v_mfma_f32_16x16x32_f16 v[98:101], v[178:181], v[196:199], v[98:101]
	v_mfma_f32_16x16x32_f16 v[86:89], v[170:173], v[204:207], v[86:89]
	v_mfma_f32_16x16x32_f16 v[82:85], v[178:181], v[204:207], v[82:85]
	v_mfma_f32_16x16x32_f16 v[70:73], v[170:173], v[212:215], v[70:73]
	v_mfma_f32_16x16x32_f16 v[66:69], v[178:181], v[212:215], v[66:69]
	s_setprio 2
	s_barrier
	v_mfma_f32_16x16x32_f16 v[118:121], v[174:177], v[192:195], v[118:121]
	v_mfma_f32_16x16x32_f16 v[114:117], v[182:185], v[192:195], v[114:117]
	v_mfma_f32_16x16x32_f16 v[102:105], v[174:177], v[200:203], v[102:105]
	v_mfma_f32_16x16x32_f16 v[98:101], v[182:185], v[200:203], v[98:101]
	v_mfma_f32_16x16x32_f16 v[86:89], v[174:177], v[208:211], v[86:89]
	v_mfma_f32_16x16x32_f16 v[82:85], v[182:185], v[208:211], v[82:85]
	v_mfma_f32_16x16x32_f16 v[70:73], v[174:177], v[216:219], v[70:73]
	v_mfma_f32_16x16x32_f16 v[66:69], v[182:185], v[216:219], v[66:69]
	s_setprio 0
	s_nop 0
	s_add_i32 s64, s48, s36
	v_lshl_add_u64 v[150:151], s[28:29], 0, v[132:133]
	s_mov_b32 m0, s64
	ds_read_b128 v[188:191], v156 offset:16384
	ds_read_b128 v[192:195], v156 offset:17408
	ds_read_b128 v[196:199], v156 offset:18432
	ds_read_b128 v[200:203], v156 offset:19456
	ds_read_b128 v[204:207], v156 offset:20480
	ds_read_b128 v[208:211], v156 offset:21504
	ds_read_b128 v[212:215], v156 offset:22528
	ds_read_b128 v[216:219], v156 offset:23552
	global_load_lds_dwordx4 v[150:151], off
	s_add_i32 m0, s64, 0x2000
	s_add_u32 s64, s28, 0x80000
	v_lshl_add_u64 v[220:221], s[28:29], 0, v[136:137]
	s_addc_u32 s65, s29, 0
	s_add_i32 s66, s49, s36
	global_load_lds_dwordx4 v[220:221], off
	v_lshl_add_u64 v[222:223], s[64:65], 0, v[132:133]
	s_mov_b32 m0, s66
	v_lshl_add_u64 v[224:225], s[30:31], 0, v[134:135]
	global_load_lds_dwordx4 v[222:223], off
	v_lshl_add_u64 v[222:223], s[64:65], 0, v[136:137]
	s_add_i32 m0, s66, 0x2000
	s_nop 0
	global_load_lds_dwordx4 v[222:223], off
	v_lshl_add_u64 v[222:223], s[30:31], 0, v[130:131]
	s_mov_b32 m0, s25
	s_nop 0
	global_load_lds_dwordx4 v[222:223], off
	s_mov_b32 m0, s37
	s_nop 0
	global_load_lds_dwordx4 v[224:225], off
	s_waitcnt vmcnt(8)
	s_waitcnt lgkmcnt(0)
	s_barrier
	s_setprio 1
	s_waitcnt lgkmcnt(0)
	v_mfma_f32_16x16x32_f16 v[62:65], v[146:149], v[188:191], v[62:65]
	v_mfma_f32_16x16x32_f16 v[58:61], v[162:165], v[188:191], v[58:61]
	v_mfma_f32_16x16x32_f16 v[46:49], v[146:149], v[196:199], v[46:49]
	v_mfma_f32_16x16x32_f16 v[42:45], v[162:165], v[196:199], v[42:45]
	v_mfma_f32_16x16x32_f16 v[30:33], v[146:149], v[204:207], v[30:33]
	v_mfma_f32_16x16x32_f16 v[26:29], v[162:165], v[204:207], v[26:29]
	v_mfma_f32_16x16x32_f16 v[14:17], v[146:149], v[212:215], v[14:17]
	v_mfma_f32_16x16x32_f16 v[10:13], v[162:165], v[212:215], v[10:13]
	v_mfma_f32_16x16x32_f16 v[62:65], v[158:161], v[192:195], v[62:65]
	v_mfma_f32_16x16x32_f16 v[58:61], v[166:169], v[192:195], v[58:61]
	v_mfma_f32_16x16x32_f16 v[46:49], v[158:161], v[200:203], v[46:49]
	v_mfma_f32_16x16x32_f16 v[42:45], v[166:169], v[200:203], v[42:45]
	v_mfma_f32_16x16x32_f16 v[30:33], v[158:161], v[208:211], v[30:33]
	v_mfma_f32_16x16x32_f16 v[26:29], v[166:169], v[208:211], v[26:29]
	v_mfma_f32_16x16x32_f16 v[14:17], v[158:161], v[216:219], v[14:17]
	v_mfma_f32_16x16x32_f16 v[10:13], v[166:169], v[216:219], v[10:13]
	s_setprio 0
	s_setprio 1
	v_mfma_f32_16x16x32_f16 v[54:57], v[170:173], v[188:191], v[54:57]
	v_mfma_f32_16x16x32_f16 v[50:53], v[178:181], v[188:191], v[50:53]
	v_mfma_f32_16x16x32_f16 v[38:41], v[170:173], v[196:199], v[38:41]
	v_mfma_f32_16x16x32_f16 v[34:37], v[178:181], v[196:199], v[34:37]
	v_mfma_f32_16x16x32_f16 v[22:25], v[170:173], v[204:207], v[22:25]
	v_mfma_f32_16x16x32_f16 v[18:21], v[178:181], v[204:207], v[18:21]
	v_mfma_f32_16x16x32_f16 v[6:9], v[170:173], v[212:215], v[6:9]
	v_mfma_f32_16x16x32_f16 v[2:5], v[178:181], v[212:215], v[2:5]
	s_setprio 2
	s_barrier
	v_mfma_f32_16x16x32_f16 v[54:57], v[174:177], v[192:195], v[54:57]
	v_mfma_f32_16x16x32_f16 v[50:53], v[182:185], v[192:195], v[50:53]
	v_mfma_f32_16x16x32_f16 v[38:41], v[174:177], v[200:203], v[38:41]
	v_mfma_f32_16x16x32_f16 v[34:37], v[182:185], v[200:203], v[34:37]
	v_mfma_f32_16x16x32_f16 v[22:25], v[174:177], v[208:211], v[22:25]
	v_mfma_f32_16x16x32_f16 v[18:21], v[182:185], v[208:211], v[18:21]
	v_mfma_f32_16x16x32_f16 v[6:9], v[174:177], v[216:219], v[6:9]
	v_mfma_f32_16x16x32_f16 v[2:5], v[182:185], v[216:219], v[2:5]
	s_setprio 0
	s_nop 0
	s_add_i32 s64, 0, 0x18000
	v_add_u32_e32 v157, s64, v152
	s_add_i32 s65, 0, 0x1c000
	ds_read_b128 v[146:149], v157
	ds_read_b128 v[158:161], v157 offset:1024
	ds_read_b128 v[162:165], v157 offset:2048
	ds_read_b128 v[166:169], v157 offset:3072
	v_add_u32_e32 v157, s65, v152
	ds_read_b128 v[170:173], v157
	ds_read_b128 v[174:177], v157 offset:1024
	ds_read_b128 v[178:181], v157 offset:2048
	ds_read_b128 v[182:185], v157 offset:3072
	s_add_u32 s30, s30, 0x80000
	s_addc_u32 s31, s31, 0
	s_mov_b32 m0, s38
	v_lshl_add_u64 v[226:227], s[30:31], 0, v[130:131]
	ds_read_b128 v[188:191], v156 offset:32768
	ds_read_b128 v[192:195], v156 offset:33792
	ds_read_b128 v[196:199], v156 offset:34816
	ds_read_b128 v[200:203], v156 offset:35840
	ds_read_b128 v[204:207], v156 offset:36864
	ds_read_b128 v[208:211], v156 offset:37888
	ds_read_b128 v[212:215], v156 offset:38912
	ds_read_b128 v[216:219], v156 offset:39936
	global_load_lds_dwordx4 v[226:227], off
	v_lshl_add_u64 v[226:227], s[30:31], 0, v[134:135]
	s_mov_b32 m0, s39
	s_nop 0
	global_load_lds_dwordx4 v[226:227], off
	s_waitcnt vmcnt(8)
	s_waitcnt lgkmcnt(0)
	s_barrier
	s_setprio 1
	s_waitcnt lgkmcnt(0)
	v_mfma_f32_16x16x32_f16 v[126:129], v[146:149], v[188:191], v[126:129]
	v_mfma_f32_16x16x32_f16 v[122:125], v[162:165], v[188:191], v[122:125]
	v_mfma_f32_16x16x32_f16 v[110:113], v[146:149], v[196:199], v[110:113]
	v_mfma_f32_16x16x32_f16 v[106:109], v[162:165], v[196:199], v[106:109]
	v_mfma_f32_16x16x32_f16 v[94:97], v[146:149], v[204:207], v[94:97]
	v_mfma_f32_16x16x32_f16 v[90:93], v[162:165], v[204:207], v[90:93]
	v_mfma_f32_16x16x32_f16 v[78:81], v[146:149], v[212:215], v[78:81]
	v_mfma_f32_16x16x32_f16 v[74:77], v[162:165], v[212:215], v[74:77]
	v_mfma_f32_16x16x32_f16 v[126:129], v[158:161], v[192:195], v[126:129]
	v_mfma_f32_16x16x32_f16 v[122:125], v[166:169], v[192:195], v[122:125]
	v_mfma_f32_16x16x32_f16 v[110:113], v[158:161], v[200:203], v[110:113]
	v_mfma_f32_16x16x32_f16 v[106:109], v[166:169], v[200:203], v[106:109]
	v_mfma_f32_16x16x32_f16 v[94:97], v[158:161], v[208:211], v[94:97]
	v_mfma_f32_16x16x32_f16 v[90:93], v[166:169], v[208:211], v[90:93]
	v_mfma_f32_16x16x32_f16 v[78:81], v[158:161], v[216:219], v[78:81]
	v_mfma_f32_16x16x32_f16 v[74:77], v[166:169], v[216:219], v[74:77]
	s_setprio 0
	s_setprio 1
	v_mfma_f32_16x16x32_f16 v[118:121], v[170:173], v[188:191], v[118:121]
	v_mfma_f32_16x16x32_f16 v[114:117], v[178:181], v[188:191], v[114:117]
	v_mfma_f32_16x16x32_f16 v[102:105], v[170:173], v[196:199], v[102:105]
	v_mfma_f32_16x16x32_f16 v[98:101], v[178:181], v[196:199], v[98:101]
	v_mfma_f32_16x16x32_f16 v[86:89], v[170:173], v[204:207], v[86:89]
	v_mfma_f32_16x16x32_f16 v[82:85], v[178:181], v[204:207], v[82:85]
	v_mfma_f32_16x16x32_f16 v[70:73], v[170:173], v[212:215], v[70:73]
	v_mfma_f32_16x16x32_f16 v[66:69], v[178:181], v[212:215], v[66:69]
	s_setprio 2
	s_barrier
	v_mfma_f32_16x16x32_f16 v[118:121], v[174:177], v[192:195], v[118:121]
	v_mfma_f32_16x16x32_f16 v[114:117], v[182:185], v[192:195], v[114:117]
	v_mfma_f32_16x16x32_f16 v[102:105], v[174:177], v[200:203], v[102:105]
	v_mfma_f32_16x16x32_f16 v[98:101], v[182:185], v[200:203], v[98:101]
	v_mfma_f32_16x16x32_f16 v[86:89], v[174:177], v[208:211], v[86:89]
	v_mfma_f32_16x16x32_f16 v[82:85], v[182:185], v[208:211], v[82:85]
	v_mfma_f32_16x16x32_f16 v[70:73], v[174:177], v[216:219], v[70:73]
	v_mfma_f32_16x16x32_f16 v[66:69], v[182:185], v[216:219], v[66:69]
	s_setprio 0
	s_nop 0
	s_add_i32 s30, s64, s36
	v_lshl_add_u64 v[150:151], v[150:151], 0, s[10:11]
	s_mov_b32 m0, s30
	ds_read_b128 v[188:191], v156 offset:49152
	ds_read_b128 v[192:195], v156 offset:50176
	ds_read_b128 v[196:199], v156 offset:51200
	ds_read_b128 v[200:203], v156 offset:52224
	ds_read_b128 v[204:207], v156 offset:53248
	ds_read_b128 v[208:211], v156 offset:54272
	ds_read_b128 v[212:215], v156 offset:55296
	ds_read_b128 v[216:219], v156 offset:56320
	global_load_lds_dwordx4 v[150:151], off
	s_add_i32 m0, s30, 0x2000
	s_add_u32 s28, s28, 0x80080
	v_lshl_add_u64 v[150:151], v[220:221], 0, s[10:11]
	s_addc_u32 s29, s29, 0
	s_add_i32 s30, s65, s36
	global_load_lds_dwordx4 v[150:151], off
	v_lshl_add_u64 v[150:151], s[28:29], 0, v[132:133]
	s_mov_b32 m0, s30
	s_nop 0
	global_load_lds_dwordx4 v[150:151], off
	v_lshl_add_u64 v[150:151], s[28:29], 0, v[136:137]
	s_add_i32 m0, s30, 0x2000
	s_nop 0
	global_load_lds_dwordx4 v[150:151], off
	v_lshl_add_u64 v[150:151], v[222:223], 0, s[10:11]
	s_mov_b32 m0, s41
	s_nop 0
	global_load_lds_dwordx4 v[150:151], off
	v_lshl_add_u64 v[150:151], v[224:225], 0, s[10:11]
	s_mov_b32 m0, s46
	s_nop 0
	global_load_lds_dwordx4 v[150:151], off
	s_waitcnt vmcnt(8)
	s_waitcnt lgkmcnt(0)
	s_barrier
	s_setprio 1
	s_waitcnt lgkmcnt(0)
	v_mfma_f32_16x16x32_f16 v[62:65], v[146:149], v[188:191], v[62:65]
	v_mfma_f32_16x16x32_f16 v[58:61], v[162:165], v[188:191], v[58:61]
	v_mfma_f32_16x16x32_f16 v[46:49], v[146:149], v[196:199], v[46:49]
	v_mfma_f32_16x16x32_f16 v[42:45], v[162:165], v[196:199], v[42:45]
	v_mfma_f32_16x16x32_f16 v[30:33], v[146:149], v[204:207], v[30:33]
	v_mfma_f32_16x16x32_f16 v[26:29], v[162:165], v[204:207], v[26:29]
	v_mfma_f32_16x16x32_f16 v[14:17], v[146:149], v[212:215], v[14:17]
	v_mfma_f32_16x16x32_f16 v[10:13], v[162:165], v[212:215], v[10:13]
	v_mfma_f32_16x16x32_f16 v[62:65], v[158:161], v[192:195], v[62:65]
	v_mfma_f32_16x16x32_f16 v[58:61], v[166:169], v[192:195], v[58:61]
	v_mfma_f32_16x16x32_f16 v[46:49], v[158:161], v[200:203], v[46:49]
	v_mfma_f32_16x16x32_f16 v[42:45], v[166:169], v[200:203], v[42:45]
	v_mfma_f32_16x16x32_f16 v[30:33], v[158:161], v[208:211], v[30:33]
	v_mfma_f32_16x16x32_f16 v[26:29], v[166:169], v[208:211], v[26:29]
	v_mfma_f32_16x16x32_f16 v[14:17], v[158:161], v[216:219], v[14:17]
	v_mfma_f32_16x16x32_f16 v[10:13], v[166:169], v[216:219], v[10:13]
	s_setprio 0
	s_setprio 1
	v_mfma_f32_16x16x32_f16 v[54:57], v[170:173], v[188:191], v[54:57]
	v_mfma_f32_16x16x32_f16 v[50:53], v[178:181], v[188:191], v[50:53]
	v_mfma_f32_16x16x32_f16 v[38:41], v[170:173], v[196:199], v[38:41]
	v_mfma_f32_16x16x32_f16 v[34:37], v[178:181], v[196:199], v[34:37]
	v_mfma_f32_16x16x32_f16 v[22:25], v[170:173], v[204:207], v[22:25]
	v_mfma_f32_16x16x32_f16 v[18:21], v[178:181], v[204:207], v[18:21]
	v_mfma_f32_16x16x32_f16 v[6:9], v[170:173], v[212:215], v[6:9]
	v_mfma_f32_16x16x32_f16 v[2:5], v[178:181], v[212:215], v[2:5]
	s_setprio 2
	s_barrier
	v_mfma_f32_16x16x32_f16 v[54:57], v[174:177], v[192:195], v[54:57]
	v_mfma_f32_16x16x32_f16 v[50:53], v[182:185], v[192:195], v[50:53]
	v_mfma_f32_16x16x32_f16 v[38:41], v[174:177], v[200:203], v[38:41]
	v_mfma_f32_16x16x32_f16 v[34:37], v[182:185], v[200:203], v[34:37]
	v_mfma_f32_16x16x32_f16 v[22:25], v[174:177], v[208:211], v[22:25]
	v_mfma_f32_16x16x32_f16 v[18:21], v[182:185], v[208:211], v[18:21]
	v_mfma_f32_16x16x32_f16 v[6:9], v[174:177], v[216:219], v[6:9]
	v_mfma_f32_16x16x32_f16 v[2:5], v[182:185], v[216:219], v[2:5]
	s_setprio 0
	s_nop 0
	s_add_i32 s63, s63, 2
	s_add_u32 s26, s26, 0x100
	s_addc_u32 s27, s27, 0
	s_add_u32 s61, s61, 0x100
	s_addc_u32 s62, s62, 0
	s_cmp_gt_u32 s63, 29
	s_cbranch_scc0 .LBB0_628
	s_and_b64 vcc, exec, s[12:13]
	s_cbranch_vccz .LBB0_631
	s_barrier

.LBB0_758:
	ds_read_b128 v[146:149], v152
	ds_read_b128 v[156:159], v152 offset:1024
	ds_read_b128 v[160:163], v152 offset:2048
	ds_read_b128 v[164:167], v152 offset:3072
	ds_read_b128 v[168:171], v153
	ds_read_b128 v[172:175], v153 offset:1024
	ds_read_b128 v[176:179], v153 offset:2048
	ds_read_b128 v[180:183], v153 offset:3072
	s_add_u32 s28, s26, 0xfff80080
	s_addc_u32 s29, s27, -1
	s_cmp_eq_u32 s61, 28
	s_cselect_b32 s31, s19, s29
	s_cselect_b32 s30, s49, s28
	s_cselect_b32 s29, s17, s60
	s_cselect_b32 s28, s50, s51
	v_lshl_add_u64 v[184:185], s[26:27], 0, v[138:139]
	s_add_i32 m0, s25, 0xc000
	ds_read_b128 v[188:191], v154
	ds_read_b128 v[192:195], v154 offset:1024
	ds_read_b128 v[196:199], v154 offset:2048
	ds_read_b128 v[200:203], v154 offset:3072
	ds_read_b128 v[204:207], v154 offset:4096
	ds_read_b128 v[208:211], v154 offset:5120
	ds_read_b128 v[212:215], v154 offset:6144
	ds_read_b128 v[216:219], v154 offset:7168
	global_load_lds_dwordx4 v[184:185], off
	v_lshl_add_u64 v[184:185], s[26:27], 0, v[140:141]
	s_add_i32 m0, s25, 0xe000
	s_nop 0
	global_load_lds_dwordx4 v[184:185], off
	s_waitcnt vmcnt(8)
	s_waitcnt lgkmcnt(0)
	s_barrier
	s_setprio 1
	s_waitcnt lgkmcnt(0)
	v_mfma_f32_16x16x32_f16 v[126:129], v[146:149], v[188:191], v[126:129]
	v_mfma_f32_16x16x32_f16 v[122:125], v[160:163], v[188:191], v[122:125]
	v_mfma_f32_16x16x32_f16 v[110:113], v[146:149], v[196:199], v[110:113]
	v_mfma_f32_16x16x32_f16 v[106:109], v[160:163], v[196:199], v[106:109]
	v_mfma_f32_16x16x32_f16 v[94:97], v[146:149], v[204:207], v[94:97]
	v_mfma_f32_16x16x32_f16 v[90:93], v[160:163], v[204:207], v[90:93]
	v_mfma_f32_16x16x32_f16 v[78:81], v[146:149], v[212:215], v[78:81]
	v_mfma_f32_16x16x32_f16 v[74:77], v[160:163], v[212:215], v[74:77]
	v_mfma_f32_16x16x32_f16 v[126:129], v[156:159], v[192:195], v[126:129]
	v_mfma_f32_16x16x32_f16 v[122:125], v[164:167], v[192:195], v[122:125]
	v_mfma_f32_16x16x32_f16 v[110:113], v[156:159], v[200:203], v[110:113]
	v_mfma_f32_16x16x32_f16 v[106:109], v[164:167], v[200:203], v[106:109]
	v_mfma_f32_16x16x32_f16 v[94:97], v[156:159], v[208:211], v[94:97]
	v_mfma_f32_16x16x32_f16 v[90:93], v[164:167], v[208:211], v[90:93]
	v_mfma_f32_16x16x32_f16 v[78:81], v[156:159], v[216:219], v[78:81]
	v_mfma_f32_16x16x32_f16 v[74:77], v[164:167], v[216:219], v[74:77]
	s_setprio 0
	s_setprio 1
	v_mfma_f32_16x16x32_f16 v[118:121], v[168:171], v[188:191], v[118:121]
	v_mfma_f32_16x16x32_f16 v[114:117], v[176:179], v[188:191], v[114:117]
	v_mfma_f32_16x16x32_f16 v[102:105], v[168:171], v[196:199], v[102:105]
	v_mfma_f32_16x16x32_f16 v[98:101], v[176:179], v[196:199], v[98:101]
	v_mfma_f32_16x16x32_f16 v[86:89], v[168:171], v[204:207], v[86:89]
	v_mfma_f32_16x16x32_f16 v[82:85], v[176:179], v[204:207], v[82:85]
	v_mfma_f32_16x16x32_f16 v[70:73], v[168:171], v[212:215], v[70:73]
	v_mfma_f32_16x16x32_f16 v[66:69], v[176:179], v[212:215], v[66:69]
	s_setprio 2
	s_barrier
	v_mfma_f32_16x16x32_f16 v[118:121], v[172:175], v[192:195], v[118:121]
	v_mfma_f32_16x16x32_f16 v[114:117], v[180:183], v[192:195], v[114:117]
	v_mfma_f32_16x16x32_f16 v[102:105], v[172:175], v[200:203], v[102:105]
	v_mfma_f32_16x16x32_f16 v[98:101], v[180:183], v[200:203], v[98:101]
	v_mfma_f32_16x16x32_f16 v[86:89], v[172:175], v[208:211], v[86:89]
	v_mfma_f32_16x16x32_f16 v[82:85], v[180:183], v[208:211], v[82:85]
	v_mfma_f32_16x16x32_f16 v[70:73], v[172:175], v[216:219], v[70:73]
	v_mfma_f32_16x16x32_f16 v[66:69], v[180:183], v[216:219], v[66:69]
	s_setprio 0
	s_nop 0
	s_add_i32 s62, s44, s34
	v_lshl_add_u64 v[184:185], s[28:29], 0, v[134:135]
	s_mov_b32 m0, s62
	ds_read_b128 v[188:191], v154 offset:16384
	ds_read_b128 v[192:195], v154 offset:17408
	ds_read_b128 v[196:199], v154 offset:18432
	ds_read_b128 v[200:203], v154 offset:19456
	ds_read_b128 v[204:207], v154 offset:20480
	ds_read_b128 v[208:211], v154 offset:21504
	ds_read_b128 v[212:215], v154 offset:22528
	ds_read_b128 v[216:219], v154 offset:23552
	global_load_lds_dwordx4 v[184:185], off
	s_add_i32 m0, s62, 0x2000
	s_add_u32 s62, s28, 0x80000
	v_lshl_add_u64 v[220:221], s[28:29], 0, v[130:131]
	s_addc_u32 s63, s29, 0
	s_add_i32 s64, s45, s34
	global_load_lds_dwordx4 v[220:221], off
	v_lshl_add_u64 v[222:223], s[62:63], 0, v[134:135]
	s_mov_b32 m0, s64
	v_lshl_add_u64 v[224:225], s[30:31], 0, v[132:133]
	global_load_lds_dwordx4 v[222:223], off
	v_lshl_add_u64 v[222:223], s[62:63], 0, v[130:131]
	s_add_i32 m0, s64, 0x2000
	s_nop 0
	global_load_lds_dwordx4 v[222:223], off
	v_lshl_add_u64 v[222:223], s[30:31], 0, v[136:137]
	s_mov_b32 m0, s25
	s_nop 0
	global_load_lds_dwordx4 v[222:223], off
	s_mov_b32 m0, s37
	s_nop 0
	global_load_lds_dwordx4 v[224:225], off
	s_waitcnt vmcnt(8)
	s_waitcnt lgkmcnt(0)
	s_barrier
	s_setprio 1
	s_waitcnt lgkmcnt(0)
	v_mfma_f32_16x16x32_f16 v[62:65], v[146:149], v[188:191], v[62:65]
	v_mfma_f32_16x16x32_f16 v[58:61], v[160:163], v[188:191], v[58:61]
	v_mfma_f32_16x16x32_f16 v[46:49], v[146:149], v[196:199], v[46:49]
	v_mfma_f32_16x16x32_f16 v[42:45], v[160:163], v[196:199], v[42:45]
	v_mfma_f32_16x16x32_f16 v[30:33], v[146:149], v[204:207], v[30:33]
	v_mfma_f32_16x16x32_f16 v[26:29], v[160:163], v[204:207], v[26:29]
	v_mfma_f32_16x16x32_f16 v[14:17], v[146:149], v[212:215], v[14:17]
	v_mfma_f32_16x16x32_f16 v[10:13], v[160:163], v[212:215], v[10:13]
	v_mfma_f32_16x16x32_f16 v[62:65], v[156:159], v[192:195], v[62:65]
	v_mfma_f32_16x16x32_f16 v[58:61], v[164:167], v[192:195], v[58:61]
	v_mfma_f32_16x16x32_f16 v[46:49], v[156:159], v[200:203], v[46:49]
	v_mfma_f32_16x16x32_f16 v[42:45], v[164:167], v[200:203], v[42:45]
	v_mfma_f32_16x16x32_f16 v[30:33], v[156:159], v[208:211], v[30:33]
	v_mfma_f32_16x16x32_f16 v[26:29], v[164:167], v[208:211], v[26:29]
	v_mfma_f32_16x16x32_f16 v[14:17], v[156:159], v[216:219], v[14:17]
	v_mfma_f32_16x16x32_f16 v[10:13], v[164:167], v[216:219], v[10:13]
	s_setprio 0
	s_setprio 1
	v_mfma_f32_16x16x32_f16 v[54:57], v[168:171], v[188:191], v[54:57]
	v_mfma_f32_16x16x32_f16 v[50:53], v[176:179], v[188:191], v[50:53]
	v_mfma_f32_16x16x32_f16 v[38:41], v[168:171], v[196:199], v[38:41]
	v_mfma_f32_16x16x32_f16 v[34:37], v[176:179], v[196:199], v[34:37]
	v_mfma_f32_16x16x32_f16 v[22:25], v[168:171], v[204:207], v[22:25]
	v_mfma_f32_16x16x32_f16 v[18:21], v[176:179], v[204:207], v[18:21]
	v_mfma_f32_16x16x32_f16 v[6:9], v[168:171], v[212:215], v[6:9]
	v_mfma_f32_16x16x32_f16 v[2:5], v[176:179], v[212:215], v[2:5]
	s_setprio 2
	s_barrier
	v_mfma_f32_16x16x32_f16 v[54:57], v[172:175], v[192:195], v[54:57]
	v_mfma_f32_16x16x32_f16 v[50:53], v[180:183], v[192:195], v[50:53]
	v_mfma_f32_16x16x32_f16 v[38:41], v[172:175], v[200:203], v[38:41]
	v_mfma_f32_16x16x32_f16 v[34:37], v[180:183], v[200:203], v[34:37]
	v_mfma_f32_16x16x32_f16 v[22:25], v[172:175], v[208:211], v[22:25]
	v_mfma_f32_16x16x32_f16 v[18:21], v[180:183], v[208:211], v[18:21]
	v_mfma_f32_16x16x32_f16 v[6:9], v[172:175], v[216:219], v[6:9]
	v_mfma_f32_16x16x32_f16 v[2:5], v[180:183], v[216:219], v[2:5]
	s_setprio 0
	s_nop 0
	s_add_i32 s62, 0, 0x18000
	s_add_i32 s63, 0, 0x1c000
	v_add_u32_e32 v164, s62, v150
	v_add_u32_e32 v180, s63, v150
	ds_read_b128 v[146:149], v164
	ds_read_b128 v[156:159], v164 offset:1024
	ds_read_b128 v[160:163], v164 offset:2048
	ds_read_b128 v[164:167], v164 offset:3072
	ds_read_b128 v[168:171], v180
	ds_read_b128 v[172:175], v180 offset:1024
	ds_read_b128 v[176:179], v180 offset:2048
	ds_read_b128 v[180:183], v180 offset:3072
	s_add_u32 s30, s30, 0x80000
	s_addc_u32 s31, s31, 0
	s_mov_b32 m0, s38
	v_lshl_add_u64 v[226:227], s[30:31], 0, v[136:137]
	ds_read_b128 v[188:191], v154 offset:32768
	ds_read_b128 v[192:195], v154 offset:33792
	ds_read_b128 v[196:199], v154 offset:34816
	ds_read_b128 v[200:203], v154 offset:35840
	ds_read_b128 v[204:207], v154 offset:36864
	ds_read_b128 v[208:211], v154 offset:37888
	ds_read_b128 v[212:215], v154 offset:38912
	ds_read_b128 v[216:219], v154 offset:39936
	global_load_lds_dwordx4 v[226:227], off
	v_lshl_add_u64 v[226:227], s[30:31], 0, v[132:133]
	s_mov_b32 m0, s39
	s_nop 0
	global_load_lds_dwordx4 v[226:227], off
	s_waitcnt vmcnt(8)
	s_waitcnt lgkmcnt(0)
	s_barrier
	s_setprio 1
	s_waitcnt lgkmcnt(0)
	v_mfma_f32_16x16x32_f16 v[126:129], v[146:149], v[188:191], v[126:129]
	v_mfma_f32_16x16x32_f16 v[122:125], v[160:163], v[188:191], v[122:125]
	v_mfma_f32_16x16x32_f16 v[110:113], v[146:149], v[196:199], v[110:113]
	v_mfma_f32_16x16x32_f16 v[106:109], v[160:163], v[196:199], v[106:109]
	v_mfma_f32_16x16x32_f16 v[94:97], v[146:149], v[204:207], v[94:97]
	v_mfma_f32_16x16x32_f16 v[90:93], v[160:163], v[204:207], v[90:93]
	v_mfma_f32_16x16x32_f16 v[78:81], v[146:149], v[212:215], v[78:81]
	v_mfma_f32_16x16x32_f16 v[74:77], v[160:163], v[212:215], v[74:77]
	v_mfma_f32_16x16x32_f16 v[126:129], v[156:159], v[192:195], v[126:129]
	v_mfma_f32_16x16x32_f16 v[122:125], v[164:167], v[192:195], v[122:125]
	v_mfma_f32_16x16x32_f16 v[110:113], v[156:159], v[200:203], v[110:113]
	v_mfma_f32_16x16x32_f16 v[106:109], v[164:167], v[200:203], v[106:109]
	v_mfma_f32_16x16x32_f16 v[94:97], v[156:159], v[208:211], v[94:97]
	v_mfma_f32_16x16x32_f16 v[90:93], v[164:167], v[208:211], v[90:93]
	v_mfma_f32_16x16x32_f16 v[78:81], v[156:159], v[216:219], v[78:81]
	v_mfma_f32_16x16x32_f16 v[74:77], v[164:167], v[216:219], v[74:77]
	s_setprio 0
	s_setprio 1
	v_mfma_f32_16x16x32_f16 v[118:121], v[168:171], v[188:191], v[118:121]
	v_mfma_f32_16x16x32_f16 v[114:117], v[176:179], v[188:191], v[114:117]
	v_mfma_f32_16x16x32_f16 v[102:105], v[168:171], v[196:199], v[102:105]
	v_mfma_f32_16x16x32_f16 v[98:101], v[176:179], v[196:199], v[98:101]
	v_mfma_f32_16x16x32_f16 v[86:89], v[168:171], v[204:207], v[86:89]
	v_mfma_f32_16x16x32_f16 v[82:85], v[176:179], v[204:207], v[82:85]
	v_mfma_f32_16x16x32_f16 v[70:73], v[168:171], v[212:215], v[70:73]
	v_mfma_f32_16x16x32_f16 v[66:69], v[176:179], v[212:215], v[66:69]
	s_setprio 2
	s_barrier
	v_mfma_f32_16x16x32_f16 v[118:121], v[172:175], v[192:195], v[118:121]
	v_mfma_f32_16x16x32_f16 v[114:117], v[180:183], v[192:195], v[114:117]
	v_mfma_f32_16x16x32_f16 v[102:105], v[172:175], v[200:203], v[102:105]
	v_mfma_f32_16x16x32_f16 v[98:101], v[180:183], v[200:203], v[98:101]
	v_mfma_f32_16x16x32_f16 v[86:89], v[172:175], v[208:211], v[86:89]
	v_mfma_f32_16x16x32_f16 v[82:85], v[180:183], v[208:211], v[82:85]
	v_mfma_f32_16x16x32_f16 v[70:73], v[172:175], v[216:219], v[70:73]
	v_mfma_f32_16x16x32_f16 v[66:69], v[180:183], v[216:219], v[66:69]
	s_setprio 0
	s_nop 0
	s_add_i32 s30, s62, s34
	v_lshl_add_u64 v[184:185], v[184:185], 0, s[12:13]
	s_mov_b32 m0, s30
	ds_read_b128 v[188:191], v154 offset:49152
	ds_read_b128 v[192:195], v154 offset:50176
	ds_read_b128 v[196:199], v154 offset:51200
	ds_read_b128 v[200:203], v154 offset:52224
	ds_read_b128 v[204:207], v154 offset:53248
	ds_read_b128 v[208:211], v154 offset:54272
	ds_read_b128 v[212:215], v154 offset:55296
	ds_read_b128 v[216:219], v154 offset:56320
	global_load_lds_dwordx4 v[184:185], off
	s_add_i32 m0, s30, 0x2000
	s_add_u32 s28, s28, 0x80080
	v_lshl_add_u64 v[184:185], v[220:221], 0, s[12:13]
	s_addc_u32 s29, s29, 0
	s_add_i32 s30, s63, s34
	global_load_lds_dwordx4 v[184:185], off
	v_lshl_add_u64 v[184:185], s[28:29], 0, v[134:135]
	s_mov_b32 m0, s30
	s_nop 0
	global_load_lds_dwordx4 v[184:185], off
	v_lshl_add_u64 v[184:185], s[28:29], 0, v[130:131]
	s_add_i32 m0, s30, 0x2000
	s_nop 0
	global_load_lds_dwordx4 v[184:185], off
	v_lshl_add_u64 v[184:185], v[222:223], 0, s[12:13]
	s_mov_b32 m0, s41
	s_nop 0
	global_load_lds_dwordx4 v[184:185], off
	v_lshl_add_u64 v[184:185], v[224:225], 0, s[12:13]
	s_mov_b32 m0, s42
	s_nop 0
	global_load_lds_dwordx4 v[184:185], off
	s_waitcnt vmcnt(8)
	s_waitcnt lgkmcnt(0)
	s_barrier
	s_setprio 1
	s_waitcnt lgkmcnt(0)
	v_mfma_f32_16x16x32_f16 v[62:65], v[146:149], v[188:191], v[62:65]
	v_mfma_f32_16x16x32_f16 v[58:61], v[160:163], v[188:191], v[58:61]
	v_mfma_f32_16x16x32_f16 v[46:49], v[146:149], v[196:199], v[46:49]
	v_mfma_f32_16x16x32_f16 v[42:45], v[160:163], v[196:199], v[42:45]
	v_mfma_f32_16x16x32_f16 v[30:33], v[146:149], v[204:207], v[30:33]
	v_mfma_f32_16x16x32_f16 v[26:29], v[160:163], v[204:207], v[26:29]
	v_mfma_f32_16x16x32_f16 v[14:17], v[146:149], v[212:215], v[14:17]
	v_mfma_f32_16x16x32_f16 v[10:13], v[160:163], v[212:215], v[10:13]
	v_mfma_f32_16x16x32_f16 v[62:65], v[156:159], v[192:195], v[62:65]
	v_mfma_f32_16x16x32_f16 v[58:61], v[164:167], v[192:195], v[58:61]
	v_mfma_f32_16x16x32_f16 v[46:49], v[156:159], v[200:203], v[46:49]
	v_mfma_f32_16x16x32_f16 v[42:45], v[164:167], v[200:203], v[42:45]
	v_mfma_f32_16x16x32_f16 v[30:33], v[156:159], v[208:211], v[30:33]
	v_mfma_f32_16x16x32_f16 v[26:29], v[164:167], v[208:211], v[26:29]
	v_mfma_f32_16x16x32_f16 v[14:17], v[156:159], v[216:219], v[14:17]
	v_mfma_f32_16x16x32_f16 v[10:13], v[164:167], v[216:219], v[10:13]
	s_setprio 0
	s_setprio 1
	v_mfma_f32_16x16x32_f16 v[54:57], v[168:171], v[188:191], v[54:57]
	v_mfma_f32_16x16x32_f16 v[50:53], v[176:179], v[188:191], v[50:53]
	v_mfma_f32_16x16x32_f16 v[38:41], v[168:171], v[196:199], v[38:41]
	v_mfma_f32_16x16x32_f16 v[34:37], v[176:179], v[196:199], v[34:37]
	v_mfma_f32_16x16x32_f16 v[22:25], v[168:171], v[204:207], v[22:25]
	v_mfma_f32_16x16x32_f16 v[18:21], v[176:179], v[204:207], v[18:21]
	v_mfma_f32_16x16x32_f16 v[6:9], v[168:171], v[212:215], v[6:9]
	v_mfma_f32_16x16x32_f16 v[2:5], v[176:179], v[212:215], v[2:5]
	s_setprio 2
	s_barrier
	v_mfma_f32_16x16x32_f16 v[54:57], v[172:175], v[192:195], v[54:57]
	v_mfma_f32_16x16x32_f16 v[50:53], v[180:183], v[192:195], v[50:53]
	v_mfma_f32_16x16x32_f16 v[38:41], v[172:175], v[200:203], v[38:41]
	v_mfma_f32_16x16x32_f16 v[34:37], v[180:183], v[200:203], v[34:37]
	v_mfma_f32_16x16x32_f16 v[22:25], v[172:175], v[208:211], v[22:25]
	v_mfma_f32_16x16x32_f16 v[18:21], v[180:183], v[208:211], v[18:21]
	v_mfma_f32_16x16x32_f16 v[6:9], v[172:175], v[216:219], v[6:9]
	v_mfma_f32_16x16x32_f16 v[2:5], v[180:183], v[216:219], v[2:5]
	s_setprio 0
	s_nop 0
	s_add_i32 s61, s61, 2
	s_add_u32 s26, s26, 0x100
	s_addc_u32 s27, s27, 0
	s_add_u32 s51, s51, 0x100
	s_addc_u32 s60, s60, 0
	s_cmp_gt_u32 s61, 29
	s_cbranch_scc0 .LBB0_758
	s_and_b64 vcc, exec, s[14:15]
	s_cbranch_vccz .LBB0_761
	s_barrier

.LBB0_841:
	ds_read_b128 v[26:29], v190
	ds_read_b128 v[30:33], v190 offset:1024
	ds_read_b128 v[18:21], v190 offset:2048
	ds_read_b128 v[22:25], v190 offset:3072
	ds_read_b128 v[10:13], v191
	ds_read_b128 v[14:17], v191 offset:1024
	ds_read_b128 v[2:5], v191 offset:2048
	ds_read_b128 v[6:9], v191 offset:3072
	s_add_u32 s24, s22, 0xfff50080
	s_addc_u32 s25, s23, -1
	s_cmp_eq_u32 s48, 40
	s_cselect_b32 s27, s9, s25
	s_cselect_b32 s26, s8, s24
	s_cselect_b32 s25, s21, s47
	s_cselect_b32 s24, s20, s46
	v_lshl_add_u64 v[218:219], s[22:23], 0, v[170:171]
	s_add_i32 m0, s31, 0xc000
	ds_read_b128 v[178:181], v192
	ds_read_b128 v[182:185], v192 offset:1024
	ds_read_b128 v[194:197], v192 offset:2048
	ds_read_b128 v[198:201], v192 offset:3072
	ds_read_b128 v[202:205], v192 offset:4096
	ds_read_b128 v[206:209], v192 offset:5120
	ds_read_b128 v[210:213], v192 offset:6144
	ds_read_b128 v[214:217], v192 offset:7168
	global_load_lds_dwordx4 v[218:219], off
	v_lshl_add_u64 v[218:219], s[22:23], 0, v[172:173]
	s_add_i32 m0, s31, 0xe000
	s_nop 0
	global_load_lds_dwordx4 v[218:219], off
	s_waitcnt vmcnt(8)
	s_waitcnt lgkmcnt(0)
	s_barrier
	s_setprio 1
	s_waitcnt lgkmcnt(0)
	v_mfma_scale_f32_16x16x128_f8f6f4 v[158:161], v[26:33], v[178:185], v[158:161], v1, v1 op_sel_hi:[0,0,0]
	v_mfma_scale_f32_16x16x128_f8f6f4 v[154:157], v[18:25], v[178:185], v[154:157], v1, v1 op_sel_hi:[0,0,0]
	v_mfma_scale_f32_16x16x128_f8f6f4 v[142:145], v[26:33], v[194:201], v[142:145], v1, v1 op_sel_hi:[0,0,0]
	v_mfma_scale_f32_16x16x128_f8f6f4 v[138:141], v[18:25], v[194:201], v[138:141], v1, v1 op_sel_hi:[0,0,0]
	v_mfma_scale_f32_16x16x128_f8f6f4 v[126:129], v[26:33], v[202:209], v[126:129], v1, v1 op_sel_hi:[0,0,0]
	v_mfma_scale_f32_16x16x128_f8f6f4 v[122:125], v[18:25], v[202:209], v[122:125], v1, v1 op_sel_hi:[0,0,0]
	v_mfma_scale_f32_16x16x128_f8f6f4 v[110:113], v[26:33], v[210:217], v[110:113], v1, v1 op_sel_hi:[0,0,0]
	v_mfma_scale_f32_16x16x128_f8f6f4 v[106:109], v[18:25], v[210:217], v[106:109], v1, v1 op_sel_hi:[0,0,0]
	s_setprio 0
	s_setprio 1
	v_mfma_scale_f32_16x16x128_f8f6f4 v[150:153], v[10:17], v[178:185], v[150:153], v1, v1 op_sel_hi:[0,0,0]
	v_mfma_scale_f32_16x16x128_f8f6f4 v[146:149], v[2:9], v[178:185], v[146:149], v1, v1 op_sel_hi:[0,0,0]
	v_mfma_scale_f32_16x16x128_f8f6f4 v[134:137], v[10:17], v[194:201], v[134:137], v1, v1 op_sel_hi:[0,0,0]
	v_mfma_scale_f32_16x16x128_f8f6f4 v[130:133], v[2:9], v[194:201], v[130:133], v1, v1 op_sel_hi:[0,0,0]
	s_setprio 2
	s_barrier
	v_mfma_scale_f32_16x16x128_f8f6f4 v[118:121], v[10:17], v[202:209], v[118:121], v1, v1 op_sel_hi:[0,0,0]
	v_mfma_scale_f32_16x16x128_f8f6f4 v[114:117], v[2:9], v[202:209], v[114:117], v1, v1 op_sel_hi:[0,0,0]
	v_mfma_scale_f32_16x16x128_f8f6f4 v[102:105], v[10:17], v[210:217], v[102:105], v1, v1 op_sel_hi:[0,0,0]
	v_mfma_scale_f32_16x16x128_f8f6f4 v[98:101], v[2:9], v[210:217], v[98:101], v1, v1 op_sel_hi:[0,0,0]
	s_setprio 0
	s_nop 0
	s_add_i32 s49, s40, s30
	v_lshl_add_u64 v[178:179], s[24:25], 0, v[164:165]
	s_mov_b32 m0, s49
	ds_read_b128 v[194:197], v192 offset:16384
	ds_read_b128 v[198:201], v192 offset:17408
	ds_read_b128 v[202:205], v192 offset:18432
	ds_read_b128 v[206:209], v192 offset:19456
	ds_read_b128 v[210:213], v192 offset:20480
	ds_read_b128 v[214:217], v192 offset:21504
	ds_read_b128 v[218:221], v192 offset:22528
	ds_read_b128 v[222:225], v192 offset:23552
	global_load_lds_dwordx4 v[178:179], off
	s_add_i32 m0, s49, 0x2000
	s_add_u32 s50, s24, 0xb0000
	v_lshl_add_u64 v[180:181], s[24:25], 0, v[168:169]
	s_addc_u32 s51, s25, 0
	s_add_i32 s49, s41, s30
	global_load_lds_dwordx4 v[180:181], off
	v_lshl_add_u64 v[182:183], s[50:51], 0, v[164:165]
	s_mov_b32 m0, s49
	v_lshl_add_u64 v[184:185], s[26:27], 0, v[166:167]
	global_load_lds_dwordx4 v[182:183], off
	v_lshl_add_u64 v[182:183], s[50:51], 0, v[168:169]
	s_add_i32 m0, s49, 0x2000
	s_nop 0
	global_load_lds_dwordx4 v[182:183], off
	v_lshl_add_u64 v[182:183], s[26:27], 0, v[162:163]
	s_mov_b32 m0, s31
	s_nop 0
	global_load_lds_dwordx4 v[182:183], off
	s_mov_b32 m0, s33
	s_nop 0
	global_load_lds_dwordx4 v[184:185], off
	s_waitcnt vmcnt(8)
	s_waitcnt lgkmcnt(0)
	s_barrier
	s_setprio 1
	s_waitcnt lgkmcnt(0)
	v_mfma_scale_f32_16x16x128_f8f6f4 v[94:97], v[26:33], v[194:201], v[94:97], v1, v1 op_sel_hi:[0,0,0]
	v_mfma_scale_f32_16x16x128_f8f6f4 v[90:93], v[18:25], v[194:201], v[90:93], v1, v1 op_sel_hi:[0,0,0]
	v_mfma_scale_f32_16x16x128_f8f6f4 v[78:81], v[26:33], v[202:209], v[78:81], v1, v1 op_sel_hi:[0,0,0]
	v_mfma_scale_f32_16x16x128_f8f6f4 v[74:77], v[18:25], v[202:209], v[74:77], v1, v1 op_sel_hi:[0,0,0]
	v_mfma_scale_f32_16x16x128_f8f6f4 v[62:65], v[26:33], v[210:217], v[62:65], v1, v1 op_sel_hi:[0,0,0]
	v_mfma_scale_f32_16x16x128_f8f6f4 v[58:61], v[18:25], v[210:217], v[58:61], v1, v1 op_sel_hi:[0,0,0]
	v_mfma_scale_f32_16x16x128_f8f6f4 v[46:49], v[26:33], v[218:225], v[46:49], v1, v1 op_sel_hi:[0,0,0]
	v_mfma_scale_f32_16x16x128_f8f6f4 v[42:45], v[18:25], v[218:225], v[42:45], v1, v1 op_sel_hi:[0,0,0]
	s_setprio 0
	s_setprio 1
	v_mfma_scale_f32_16x16x128_f8f6f4 v[86:89], v[10:17], v[194:201], v[86:89], v1, v1 op_sel_hi:[0,0,0]
	v_mfma_scale_f32_16x16x128_f8f6f4 v[82:85], v[2:9], v[194:201], v[82:85], v1, v1 op_sel_hi:[0,0,0]
	v_mfma_scale_f32_16x16x128_f8f6f4 v[70:73], v[10:17], v[202:209], v[70:73], v1, v1 op_sel_hi:[0,0,0]
	v_mfma_scale_f32_16x16x128_f8f6f4 v[66:69], v[2:9], v[202:209], v[66:69], v1, v1 op_sel_hi:[0,0,0]
	s_setprio 2
	s_barrier
	v_mfma_scale_f32_16x16x128_f8f6f4 v[54:57], v[10:17], v[210:217], v[54:57], v1, v1 op_sel_hi:[0,0,0]
	v_mfma_scale_f32_16x16x128_f8f6f4 v[50:53], v[2:9], v[210:217], v[50:53], v1, v1 op_sel_hi:[0,0,0]
	v_mfma_scale_f32_16x16x128_f8f6f4 v[38:41], v[10:17], v[218:225], v[38:41], v1, v1 op_sel_hi:[0,0,0]
	v_mfma_scale_f32_16x16x128_f8f6f4 v[34:37], v[2:9], v[218:225], v[34:37], v1, v1 op_sel_hi:[0,0,0]
	s_setprio 0
	s_nop 0
	s_add_i32 s49, 0, 0x18000
	s_add_i32 s50, 0, 0x1c000
	v_add_u32_e32 v14, s49, v188
	v_add_u32_e32 v30, s50, v188
	ds_read_b128 v[2:5], v14
	ds_read_b128 v[6:9], v14 offset:1024
	ds_read_b128 v[10:13], v14 offset:2048
	ds_read_b128 v[14:17], v14 offset:3072
	ds_read_b128 v[18:21], v30
	ds_read_b128 v[22:25], v30 offset:1024
	ds_read_b128 v[26:29], v30 offset:2048
	ds_read_b128 v[30:33], v30 offset:3072
	s_add_u32 s26, s26, 0xb0000
	s_addc_u32 s27, s27, 0
	s_mov_b32 m0, s34
	v_lshl_add_u64 v[226:227], s[26:27], 0, v[162:163]
	ds_read_b128 v[194:197], v192 offset:32768
	ds_read_b128 v[198:201], v192 offset:33792
	ds_read_b128 v[202:205], v192 offset:34816
	ds_read_b128 v[206:209], v192 offset:35840
	ds_read_b128 v[210:213], v192 offset:36864
	ds_read_b128 v[214:217], v192 offset:37888
	ds_read_b128 v[218:221], v192 offset:38912
	ds_read_b128 v[222:225], v192 offset:39936
	global_load_lds_dwordx4 v[226:227], off
	v_lshl_add_u64 v[226:227], s[26:27], 0, v[166:167]
	s_mov_b32 m0, s35
	s_nop 0
	global_load_lds_dwordx4 v[226:227], off
	s_waitcnt vmcnt(8)
	s_waitcnt lgkmcnt(0)
	s_barrier
	s_setprio 1
	s_waitcnt lgkmcnt(0)
	v_mfma_scale_f32_16x16x128_f8f6f4 v[158:161], v[2:9], v[194:201], v[158:161], v1, v1 op_sel_hi:[0,0,0]
	v_mfma_scale_f32_16x16x128_f8f6f4 v[154:157], v[10:17], v[194:201], v[154:157], v1, v1 op_sel_hi:[0,0,0]
	v_mfma_scale_f32_16x16x128_f8f6f4 v[142:145], v[2:9], v[202:209], v[142:145], v1, v1 op_sel_hi:[0,0,0]
	v_mfma_scale_f32_16x16x128_f8f6f4 v[138:141], v[10:17], v[202:209], v[138:141], v1, v1 op_sel_hi:[0,0,0]
	v_mfma_scale_f32_16x16x128_f8f6f4 v[126:129], v[2:9], v[210:217], v[126:129], v1, v1 op_sel_hi:[0,0,0]
	v_mfma_scale_f32_16x16x128_f8f6f4 v[122:125], v[10:17], v[210:217], v[122:125], v1, v1 op_sel_hi:[0,0,0]
	v_mfma_scale_f32_16x16x128_f8f6f4 v[110:113], v[2:9], v[218:225], v[110:113], v1, v1 op_sel_hi:[0,0,0]
	v_mfma_scale_f32_16x16x128_f8f6f4 v[106:109], v[10:17], v[218:225], v[106:109], v1, v1 op_sel_hi:[0,0,0]
	s_setprio 0
	s_setprio 1
	v_mfma_scale_f32_16x16x128_f8f6f4 v[150:153], v[18:25], v[194:201], v[150:153], v1, v1 op_sel_hi:[0,0,0]
	v_mfma_scale_f32_16x16x128_f8f6f4 v[146:149], v[26:33], v[194:201], v[146:149], v1, v1 op_sel_hi:[0,0,0]
	v_mfma_scale_f32_16x16x128_f8f6f4 v[134:137], v[18:25], v[202:209], v[134:137], v1, v1 op_sel_hi:[0,0,0]
	v_mfma_scale_f32_16x16x128_f8f6f4 v[130:133], v[26:33], v[202:209], v[130:133], v1, v1 op_sel_hi:[0,0,0]
	s_setprio 2
	s_barrier
	v_mfma_scale_f32_16x16x128_f8f6f4 v[118:121], v[18:25], v[210:217], v[118:121], v1, v1 op_sel_hi:[0,0,0]
	v_mfma_scale_f32_16x16x128_f8f6f4 v[114:117], v[26:33], v[210:217], v[114:117], v1, v1 op_sel_hi:[0,0,0]
	v_mfma_scale_f32_16x16x128_f8f6f4 v[102:105], v[18:25], v[218:225], v[102:105], v1, v1 op_sel_hi:[0,0,0]
	v_mfma_scale_f32_16x16x128_f8f6f4 v[98:101], v[26:33], v[218:225], v[98:101], v1, v1 op_sel_hi:[0,0,0]
	s_setprio 0
	s_nop 0
	s_add_i32 s26, s49, s30
	v_lshl_add_u64 v[178:179], v[178:179], 0, s[12:13]
	s_mov_b32 m0, s26
	ds_read_b128 v[194:197], v192 offset:49152
	ds_read_b128 v[198:201], v192 offset:50176
	ds_read_b128 v[202:205], v192 offset:51200
	ds_read_b128 v[206:209], v192 offset:52224
	ds_read_b128 v[210:213], v192 offset:53248
	ds_read_b128 v[214:217], v192 offset:54272
	ds_read_b128 v[218:221], v192 offset:55296
	ds_read_b128 v[222:225], v192 offset:56320
	global_load_lds_dwordx4 v[178:179], off
	s_add_i32 m0, s26, 0x2000
	s_add_u32 s24, s24, 0xb0080
	v_lshl_add_u64 v[178:179], v[180:181], 0, s[12:13]
	s_addc_u32 s25, s25, 0
	s_add_i32 s26, s50, s30
	global_load_lds_dwordx4 v[178:179], off
	v_lshl_add_u64 v[178:179], s[24:25], 0, v[164:165]
	s_mov_b32 m0, s26
	s_nop 0
	global_load_lds_dwordx4 v[178:179], off
	v_lshl_add_u64 v[178:179], s[24:25], 0, v[168:169]
	s_add_i32 m0, s26, 0x2000
	s_nop 0
	global_load_lds_dwordx4 v[178:179], off
	v_lshl_add_u64 v[178:179], v[182:183], 0, s[12:13]
	s_mov_b32 m0, s37
	s_nop 0
	global_load_lds_dwordx4 v[178:179], off
	v_lshl_add_u64 v[178:179], v[184:185], 0, s[12:13]
	s_mov_b32 m0, s38
	s_nop 0
	global_load_lds_dwordx4 v[178:179], off
	s_waitcnt vmcnt(8)
	s_waitcnt lgkmcnt(0)
	s_barrier
	s_setprio 1
	s_waitcnt lgkmcnt(0)
	v_mfma_scale_f32_16x16x128_f8f6f4 v[94:97], v[2:9], v[194:201], v[94:97], v1, v1 op_sel_hi:[0,0,0]
	v_mfma_scale_f32_16x16x128_f8f6f4 v[90:93], v[10:17], v[194:201], v[90:93], v1, v1 op_sel_hi:[0,0,0]
	v_mfma_scale_f32_16x16x128_f8f6f4 v[78:81], v[2:9], v[202:209], v[78:81], v1, v1 op_sel_hi:[0,0,0]
	v_mfma_scale_f32_16x16x128_f8f6f4 v[74:77], v[10:17], v[202:209], v[74:77], v1, v1 op_sel_hi:[0,0,0]
	v_mfma_scale_f32_16x16x128_f8f6f4 v[62:65], v[2:9], v[210:217], v[62:65], v1, v1 op_sel_hi:[0,0,0]
	v_mfma_scale_f32_16x16x128_f8f6f4 v[58:61], v[10:17], v[210:217], v[58:61], v1, v1 op_sel_hi:[0,0,0]
	v_mfma_scale_f32_16x16x128_f8f6f4 v[46:49], v[2:9], v[218:225], v[46:49], v1, v1 op_sel_hi:[0,0,0]
	v_mfma_scale_f32_16x16x128_f8f6f4 v[42:45], v[10:17], v[218:225], v[42:45], v1, v1 op_sel_hi:[0,0,0]
	s_setprio 0
	s_setprio 1
	v_mfma_scale_f32_16x16x128_f8f6f4 v[86:89], v[18:25], v[194:201], v[86:89], v1, v1 op_sel_hi:[0,0,0]
	v_mfma_scale_f32_16x16x128_f8f6f4 v[82:85], v[26:33], v[194:201], v[82:85], v1, v1 op_sel_hi:[0,0,0]
	v_mfma_scale_f32_16x16x128_f8f6f4 v[70:73], v[18:25], v[202:209], v[70:73], v1, v1 op_sel_hi:[0,0,0]
	v_mfma_scale_f32_16x16x128_f8f6f4 v[66:69], v[26:33], v[202:209], v[66:69], v1, v1 op_sel_hi:[0,0,0]
	s_setprio 2
	s_barrier
	v_mfma_scale_f32_16x16x128_f8f6f4 v[54:57], v[18:25], v[210:217], v[54:57], v1, v1 op_sel_hi:[0,0,0]
	v_mfma_scale_f32_16x16x128_f8f6f4 v[50:53], v[26:33], v[210:217], v[50:53], v1, v1 op_sel_hi:[0,0,0]
	v_mfma_scale_f32_16x16x128_f8f6f4 v[38:41], v[18:25], v[218:225], v[38:41], v1, v1 op_sel_hi:[0,0,0]
	v_mfma_scale_f32_16x16x128_f8f6f4 v[34:37], v[26:33], v[218:225], v[34:37], v1, v1 op_sel_hi:[0,0,0]
	s_setprio 0
	s_nop 0
	s_add_i32 s48, s48, 2
	s_add_u32 s22, s22, 0x100
	s_addc_u32 s23, s23, 0
	s_add_u32 s46, s46, 0x100
	s_addc_u32 s47, s47, 0
	s_cmp_gt_u32 s48, 41
	s_cbranch_scc0 .LBB0_841
	s_and_b64 vcc, exec, s[14:15]
	s_cbranch_vccz .LBB0_844
	s_barrier

.LBB0_973:
	ds_read_b128 v[158:161], v155
	ds_read_b128 v[162:165], v155 offset:1024
	ds_read_b128 v[166:169], v155 offset:2048
	ds_read_b128 v[170:173], v155 offset:3072
	ds_read_b128 v[174:177], v156
	ds_read_b128 v[178:181], v156 offset:1024
	ds_read_b128 v[182:185], v156 offset:2048
	ds_read_b128 v[188:191], v156 offset:3072
	s_add_u32 s34, s30, 0xfff80080
	s_addc_u32 s35, s31, -1
	s_cmp_eq_u32 s64, 28
	s_cselect_b32 s37, s9, s35
	s_cselect_b32 s36, s23, s34
	s_cselect_b32 s35, s21, s63
	s_cselect_b32 s34, s29, s62
	v_lshl_add_u64 v[152:153], s[30:31], 0, v[144:145]
	s_add_i32 m0, s39, 0xc000
	ds_read_b128 v[192:195], v157
	ds_read_b128 v[196:199], v157 offset:1024
	ds_read_b128 v[200:203], v157 offset:2048
	ds_read_b128 v[204:207], v157 offset:3072
	ds_read_b128 v[208:211], v157 offset:4096
	ds_read_b128 v[212:215], v157 offset:5120
	ds_read_b128 v[216:219], v157 offset:6144
	ds_read_b128 v[220:223], v157 offset:7168
	global_load_lds_dwordx4 v[152:153], off
	v_lshl_add_u64 v[152:153], s[30:31], 0, v[146:147]
	s_add_i32 m0, s39, 0xe000
	s_nop 0
	global_load_lds_dwordx4 v[152:153], off
	s_waitcnt vmcnt(8)
	s_waitcnt lgkmcnt(0)
	s_barrier
	s_setprio 1
	s_waitcnt lgkmcnt(0)
	v_mfma_f32_16x16x32_f16 v[126:129], v[158:161], v[192:195], v[126:129]
	v_mfma_f32_16x16x32_f16 v[122:125], v[166:169], v[192:195], v[122:125]
	v_mfma_f32_16x16x32_f16 v[110:113], v[158:161], v[200:203], v[110:113]
	v_mfma_f32_16x16x32_f16 v[106:109], v[166:169], v[200:203], v[106:109]
	v_mfma_f32_16x16x32_f16 v[94:97], v[158:161], v[208:211], v[94:97]
	v_mfma_f32_16x16x32_f16 v[90:93], v[166:169], v[208:211], v[90:93]
	v_mfma_f32_16x16x32_f16 v[78:81], v[158:161], v[216:219], v[78:81]
	v_mfma_f32_16x16x32_f16 v[74:77], v[166:169], v[216:219], v[74:77]
	v_mfma_f32_16x16x32_f16 v[126:129], v[162:165], v[196:199], v[126:129]
	v_mfma_f32_16x16x32_f16 v[122:125], v[170:173], v[196:199], v[122:125]
	v_mfma_f32_16x16x32_f16 v[110:113], v[162:165], v[204:207], v[110:113]
	v_mfma_f32_16x16x32_f16 v[106:109], v[170:173], v[204:207], v[106:109]
	v_mfma_f32_16x16x32_f16 v[94:97], v[162:165], v[212:215], v[94:97]
	v_mfma_f32_16x16x32_f16 v[90:93], v[170:173], v[212:215], v[90:93]
	v_mfma_f32_16x16x32_f16 v[78:81], v[162:165], v[220:223], v[78:81]
	v_mfma_f32_16x16x32_f16 v[74:77], v[170:173], v[220:223], v[74:77]
	s_setprio 0
	s_setprio 1
	v_mfma_f32_16x16x32_f16 v[118:121], v[174:177], v[192:195], v[118:121]
	v_mfma_f32_16x16x32_f16 v[114:117], v[182:185], v[192:195], v[114:117]
	v_mfma_f32_16x16x32_f16 v[102:105], v[174:177], v[200:203], v[102:105]
	v_mfma_f32_16x16x32_f16 v[98:101], v[182:185], v[200:203], v[98:101]
	v_mfma_f32_16x16x32_f16 v[86:89], v[174:177], v[208:211], v[86:89]
	v_mfma_f32_16x16x32_f16 v[82:85], v[182:185], v[208:211], v[82:85]
	v_mfma_f32_16x16x32_f16 v[70:73], v[174:177], v[216:219], v[70:73]
	v_mfma_f32_16x16x32_f16 v[66:69], v[182:185], v[216:219], v[66:69]
	s_setprio 2
	s_barrier
	v_mfma_f32_16x16x32_f16 v[118:121], v[178:181], v[196:199], v[118:121]
	v_mfma_f32_16x16x32_f16 v[114:117], v[188:191], v[196:199], v[114:117]
	v_mfma_f32_16x16x32_f16 v[102:105], v[178:181], v[204:207], v[102:105]
	v_mfma_f32_16x16x32_f16 v[98:101], v[188:191], v[204:207], v[98:101]
	v_mfma_f32_16x16x32_f16 v[86:89], v[178:181], v[212:215], v[86:89]
	v_mfma_f32_16x16x32_f16 v[82:85], v[188:191], v[212:215], v[82:85]
	v_mfma_f32_16x16x32_f16 v[70:73], v[178:181], v[220:223], v[70:73]
	v_mfma_f32_16x16x32_f16 v[66:69], v[188:191], v[220:223], v[66:69]
	s_setprio 0
	s_nop 0
	s_add_i32 s65, s49, s38
	v_lshl_add_u64 v[152:153], s[34:35], 0, v[132:133]
	s_mov_b32 m0, s65
	ds_read_b128 v[192:195], v157 offset:16384
	ds_read_b128 v[196:199], v157 offset:17408
	ds_read_b128 v[200:203], v157 offset:18432
	ds_read_b128 v[204:207], v157 offset:19456
	ds_read_b128 v[208:211], v157 offset:20480
	ds_read_b128 v[212:215], v157 offset:21504
	ds_read_b128 v[216:219], v157 offset:22528
	ds_read_b128 v[220:223], v157 offset:23552
	global_load_lds_dwordx4 v[152:153], off
	s_add_i32 m0, s65, 0x2000
	s_add_u32 s66, s34, 0x80000
	v_lshl_add_u64 v[224:225], s[34:35], 0, v[136:137]
	s_addc_u32 s67, s35, 0
	s_add_i32 s65, s50, s38
	global_load_lds_dwordx4 v[224:225], off
	v_lshl_add_u64 v[226:227], s[66:67], 0, v[132:133]
	s_mov_b32 m0, s65
	v_lshl_add_u64 v[228:229], s[36:37], 0, v[134:135]
	global_load_lds_dwordx4 v[226:227], off
	v_lshl_add_u64 v[226:227], s[66:67], 0, v[136:137]
	s_add_i32 m0, s65, 0x2000
	s_nop 0
	global_load_lds_dwordx4 v[226:227], off
	v_lshl_add_u64 v[226:227], s[36:37], 0, v[130:131]
	s_mov_b32 m0, s39
	s_nop 0
	global_load_lds_dwordx4 v[226:227], off
	s_mov_b32 m0, s40
	s_nop 0
	global_load_lds_dwordx4 v[228:229], off
	s_waitcnt vmcnt(8)
	s_waitcnt lgkmcnt(0)
	s_barrier
	s_setprio 1
	s_waitcnt lgkmcnt(0)
	v_mfma_f32_16x16x32_f16 v[62:65], v[158:161], v[192:195], v[62:65]
	v_mfma_f32_16x16x32_f16 v[58:61], v[166:169], v[192:195], v[58:61]
	v_mfma_f32_16x16x32_f16 v[46:49], v[158:161], v[200:203], v[46:49]
	v_mfma_f32_16x16x32_f16 v[42:45], v[166:169], v[200:203], v[42:45]
	v_mfma_f32_16x16x32_f16 v[30:33], v[158:161], v[208:211], v[30:33]
	v_mfma_f32_16x16x32_f16 v[26:29], v[166:169], v[208:211], v[26:29]
	v_mfma_f32_16x16x32_f16 v[14:17], v[158:161], v[216:219], v[14:17]
	v_mfma_f32_16x16x32_f16 v[10:13], v[166:169], v[216:219], v[10:13]
	v_mfma_f32_16x16x32_f16 v[62:65], v[162:165], v[196:199], v[62:65]
	v_mfma_f32_16x16x32_f16 v[58:61], v[170:173], v[196:199], v[58:61]
	v_mfma_f32_16x16x32_f16 v[46:49], v[162:165], v[204:207], v[46:49]
	v_mfma_f32_16x16x32_f16 v[42:45], v[170:173], v[204:207], v[42:45]
	v_mfma_f32_16x16x32_f16 v[30:33], v[162:165], v[212:215], v[30:33]
	v_mfma_f32_16x16x32_f16 v[26:29], v[170:173], v[212:215], v[26:29]
	v_mfma_f32_16x16x32_f16 v[14:17], v[162:165], v[220:223], v[14:17]
	v_mfma_f32_16x16x32_f16 v[10:13], v[170:173], v[220:223], v[10:13]
	s_setprio 0
	s_setprio 1
	v_mfma_f32_16x16x32_f16 v[54:57], v[174:177], v[192:195], v[54:57]
	v_mfma_f32_16x16x32_f16 v[50:53], v[182:185], v[192:195], v[50:53]
	v_mfma_f32_16x16x32_f16 v[38:41], v[174:177], v[200:203], v[38:41]
	v_mfma_f32_16x16x32_f16 v[34:37], v[182:185], v[200:203], v[34:37]
	v_mfma_f32_16x16x32_f16 v[22:25], v[174:177], v[208:211], v[22:25]
	v_mfma_f32_16x16x32_f16 v[18:21], v[182:185], v[208:211], v[18:21]
	v_mfma_f32_16x16x32_f16 v[6:9], v[174:177], v[216:219], v[6:9]
	v_mfma_f32_16x16x32_f16 v[2:5], v[182:185], v[216:219], v[2:5]
	s_setprio 2
	s_barrier
	v_mfma_f32_16x16x32_f16 v[54:57], v[178:181], v[196:199], v[54:57]
	v_mfma_f32_16x16x32_f16 v[50:53], v[188:191], v[196:199], v[50:53]
	v_mfma_f32_16x16x32_f16 v[38:41], v[178:181], v[204:207], v[38:41]
	v_mfma_f32_16x16x32_f16 v[34:37], v[188:191], v[204:207], v[34:37]
	v_mfma_f32_16x16x32_f16 v[22:25], v[178:181], v[212:215], v[22:25]
	v_mfma_f32_16x16x32_f16 v[18:21], v[188:191], v[212:215], v[18:21]
	v_mfma_f32_16x16x32_f16 v[6:9], v[178:181], v[220:223], v[6:9]
	v_mfma_f32_16x16x32_f16 v[2:5], v[188:191], v[220:223], v[2:5]
	s_setprio 0
	s_nop 0
	s_add_i32 s65, 0, 0x18000
	v_add_u32_e32 v138, s65, v141
	s_add_i32 s66, 0, 0x1c000
	ds_read_b128 v[158:161], v138
	ds_read_b128 v[162:165], v138 offset:1024
	ds_read_b128 v[166:169], v138 offset:2048
	ds_read_b128 v[170:173], v138 offset:3072
	v_add_u32_e32 v138, s66, v141
	ds_read_b128 v[174:177], v138
	ds_read_b128 v[178:181], v138 offset:1024
	ds_read_b128 v[182:185], v138 offset:2048
	ds_read_b128 v[188:191], v138 offset:3072
	s_add_u32 s36, s36, 0x80000
	s_addc_u32 s37, s37, 0
	s_mov_b32 m0, s41
	v_lshl_add_u64 v[230:231], s[36:37], 0, v[130:131]
	ds_read_b128 v[192:195], v157 offset:32768
	ds_read_b128 v[196:199], v157 offset:33792
	ds_read_b128 v[200:203], v157 offset:34816
	ds_read_b128 v[204:207], v157 offset:35840
	ds_read_b128 v[208:211], v157 offset:36864
	ds_read_b128 v[212:215], v157 offset:37888
	ds_read_b128 v[216:219], v157 offset:38912
	ds_read_b128 v[220:223], v157 offset:39936
	global_load_lds_dwordx4 v[230:231], off
	v_lshl_add_u64 v[230:231], s[36:37], 0, v[134:135]
	s_mov_b32 m0, s42
	s_nop 0
	global_load_lds_dwordx4 v[230:231], off
	s_waitcnt vmcnt(8)
	s_waitcnt lgkmcnt(0)
	s_barrier
	s_setprio 1
	s_waitcnt lgkmcnt(0)
	v_mfma_f32_16x16x32_f16 v[126:129], v[158:161], v[192:195], v[126:129]
	v_mfma_f32_16x16x32_f16 v[122:125], v[166:169], v[192:195], v[122:125]
	v_mfma_f32_16x16x32_f16 v[110:113], v[158:161], v[200:203], v[110:113]
	v_mfma_f32_16x16x32_f16 v[106:109], v[166:169], v[200:203], v[106:109]
	v_mfma_f32_16x16x32_f16 v[94:97], v[158:161], v[208:211], v[94:97]
	v_mfma_f32_16x16x32_f16 v[90:93], v[166:169], v[208:211], v[90:93]
	v_mfma_f32_16x16x32_f16 v[78:81], v[158:161], v[216:219], v[78:81]
	v_mfma_f32_16x16x32_f16 v[74:77], v[166:169], v[216:219], v[74:77]
	v_mfma_f32_16x16x32_f16 v[126:129], v[162:165], v[196:199], v[126:129]
	v_mfma_f32_16x16x32_f16 v[122:125], v[170:173], v[196:199], v[122:125]
	v_mfma_f32_16x16x32_f16 v[110:113], v[162:165], v[204:207], v[110:113]
	v_mfma_f32_16x16x32_f16 v[106:109], v[170:173], v[204:207], v[106:109]
	v_mfma_f32_16x16x32_f16 v[94:97], v[162:165], v[212:215], v[94:97]
	v_mfma_f32_16x16x32_f16 v[90:93], v[170:173], v[212:215], v[90:93]
	v_mfma_f32_16x16x32_f16 v[78:81], v[162:165], v[220:223], v[78:81]
	v_mfma_f32_16x16x32_f16 v[74:77], v[170:173], v[220:223], v[74:77]
	s_setprio 0
	s_setprio 1
	v_mfma_f32_16x16x32_f16 v[118:121], v[174:177], v[192:195], v[118:121]
	v_mfma_f32_16x16x32_f16 v[114:117], v[182:185], v[192:195], v[114:117]
	v_mfma_f32_16x16x32_f16 v[102:105], v[174:177], v[200:203], v[102:105]
	v_mfma_f32_16x16x32_f16 v[98:101], v[182:185], v[200:203], v[98:101]
	v_mfma_f32_16x16x32_f16 v[86:89], v[174:177], v[208:211], v[86:89]
	v_mfma_f32_16x16x32_f16 v[82:85], v[182:185], v[208:211], v[82:85]
	v_mfma_f32_16x16x32_f16 v[70:73], v[174:177], v[216:219], v[70:73]
	v_mfma_f32_16x16x32_f16 v[66:69], v[182:185], v[216:219], v[66:69]
	s_setprio 2
	s_barrier
	v_mfma_f32_16x16x32_f16 v[118:121], v[178:181], v[196:199], v[118:121]
	v_mfma_f32_16x16x32_f16 v[114:117], v[188:191], v[196:199], v[114:117]
	v_mfma_f32_16x16x32_f16 v[102:105], v[178:181], v[204:207], v[102:105]
	v_mfma_f32_16x16x32_f16 v[98:101], v[188:191], v[204:207], v[98:101]
	v_mfma_f32_16x16x32_f16 v[86:89], v[178:181], v[212:215], v[86:89]
	v_mfma_f32_16x16x32_f16 v[82:85], v[188:191], v[212:215], v[82:85]
	v_mfma_f32_16x16x32_f16 v[70:73], v[178:181], v[220:223], v[70:73]
	v_mfma_f32_16x16x32_f16 v[66:69], v[188:191], v[220:223], v[66:69]
	s_setprio 0
	s_nop 0
	s_add_i32 s36, s65, s38
	v_lshl_add_u64 v[152:153], v[152:153], 0, s[16:17]
	s_mov_b32 m0, s36
	ds_read_b128 v[192:195], v157 offset:49152
	ds_read_b128 v[196:199], v157 offset:50176
	ds_read_b128 v[200:203], v157 offset:51200
	ds_read_b128 v[204:207], v157 offset:52224
	ds_read_b128 v[208:211], v157 offset:53248
	ds_read_b128 v[212:215], v157 offset:54272
	ds_read_b128 v[216:219], v157 offset:55296
	ds_read_b128 v[220:223], v157 offset:56320
	global_load_lds_dwordx4 v[152:153], off
	s_add_i32 m0, s36, 0x2000
	s_add_u32 s34, s34, 0x80080
	v_lshl_add_u64 v[152:153], v[224:225], 0, s[16:17]
	s_addc_u32 s35, s35, 0
	s_add_i32 s36, s66, s38
	global_load_lds_dwordx4 v[152:153], off
	v_lshl_add_u64 v[152:153], s[34:35], 0, v[132:133]
	s_mov_b32 m0, s36
	s_nop 0
	global_load_lds_dwordx4 v[152:153], off
	v_lshl_add_u64 v[152:153], s[34:35], 0, v[136:137]
	s_add_i32 m0, s36, 0x2000
	s_nop 0
	global_load_lds_dwordx4 v[152:153], off
	v_lshl_add_u64 v[152:153], v[226:227], 0, s[16:17]
	s_mov_b32 m0, s45
	s_nop 0
	global_load_lds_dwordx4 v[152:153], off
	v_lshl_add_u64 v[152:153], v[228:229], 0, s[16:17]
	s_mov_b32 m0, s46
	s_nop 0
	global_load_lds_dwordx4 v[152:153], off
	s_waitcnt vmcnt(8)
	s_waitcnt lgkmcnt(0)
	s_barrier
	s_setprio 1
	s_waitcnt lgkmcnt(0)
	v_mfma_f32_16x16x32_f16 v[62:65], v[158:161], v[192:195], v[62:65]
	v_mfma_f32_16x16x32_f16 v[58:61], v[166:169], v[192:195], v[58:61]
	v_mfma_f32_16x16x32_f16 v[46:49], v[158:161], v[200:203], v[46:49]
	v_mfma_f32_16x16x32_f16 v[42:45], v[166:169], v[200:203], v[42:45]
	v_mfma_f32_16x16x32_f16 v[30:33], v[158:161], v[208:211], v[30:33]
	v_mfma_f32_16x16x32_f16 v[26:29], v[166:169], v[208:211], v[26:29]
	v_mfma_f32_16x16x32_f16 v[14:17], v[158:161], v[216:219], v[14:17]
	v_mfma_f32_16x16x32_f16 v[10:13], v[166:169], v[216:219], v[10:13]
	v_mfma_f32_16x16x32_f16 v[62:65], v[162:165], v[196:199], v[62:65]
	v_mfma_f32_16x16x32_f16 v[58:61], v[170:173], v[196:199], v[58:61]
	v_mfma_f32_16x16x32_f16 v[46:49], v[162:165], v[204:207], v[46:49]
	v_mfma_f32_16x16x32_f16 v[42:45], v[170:173], v[204:207], v[42:45]
	v_mfma_f32_16x16x32_f16 v[30:33], v[162:165], v[212:215], v[30:33]
	v_mfma_f32_16x16x32_f16 v[26:29], v[170:173], v[212:215], v[26:29]
	v_mfma_f32_16x16x32_f16 v[14:17], v[162:165], v[220:223], v[14:17]
	v_mfma_f32_16x16x32_f16 v[10:13], v[170:173], v[220:223], v[10:13]
	s_setprio 0
	s_setprio 1
	v_mfma_f32_16x16x32_f16 v[54:57], v[174:177], v[192:195], v[54:57]
	v_mfma_f32_16x16x32_f16 v[50:53], v[182:185], v[192:195], v[50:53]
	v_mfma_f32_16x16x32_f16 v[38:41], v[174:177], v[200:203], v[38:41]
	v_mfma_f32_16x16x32_f16 v[34:37], v[182:185], v[200:203], v[34:37]
	v_mfma_f32_16x16x32_f16 v[22:25], v[174:177], v[208:211], v[22:25]
	v_mfma_f32_16x16x32_f16 v[18:21], v[182:185], v[208:211], v[18:21]
	v_mfma_f32_16x16x32_f16 v[6:9], v[174:177], v[216:219], v[6:9]
	v_mfma_f32_16x16x32_f16 v[2:5], v[182:185], v[216:219], v[2:5]
	s_setprio 2
	s_barrier
	v_mfma_f32_16x16x32_f16 v[54:57], v[178:181], v[196:199], v[54:57]
	v_mfma_f32_16x16x32_f16 v[50:53], v[188:191], v[196:199], v[50:53]
	v_mfma_f32_16x16x32_f16 v[38:41], v[178:181], v[204:207], v[38:41]
	v_mfma_f32_16x16x32_f16 v[34:37], v[188:191], v[204:207], v[34:37]
	v_mfma_f32_16x16x32_f16 v[22:25], v[178:181], v[212:215], v[22:25]
	v_mfma_f32_16x16x32_f16 v[18:21], v[188:191], v[212:215], v[18:21]
	v_mfma_f32_16x16x32_f16 v[6:9], v[178:181], v[220:223], v[6:9]
	v_mfma_f32_16x16x32_f16 v[2:5], v[188:191], v[220:223], v[2:5]
	s_setprio 0
	s_nop 0
	s_add_i32 s64, s64, 2
	s_add_u32 s30, s30, 0x100
	s_addc_u32 s31, s31, 0
	s_add_u32 s62, s62, 0x100
	s_addc_u32 s63, s63, 0
	s_cmp_gt_u32 s64, 29
	s_cbranch_scc0 .LBB0_973
	s_and_b64 vcc, exec, s[18:19]
	s_cbranch_vccz .LBB0_976
	s_barrier

.LBB0_1120:
	ds_read_b128 v[88:91], v85
	ds_read_b128 v[92:95], v85 offset:1024
	ds_read_b128 v[96:99], v85 offset:2048
	ds_read_b128 v[100:103], v85 offset:3072
	s_add_u32 s26, s24, 0xfffd8080
	s_addc_u32 s27, s25, -1
	s_cmp_eq_u32 s51, 4
	s_cselect_b32 s29, s1, s27
	s_cselect_b32 s28, s0, s26
	s_cselect_b32 s27, s23, s50
	s_cselect_b32 s26, s22, s21
	v_lshl_add_u64 v[136:137], s[24:25], 0, v[76:77]
	s_add_i32 m0, s15, 0xc000
	ds_read_b128 v[104:107], v86
	ds_read_b128 v[108:111], v86 offset:1024
	ds_read_b128 v[112:115], v86 offset:2048
	ds_read_b128 v[116:119], v86 offset:3072
	ds_read_b128 v[120:123], v86 offset:4096
	ds_read_b128 v[124:127], v86 offset:5120
	ds_read_b128 v[128:131], v86 offset:6144
	ds_read_b128 v[132:135], v86 offset:7168
	global_load_lds_dwordx4 v[136:137], off
	v_lshl_add_u64 v[136:137], s[24:25], 0, v[78:79]
	s_add_i32 m0, s15, 0xe000
	s_nop 0
	global_load_lds_dwordx4 v[136:137], off
	s_waitcnt vmcnt(8)
	s_waitcnt lgkmcnt(0)
	s_barrier
	s_setprio 1
	s_waitcnt lgkmcnt(0)
	v_mfma_f32_16x16x32_f16 v[62:65], v[88:91], v[104:107], v[62:65]
	v_mfma_f32_16x16x32_f16 v[58:61], v[96:99], v[104:107], v[58:61]
	v_mfma_f32_16x16x32_f16 v[54:57], v[88:91], v[112:115], v[54:57]
	v_mfma_f32_16x16x32_f16 v[50:53], v[96:99], v[112:115], v[50:53]
	v_mfma_f32_16x16x32_f16 v[46:49], v[88:91], v[120:123], v[46:49]
	v_mfma_f32_16x16x32_f16 v[42:45], v[96:99], v[120:123], v[42:45]
	v_mfma_f32_16x16x32_f16 v[38:41], v[88:91], v[128:131], v[38:41]
	v_mfma_f32_16x16x32_f16 v[34:37], v[96:99], v[128:131], v[34:37]
	s_setprio 2
	s_barrier
	v_mfma_f32_16x16x32_f16 v[62:65], v[92:95], v[108:111], v[62:65]
	v_mfma_f32_16x16x32_f16 v[58:61], v[100:103], v[108:111], v[58:61]
	v_mfma_f32_16x16x32_f16 v[54:57], v[92:95], v[116:119], v[54:57]
	v_mfma_f32_16x16x32_f16 v[50:53], v[100:103], v[116:119], v[50:53]
	v_mfma_f32_16x16x32_f16 v[46:49], v[92:95], v[124:127], v[46:49]
	v_mfma_f32_16x16x32_f16 v[42:45], v[100:103], v[124:127], v[42:45]
	v_mfma_f32_16x16x32_f16 v[38:41], v[92:95], v[132:135], v[38:41]
	v_mfma_f32_16x16x32_f16 v[34:37], v[100:103], v[132:135], v[34:37]
	s_setprio 0
	s_setprio 1
	s_setprio 0
	s_nop 0
	s_add_i32 s60, s48, s34
	v_lshl_add_u64 v[136:137], s[26:27], 0, v[70:71]
	s_mov_b32 m0, s60
	ds_read_b128 v[104:107], v86 offset:16384
	ds_read_b128 v[108:111], v86 offset:17408
	ds_read_b128 v[112:115], v86 offset:18432
	ds_read_b128 v[116:119], v86 offset:19456
	ds_read_b128 v[120:123], v86 offset:20480
	ds_read_b128 v[124:127], v86 offset:21504
	ds_read_b128 v[128:131], v86 offset:22528
	ds_read_b128 v[132:135], v86 offset:23552
	global_load_lds_dwordx4 v[136:137], off
	s_add_i32 m0, s60, 0x2000
	s_add_u32 s60, s26, 0x20000
	v_lshl_add_u64 v[138:139], s[26:27], 0, v[66:67]
	s_addc_u32 s61, s27, 0
	global_load_lds_dwordx4 v[138:139], off
	v_lshl_add_u64 v[140:141], s[60:61], 0, v[70:71]
	s_mov_b32 m0, s35
	v_lshl_add_u64 v[142:143], s[28:29], 0, v[68:69]
	global_load_lds_dwordx4 v[140:141], off
	v_lshl_add_u64 v[140:141], s[60:61], 0, v[66:67]
	s_mov_b32 m0, s36
	s_nop 0
	global_load_lds_dwordx4 v[140:141], off
	v_lshl_add_u64 v[140:141], s[28:29], 0, v[72:73]
	s_mov_b32 m0, s15
	s_nop 0
	global_load_lds_dwordx4 v[140:141], off
	s_mov_b32 m0, s37
	s_nop 0
	global_load_lds_dwordx4 v[142:143], off
	s_waitcnt vmcnt(8)
	s_waitcnt lgkmcnt(0)
	s_barrier
	s_setprio 1
	s_waitcnt lgkmcnt(0)
	v_mfma_f32_16x16x32_f16 v[30:33], v[88:91], v[104:107], v[30:33]
	v_mfma_f32_16x16x32_f16 v[26:29], v[96:99], v[104:107], v[26:29]
	v_mfma_f32_16x16x32_f16 v[22:25], v[88:91], v[112:115], v[22:25]
	v_mfma_f32_16x16x32_f16 v[18:21], v[96:99], v[112:115], v[18:21]
	v_mfma_f32_16x16x32_f16 v[14:17], v[88:91], v[120:123], v[14:17]
	v_mfma_f32_16x16x32_f16 v[10:13], v[96:99], v[120:123], v[10:13]
	v_mfma_f32_16x16x32_f16 v[6:9], v[88:91], v[128:131], v[6:9]
	v_mfma_f32_16x16x32_f16 v[2:5], v[96:99], v[128:131], v[2:5]
	s_setprio 2
	s_barrier
	v_mfma_f32_16x16x32_f16 v[30:33], v[92:95], v[108:111], v[30:33]
	v_mfma_f32_16x16x32_f16 v[26:29], v[100:103], v[108:111], v[26:29]
	v_mfma_f32_16x16x32_f16 v[22:25], v[92:95], v[116:119], v[22:25]
	v_mfma_f32_16x16x32_f16 v[18:21], v[100:103], v[116:119], v[18:21]
	v_mfma_f32_16x16x32_f16 v[14:17], v[92:95], v[124:127], v[14:17]
	v_mfma_f32_16x16x32_f16 v[10:13], v[100:103], v[124:127], v[10:13]
	v_mfma_f32_16x16x32_f16 v[6:9], v[92:95], v[132:135], v[6:9]
	v_mfma_f32_16x16x32_f16 v[2:5], v[100:103], v[132:135], v[2:5]
	s_setprio 0
	s_setprio 1
	s_setprio 0
	s_nop 0
	s_add_i32 s60, 0, 0x18000
	v_add_u32_e32 v87, s60, v84
	ds_read_b128 v[88:91], v87
	ds_read_b128 v[92:95], v87 offset:1024
	ds_read_b128 v[96:99], v87 offset:2048
	ds_read_b128 v[100:103], v87 offset:3072
	s_add_u32 s28, s28, 0x28000
	s_addc_u32 s29, s29, 0
	s_mov_b32 m0, s38
	v_lshl_add_u64 v[144:145], s[28:29], 0, v[72:73]
	ds_read_b128 v[104:107], v86 offset:32768
	ds_read_b128 v[108:111], v86 offset:33792
	ds_read_b128 v[112:115], v86 offset:34816
	ds_read_b128 v[116:119], v86 offset:35840
	ds_read_b128 v[120:123], v86 offset:36864
	ds_read_b128 v[124:127], v86 offset:37888
	ds_read_b128 v[128:131], v86 offset:38912
	ds_read_b128 v[132:135], v86 offset:39936
	global_load_lds_dwordx4 v[144:145], off
	v_lshl_add_u64 v[144:145], s[28:29], 0, v[68:69]
	s_mov_b32 m0, s39
	s_nop 0
	global_load_lds_dwordx4 v[144:145], off
	s_waitcnt vmcnt(8)
	s_waitcnt lgkmcnt(0)
	s_barrier
	s_setprio 1
	s_waitcnt lgkmcnt(0)
	v_mfma_f32_16x16x32_f16 v[62:65], v[88:91], v[104:107], v[62:65]
	v_mfma_f32_16x16x32_f16 v[58:61], v[96:99], v[104:107], v[58:61]
	v_mfma_f32_16x16x32_f16 v[54:57], v[88:91], v[112:115], v[54:57]
	v_mfma_f32_16x16x32_f16 v[50:53], v[96:99], v[112:115], v[50:53]
	v_mfma_f32_16x16x32_f16 v[46:49], v[88:91], v[120:123], v[46:49]
	v_mfma_f32_16x16x32_f16 v[42:45], v[96:99], v[120:123], v[42:45]
	v_mfma_f32_16x16x32_f16 v[38:41], v[88:91], v[128:131], v[38:41]
	v_mfma_f32_16x16x32_f16 v[34:37], v[96:99], v[128:131], v[34:37]
	s_setprio 2
	s_barrier
	v_mfma_f32_16x16x32_f16 v[62:65], v[92:95], v[108:111], v[62:65]
	v_mfma_f32_16x16x32_f16 v[58:61], v[100:103], v[108:111], v[58:61]
	v_mfma_f32_16x16x32_f16 v[54:57], v[92:95], v[116:119], v[54:57]
	v_mfma_f32_16x16x32_f16 v[50:53], v[100:103], v[116:119], v[50:53]
	v_mfma_f32_16x16x32_f16 v[46:49], v[92:95], v[124:127], v[46:49]
	v_mfma_f32_16x16x32_f16 v[42:45], v[100:103], v[124:127], v[42:45]
	v_mfma_f32_16x16x32_f16 v[38:41], v[92:95], v[132:135], v[38:41]
	v_mfma_f32_16x16x32_f16 v[34:37], v[100:103], v[132:135], v[34:37]
	s_setprio 0
	s_setprio 1
	s_setprio 0
	s_nop 0
	s_add_i32 s28, s60, s34
	v_lshl_add_u64 v[136:137], v[136:137], 0, s[16:17]
	s_mov_b32 m0, s28
	ds_read_b128 v[104:107], v86 offset:49152
	ds_read_b128 v[108:111], v86 offset:50176
	ds_read_b128 v[112:115], v86 offset:51200
	ds_read_b128 v[116:119], v86 offset:52224
	ds_read_b128 v[120:123], v86 offset:53248
	ds_read_b128 v[124:127], v86 offset:54272
	ds_read_b128 v[128:131], v86 offset:55296
	ds_read_b128 v[132:135], v86 offset:56320
	global_load_lds_dwordx4 v[136:137], off
	s_add_i32 m0, s28, 0x2000
	s_add_u32 s26, s26, 0x20080
	v_lshl_add_u64 v[136:137], v[138:139], 0, s[16:17]
	s_addc_u32 s27, s27, 0
	global_load_lds_dwordx4 v[136:137], off
	v_lshl_add_u64 v[136:137], s[26:27], 0, v[70:71]
	s_mov_b32 m0, s45
	s_nop 0
	global_load_lds_dwordx4 v[136:137], off
	v_lshl_add_u64 v[136:137], s[26:27], 0, v[66:67]
	s_mov_b32 m0, s46
	s_nop 0
	global_load_lds_dwordx4 v[136:137], off
	v_lshl_add_u64 v[136:137], v[140:141], 0, s[16:17]
	s_mov_b32 m0, s43
	s_nop 0
	global_load_lds_dwordx4 v[136:137], off
	v_lshl_add_u64 v[136:137], v[142:143], 0, s[16:17]
	s_mov_b32 m0, s44
	s_nop 0
	global_load_lds_dwordx4 v[136:137], off
	s_waitcnt vmcnt(8)
	s_waitcnt lgkmcnt(0)
	s_barrier
	s_setprio 1
	s_waitcnt lgkmcnt(0)
	v_mfma_f32_16x16x32_f16 v[30:33], v[88:91], v[104:107], v[30:33]
	v_mfma_f32_16x16x32_f16 v[26:29], v[96:99], v[104:107], v[26:29]
	v_mfma_f32_16x16x32_f16 v[22:25], v[88:91], v[112:115], v[22:25]
	v_mfma_f32_16x16x32_f16 v[18:21], v[96:99], v[112:115], v[18:21]
	v_mfma_f32_16x16x32_f16 v[14:17], v[88:91], v[120:123], v[14:17]
	v_mfma_f32_16x16x32_f16 v[10:13], v[96:99], v[120:123], v[10:13]
	v_mfma_f32_16x16x32_f16 v[6:9], v[88:91], v[128:131], v[6:9]
	v_mfma_f32_16x16x32_f16 v[2:5], v[96:99], v[128:131], v[2:5]
	s_setprio 2
	s_barrier
	v_mfma_f32_16x16x32_f16 v[30:33], v[92:95], v[108:111], v[30:33]
	v_mfma_f32_16x16x32_f16 v[26:29], v[100:103], v[108:111], v[26:29]
	v_mfma_f32_16x16x32_f16 v[22:25], v[92:95], v[116:119], v[22:25]
	v_mfma_f32_16x16x32_f16 v[18:21], v[100:103], v[116:119], v[18:21]
	v_mfma_f32_16x16x32_f16 v[14:17], v[92:95], v[124:127], v[14:17]
	v_mfma_f32_16x16x32_f16 v[10:13], v[100:103], v[124:127], v[10:13]
	v_mfma_f32_16x16x32_f16 v[6:9], v[92:95], v[132:135], v[6:9]
	v_mfma_f32_16x16x32_f16 v[2:5], v[100:103], v[132:135], v[2:5]
	s_setprio 0
	s_setprio 1
	s_setprio 0
	s_nop 0
	s_add_i32 s51, s51, 2
	s_add_u32 s24, s24, 0x100
	s_addc_u32 s25, s25, 0
	s_add_u32 s21, s21, 0x100
	s_addc_u32 s50, s50, 0
	s_cmp_gt_u32 s51, 5
	s_cbranch_scc0 .LBB0_1120
	s_and_b64 vcc, exec, s[18:19]
	s_cbranch_vccz .LBB0_1123
	s_barrier

.LBB0_1649:
	ds_read_b128 v[98:101], v174
	ds_read_b128 v[102:105], v174 offset:1024
	ds_read_b128 v[158:161], v174 offset:2048
	ds_read_b128 v[164:167], v174 offset:3072
	ds_read_b128 v[178:181], v175
	ds_read_b128 v[182:185], v175 offset:1024
	ds_read_b128 v[188:191], v175 offset:2048
	ds_read_b128 v[192:195], v175 offset:3072
	s_add_u32 s22, s20, 0xfffd8080
	s_addc_u32 s23, s21, -1
	s_cmp_eq_u32 s50, 6
	s_cselect_b32 s25, s1, s23
	s_cselect_b32 s24, s0, s22
	s_cselect_b32 s23, s19, s49
	s_cselect_b32 s22, s18, s48
	v_lshl_add_u64 v[168:169], s[20:21], 0, v[150:151]
	s_add_i32 m0, s29, 0xc000
	ds_read_b128 v[196:199], v176
	ds_read_b128 v[200:203], v176 offset:1024
	ds_read_b128 v[204:207], v176 offset:2048
	ds_read_b128 v[208:211], v176 offset:3072
	ds_read_b128 v[212:215], v176 offset:4096
	ds_read_b128 v[216:219], v176 offset:5120
	ds_read_b128 v[220:223], v176 offset:6144
	ds_read_b128 v[224:227], v176 offset:7168
	global_load_lds_dwordx4 v[168:169], off
	v_lshl_add_u64 v[168:169], s[20:21], 0, v[152:153]
	s_add_i32 m0, s29, 0xe000
	s_nop 0
	global_load_lds_dwordx4 v[168:169], off
	s_waitcnt vmcnt(8)
	s_waitcnt lgkmcnt(0)
	s_barrier
	s_setprio 1
	s_waitcnt lgkmcnt(0)
	v_mfma_f32_16x16x32_f16 v[134:137], v[98:101], v[196:199], v[134:137]
	v_mfma_f32_16x16x32_f16 v[130:133], v[158:161], v[196:199], v[130:133]
	v_mfma_f32_16x16x32_f16 v[126:129], v[98:101], v[204:207], v[126:129]
	v_mfma_f32_16x16x32_f16 v[122:125], v[158:161], v[204:207], v[122:125]
	v_mfma_f32_16x16x32_f16 v[118:121], v[98:101], v[212:215], v[118:121]
	v_mfma_f32_16x16x32_f16 v[114:117], v[158:161], v[212:215], v[114:117]
	v_mfma_f32_16x16x32_f16 v[110:113], v[98:101], v[220:223], v[110:113]
	v_mfma_f32_16x16x32_f16 v[106:109], v[158:161], v[220:223], v[106:109]
	v_mfma_f32_16x16x32_f16 v[134:137], v[102:105], v[200:203], v[134:137]
	v_mfma_f32_16x16x32_f16 v[130:133], v[164:167], v[200:203], v[130:133]
	v_mfma_f32_16x16x32_f16 v[126:129], v[102:105], v[208:211], v[126:129]
	v_mfma_f32_16x16x32_f16 v[122:125], v[164:167], v[208:211], v[122:125]
	v_mfma_f32_16x16x32_f16 v[118:121], v[102:105], v[216:219], v[118:121]
	v_mfma_f32_16x16x32_f16 v[114:117], v[164:167], v[216:219], v[114:117]
	v_mfma_f32_16x16x32_f16 v[110:113], v[102:105], v[224:227], v[110:113]
	v_mfma_f32_16x16x32_f16 v[106:109], v[164:167], v[224:227], v[106:109]
	s_setprio 0
	s_setprio 1
	v_mfma_f32_16x16x32_f16 v[62:65], v[178:181], v[196:199], v[62:65]
	v_mfma_f32_16x16x32_f16 v[58:61], v[188:191], v[196:199], v[58:61]
	v_mfma_f32_16x16x32_f16 v[54:57], v[178:181], v[204:207], v[54:57]
	v_mfma_f32_16x16x32_f16 v[50:53], v[188:191], v[204:207], v[50:53]
	v_mfma_f32_16x16x32_f16 v[46:49], v[178:181], v[212:215], v[46:49]
	v_mfma_f32_16x16x32_f16 v[42:45], v[188:191], v[212:215], v[42:45]
	v_mfma_f32_16x16x32_f16 v[38:41], v[178:181], v[220:223], v[38:41]
	v_mfma_f32_16x16x32_f16 v[34:37], v[188:191], v[220:223], v[34:37]
	s_setprio 2
	s_barrier
	v_mfma_f32_16x16x32_f16 v[62:65], v[182:185], v[200:203], v[62:65]
	v_mfma_f32_16x16x32_f16 v[58:61], v[192:195], v[200:203], v[58:61]
	v_mfma_f32_16x16x32_f16 v[54:57], v[182:185], v[208:211], v[54:57]
	v_mfma_f32_16x16x32_f16 v[50:53], v[192:195], v[208:211], v[50:53]
	v_mfma_f32_16x16x32_f16 v[46:49], v[182:185], v[216:219], v[46:49]
	v_mfma_f32_16x16x32_f16 v[42:45], v[192:195], v[216:219], v[42:45]
	v_mfma_f32_16x16x32_f16 v[38:41], v[182:185], v[224:227], v[38:41]
	v_mfma_f32_16x16x32_f16 v[34:37], v[192:195], v[224:227], v[34:37]
	s_setprio 0
	s_nop 0
	s_add_i32 s51, s39, s27
	v_lshl_add_u64 v[168:169], s[22:23], 0, v[142:143]
	s_mov_b32 m0, s51
	ds_read_b128 v[196:199], v176 offset:16384
	ds_read_b128 v[200:203], v176 offset:17408
	ds_read_b128 v[204:207], v176 offset:18432
	ds_read_b128 v[208:211], v176 offset:19456
	ds_read_b128 v[212:215], v176 offset:20480
	ds_read_b128 v[216:219], v176 offset:21504
	ds_read_b128 v[220:223], v176 offset:22528
	ds_read_b128 v[224:227], v176 offset:23552
	global_load_lds_dwordx4 v[168:169], off
	s_add_i32 m0, s51, 0x2000
	s_add_u32 s60, s22, 0x28000
	v_lshl_add_u64 v[228:229], s[22:23], 0, v[138:139]
	s_addc_u32 s61, s23, 0
	s_add_i32 s51, s40, s27
	global_load_lds_dwordx4 v[228:229], off
	v_lshl_add_u64 v[230:231], s[60:61], 0, v[142:143]
	s_mov_b32 m0, s51
	v_lshl_add_u64 v[232:233], s[24:25], 0, v[140:141]
	global_load_lds_dwordx4 v[230:231], off
	v_lshl_add_u64 v[230:231], s[60:61], 0, v[138:139]
	s_add_i32 m0, s51, 0x2000
	s_nop 0
	global_load_lds_dwordx4 v[230:231], off
	v_lshl_add_u64 v[230:231], s[24:25], 0, v[144:145]
	s_mov_b32 m0, s29
	s_nop 0
	global_load_lds_dwordx4 v[230:231], off
	s_mov_b32 m0, s30
	s_nop 0
	global_load_lds_dwordx4 v[232:233], off
	s_waitcnt vmcnt(8)
	s_waitcnt lgkmcnt(0)
	s_barrier
	s_setprio 1
	s_waitcnt lgkmcnt(0)
	v_mfma_f32_16x16x32_f16 v[94:97], v[98:101], v[196:199], v[94:97]
	v_mfma_f32_16x16x32_f16 v[90:93], v[158:161], v[196:199], v[90:93]
	v_mfma_f32_16x16x32_f16 v[86:89], v[98:101], v[204:207], v[86:89]
	v_mfma_f32_16x16x32_f16 v[82:85], v[158:161], v[204:207], v[82:85]
	v_mfma_f32_16x16x32_f16 v[78:81], v[98:101], v[212:215], v[78:81]
	v_mfma_f32_16x16x32_f16 v[74:77], v[158:161], v[212:215], v[74:77]
	v_mfma_f32_16x16x32_f16 v[70:73], v[98:101], v[220:223], v[70:73]
	v_mfma_f32_16x16x32_f16 v[66:69], v[158:161], v[220:223], v[66:69]
	v_mfma_f32_16x16x32_f16 v[94:97], v[102:105], v[200:203], v[94:97]
	v_mfma_f32_16x16x32_f16 v[90:93], v[164:167], v[200:203], v[90:93]
	v_mfma_f32_16x16x32_f16 v[86:89], v[102:105], v[208:211], v[86:89]
	v_mfma_f32_16x16x32_f16 v[82:85], v[164:167], v[208:211], v[82:85]
	v_mfma_f32_16x16x32_f16 v[78:81], v[102:105], v[216:219], v[78:81]
	v_mfma_f32_16x16x32_f16 v[74:77], v[164:167], v[216:219], v[74:77]
	v_mfma_f32_16x16x32_f16 v[70:73], v[102:105], v[224:227], v[70:73]
	v_mfma_f32_16x16x32_f16 v[66:69], v[164:167], v[224:227], v[66:69]
	s_setprio 0
	s_setprio 1
	v_mfma_f32_16x16x32_f16 v[30:33], v[178:181], v[196:199], v[30:33]
	v_mfma_f32_16x16x32_f16 v[26:29], v[188:191], v[196:199], v[26:29]
	v_mfma_f32_16x16x32_f16 v[22:25], v[178:181], v[204:207], v[22:25]
	v_mfma_f32_16x16x32_f16 v[18:21], v[188:191], v[204:207], v[18:21]
	v_mfma_f32_16x16x32_f16 v[14:17], v[178:181], v[212:215], v[14:17]
	v_mfma_f32_16x16x32_f16 v[10:13], v[188:191], v[212:215], v[10:13]
	v_mfma_f32_16x16x32_f16 v[6:9], v[178:181], v[220:223], v[6:9]
	v_mfma_f32_16x16x32_f16 v[2:5], v[188:191], v[220:223], v[2:5]
	s_setprio 2
	s_barrier
	v_mfma_f32_16x16x32_f16 v[30:33], v[182:185], v[200:203], v[30:33]
	v_mfma_f32_16x16x32_f16 v[26:29], v[192:195], v[200:203], v[26:29]
	v_mfma_f32_16x16x32_f16 v[22:25], v[182:185], v[208:211], v[22:25]
	v_mfma_f32_16x16x32_f16 v[18:21], v[192:195], v[208:211], v[18:21]
	v_mfma_f32_16x16x32_f16 v[14:17], v[182:185], v[216:219], v[14:17]
	v_mfma_f32_16x16x32_f16 v[10:13], v[192:195], v[216:219], v[10:13]
	v_mfma_f32_16x16x32_f16 v[6:9], v[182:185], v[224:227], v[6:9]
	v_mfma_f32_16x16x32_f16 v[2:5], v[192:195], v[224:227], v[2:5]
	s_setprio 0
	s_nop 0
	s_add_i32 s51, 0, 0x18000
	s_add_i32 s60, 0, 0x1c000
	v_add_u32_e32 v164, s51, v163
	v_add_u32_e32 v177, s60, v163
	ds_read_b128 v[98:101], v164
	ds_read_b128 v[102:105], v164 offset:1024
	ds_read_b128 v[158:161], v164 offset:2048
	ds_read_b128 v[164:167], v164 offset:3072
	ds_read_b128 v[178:181], v177
	ds_read_b128 v[182:185], v177 offset:1024
	ds_read_b128 v[188:191], v177 offset:2048
	ds_read_b128 v[192:195], v177 offset:3072
	s_add_u32 s24, s24, 0x28000
	s_addc_u32 s25, s25, 0
	s_mov_b32 m0, s31
	v_lshl_add_u64 v[234:235], s[24:25], 0, v[144:145]
	ds_read_b128 v[196:199], v176 offset:32768
	ds_read_b128 v[200:203], v176 offset:33792
	ds_read_b128 v[204:207], v176 offset:34816
	ds_read_b128 v[208:211], v176 offset:35840
	ds_read_b128 v[212:215], v176 offset:36864
	ds_read_b128 v[216:219], v176 offset:37888
	ds_read_b128 v[220:223], v176 offset:38912
	ds_read_b128 v[224:227], v176 offset:39936
	global_load_lds_dwordx4 v[234:235], off
	v_lshl_add_u64 v[234:235], s[24:25], 0, v[140:141]
	s_mov_b32 m0, s33
	s_nop 0
	global_load_lds_dwordx4 v[234:235], off
	s_waitcnt vmcnt(8)
	s_waitcnt lgkmcnt(0)
	s_barrier
	s_setprio 1
	s_waitcnt lgkmcnt(0)
	v_mfma_f32_16x16x32_f16 v[134:137], v[98:101], v[196:199], v[134:137]
	v_mfma_f32_16x16x32_f16 v[130:133], v[158:161], v[196:199], v[130:133]
	v_mfma_f32_16x16x32_f16 v[126:129], v[98:101], v[204:207], v[126:129]
	v_mfma_f32_16x16x32_f16 v[122:125], v[158:161], v[204:207], v[122:125]
	v_mfma_f32_16x16x32_f16 v[118:121], v[98:101], v[212:215], v[118:121]
	v_mfma_f32_16x16x32_f16 v[114:117], v[158:161], v[212:215], v[114:117]
	v_mfma_f32_16x16x32_f16 v[110:113], v[98:101], v[220:223], v[110:113]
	v_mfma_f32_16x16x32_f16 v[106:109], v[158:161], v[220:223], v[106:109]
	v_mfma_f32_16x16x32_f16 v[134:137], v[102:105], v[200:203], v[134:137]
	v_mfma_f32_16x16x32_f16 v[130:133], v[164:167], v[200:203], v[130:133]
	v_mfma_f32_16x16x32_f16 v[126:129], v[102:105], v[208:211], v[126:129]
	v_mfma_f32_16x16x32_f16 v[122:125], v[164:167], v[208:211], v[122:125]
	v_mfma_f32_16x16x32_f16 v[118:121], v[102:105], v[216:219], v[118:121]
	v_mfma_f32_16x16x32_f16 v[114:117], v[164:167], v[216:219], v[114:117]
	v_mfma_f32_16x16x32_f16 v[110:113], v[102:105], v[224:227], v[110:113]
	v_mfma_f32_16x16x32_f16 v[106:109], v[164:167], v[224:227], v[106:109]
	s_setprio 0
	s_setprio 1
	v_mfma_f32_16x16x32_f16 v[62:65], v[178:181], v[196:199], v[62:65]
	v_mfma_f32_16x16x32_f16 v[58:61], v[188:191], v[196:199], v[58:61]
	v_mfma_f32_16x16x32_f16 v[54:57], v[178:181], v[204:207], v[54:57]
	v_mfma_f32_16x16x32_f16 v[50:53], v[188:191], v[204:207], v[50:53]
	v_mfma_f32_16x16x32_f16 v[46:49], v[178:181], v[212:215], v[46:49]
	v_mfma_f32_16x16x32_f16 v[42:45], v[188:191], v[212:215], v[42:45]
	v_mfma_f32_16x16x32_f16 v[38:41], v[178:181], v[220:223], v[38:41]
	v_mfma_f32_16x16x32_f16 v[34:37], v[188:191], v[220:223], v[34:37]
	s_setprio 2
	s_barrier
	v_mfma_f32_16x16x32_f16 v[62:65], v[182:185], v[200:203], v[62:65]
	v_mfma_f32_16x16x32_f16 v[58:61], v[192:195], v[200:203], v[58:61]
	v_mfma_f32_16x16x32_f16 v[54:57], v[182:185], v[208:211], v[54:57]
	v_mfma_f32_16x16x32_f16 v[50:53], v[192:195], v[208:211], v[50:53]
	v_mfma_f32_16x16x32_f16 v[46:49], v[182:185], v[216:219], v[46:49]
	v_mfma_f32_16x16x32_f16 v[42:45], v[192:195], v[216:219], v[42:45]
	v_mfma_f32_16x16x32_f16 v[38:41], v[182:185], v[224:227], v[38:41]
	v_mfma_f32_16x16x32_f16 v[34:37], v[192:195], v[224:227], v[34:37]
	s_setprio 0
	s_nop 0
	s_add_i32 s24, s51, s27
	v_lshl_add_u64 v[168:169], v[168:169], 0, s[14:15]
	s_mov_b32 m0, s24
	ds_read_b128 v[196:199], v176 offset:49152
	ds_read_b128 v[200:203], v176 offset:50176
	ds_read_b128 v[204:207], v176 offset:51200
	ds_read_b128 v[208:211], v176 offset:52224
	ds_read_b128 v[212:215], v176 offset:53248
	ds_read_b128 v[216:219], v176 offset:54272
	ds_read_b128 v[220:223], v176 offset:55296
	ds_read_b128 v[224:227], v176 offset:56320
	global_load_lds_dwordx4 v[168:169], off
	s_add_i32 m0, s24, 0x2000
	s_add_u32 s22, s22, 0x28080
	v_lshl_add_u64 v[168:169], v[228:229], 0, s[14:15]
	s_addc_u32 s23, s23, 0
	s_add_i32 s24, s60, s27
	global_load_lds_dwordx4 v[168:169], off
	v_lshl_add_u64 v[168:169], s[22:23], 0, v[142:143]
	s_mov_b32 m0, s24
	s_nop 0
	global_load_lds_dwordx4 v[168:169], off
	v_lshl_add_u64 v[168:169], s[22:23], 0, v[138:139]
	s_add_i32 m0, s24, 0x2000
	s_nop 0
	global_load_lds_dwordx4 v[168:169], off
	v_lshl_add_u64 v[168:169], v[230:231], 0, s[14:15]
	s_mov_b32 m0, s36
	s_nop 0
	global_load_lds_dwordx4 v[168:169], off
	v_lshl_add_u64 v[168:169], v[232:233], 0, s[14:15]
	s_mov_b32 m0, s37
	s_nop 0
	global_load_lds_dwordx4 v[168:169], off
	s_waitcnt vmcnt(8)
	s_waitcnt lgkmcnt(0)
	s_barrier
	s_setprio 1
	s_waitcnt lgkmcnt(0)
	v_mfma_f32_16x16x32_f16 v[94:97], v[98:101], v[196:199], v[94:97]
	v_mfma_f32_16x16x32_f16 v[90:93], v[158:161], v[196:199], v[90:93]
	v_mfma_f32_16x16x32_f16 v[86:89], v[98:101], v[204:207], v[86:89]
	v_mfma_f32_16x16x32_f16 v[82:85], v[158:161], v[204:207], v[82:85]
	v_mfma_f32_16x16x32_f16 v[78:81], v[98:101], v[212:215], v[78:81]
	v_mfma_f32_16x16x32_f16 v[74:77], v[158:161], v[212:215], v[74:77]
	v_mfma_f32_16x16x32_f16 v[70:73], v[98:101], v[220:223], v[70:73]
	v_mfma_f32_16x16x32_f16 v[66:69], v[158:161], v[220:223], v[66:69]
	v_mfma_f32_16x16x32_f16 v[94:97], v[102:105], v[200:203], v[94:97]
	v_mfma_f32_16x16x32_f16 v[90:93], v[164:167], v[200:203], v[90:93]
	v_mfma_f32_16x16x32_f16 v[86:89], v[102:105], v[208:211], v[86:89]
	v_mfma_f32_16x16x32_f16 v[82:85], v[164:167], v[208:211], v[82:85]
	v_mfma_f32_16x16x32_f16 v[78:81], v[102:105], v[216:219], v[78:81]
	v_mfma_f32_16x16x32_f16 v[74:77], v[164:167], v[216:219], v[74:77]
	v_mfma_f32_16x16x32_f16 v[70:73], v[102:105], v[224:227], v[70:73]
	v_mfma_f32_16x16x32_f16 v[66:69], v[164:167], v[224:227], v[66:69]
	s_setprio 0
	s_setprio 1
	v_mfma_f32_16x16x32_f16 v[30:33], v[178:181], v[196:199], v[30:33]
	v_mfma_f32_16x16x32_f16 v[26:29], v[188:191], v[196:199], v[26:29]
	v_mfma_f32_16x16x32_f16 v[22:25], v[178:181], v[204:207], v[22:25]
	v_mfma_f32_16x16x32_f16 v[18:21], v[188:191], v[204:207], v[18:21]
	v_mfma_f32_16x16x32_f16 v[14:17], v[178:181], v[212:215], v[14:17]
	v_mfma_f32_16x16x32_f16 v[10:13], v[188:191], v[212:215], v[10:13]
	v_mfma_f32_16x16x32_f16 v[6:9], v[178:181], v[220:223], v[6:9]
	v_mfma_f32_16x16x32_f16 v[2:5], v[188:191], v[220:223], v[2:5]
	s_setprio 2
	s_barrier
	v_mfma_f32_16x16x32_f16 v[30:33], v[182:185], v[200:203], v[30:33]
	v_mfma_f32_16x16x32_f16 v[26:29], v[192:195], v[200:203], v[26:29]
	v_mfma_f32_16x16x32_f16 v[22:25], v[182:185], v[208:211], v[22:25]
	v_mfma_f32_16x16x32_f16 v[18:21], v[192:195], v[208:211], v[18:21]
	v_mfma_f32_16x16x32_f16 v[14:17], v[182:185], v[216:219], v[14:17]
	v_mfma_f32_16x16x32_f16 v[10:13], v[192:195], v[216:219], v[10:13]
	v_mfma_f32_16x16x32_f16 v[6:9], v[182:185], v[224:227], v[6:9]
	v_mfma_f32_16x16x32_f16 v[2:5], v[192:195], v[224:227], v[2:5]
	s_setprio 0
	s_nop 0
	s_add_i32 s50, s50, 2
	s_add_u32 s20, s20, 0x100
	s_addc_u32 s21, s21, 0
	s_add_u32 s48, s48, 0x100
	s_addc_u32 s49, s49, 0
	s_cmp_gt_u32 s50, 7
	s_cbranch_scc0 .LBB0_1649
	s_and_b64 vcc, exec, s[16:17]
	s_cbranch_vccz .LBB0_1652
	s_barrier

.LBB0_1734:
	ds_read_b128 v[130:133], v177
	ds_read_b128 v[134:137], v177 offset:1024
	ds_read_b128 v[138:141], v177 offset:2048
	ds_read_b128 v[142:145], v177 offset:3072
	ds_read_b128 v[164:167], v178
	ds_read_b128 v[168:171], v178 offset:1024
	ds_read_b128 v[172:175], v178 offset:2048
	ds_read_b128 v[180:183], v178 offset:3072
	s_add_u32 s28, s26, 0xfffc0080
	s_addc_u32 s29, s27, -1
	s_cmp_eq_u32 s50, 12
	s_cselect_b32 s31, s19, s29
	s_cselect_b32 s30, s46, s28
	s_cselect_b32 s29, s17, s49
	s_cselect_b32 s28, s47, s48
	v_lshl_add_u64 v[184:185], s[26:27], 0, v[154:155]
	s_add_i32 m0, s25, 0xc000
	ds_read_b128 v[188:191], v179
	ds_read_b128 v[192:195], v179 offset:1024
	ds_read_b128 v[196:199], v179 offset:2048
	ds_read_b128 v[200:203], v179 offset:3072
	ds_read_b128 v[204:207], v179 offset:4096
	ds_read_b128 v[208:211], v179 offset:5120
	ds_read_b128 v[212:215], v179 offset:6144
	ds_read_b128 v[216:219], v179 offset:7168
	global_load_lds_dwordx4 v[184:185], off
	v_lshl_add_u64 v[184:185], s[26:27], 0, v[156:157]
	s_add_i32 m0, s25, 0xe000
	s_nop 0
	global_load_lds_dwordx4 v[184:185], off
	s_waitcnt vmcnt(8)
	s_waitcnt lgkmcnt(0)
	s_barrier
	s_setprio 1
	s_waitcnt lgkmcnt(0)
	v_mfma_f32_16x16x32_f16 v[126:129], v[130:133], v[188:191], v[126:129]
	v_mfma_f32_16x16x32_f16 v[122:125], v[138:141], v[188:191], v[122:125]
	v_mfma_f32_16x16x32_f16 v[118:121], v[130:133], v[196:199], v[118:121]
	v_mfma_f32_16x16x32_f16 v[114:117], v[138:141], v[196:199], v[114:117]
	v_mfma_f32_16x16x32_f16 v[110:113], v[130:133], v[204:207], v[110:113]
	v_mfma_f32_16x16x32_f16 v[106:109], v[138:141], v[204:207], v[106:109]
	v_mfma_f32_16x16x32_f16 v[102:105], v[130:133], v[212:215], v[102:105]
	v_mfma_f32_16x16x32_f16 v[98:101], v[138:141], v[212:215], v[98:101]
	v_mfma_f32_16x16x32_f16 v[126:129], v[134:137], v[192:195], v[126:129]
	v_mfma_f32_16x16x32_f16 v[122:125], v[142:145], v[192:195], v[122:125]
	v_mfma_f32_16x16x32_f16 v[118:121], v[134:137], v[200:203], v[118:121]
	v_mfma_f32_16x16x32_f16 v[114:117], v[142:145], v[200:203], v[114:117]
	v_mfma_f32_16x16x32_f16 v[110:113], v[134:137], v[208:211], v[110:113]
	v_mfma_f32_16x16x32_f16 v[106:109], v[142:145], v[208:211], v[106:109]
	v_mfma_f32_16x16x32_f16 v[102:105], v[134:137], v[216:219], v[102:105]
	v_mfma_f32_16x16x32_f16 v[98:101], v[142:145], v[216:219], v[98:101]
	s_setprio 0
	s_setprio 1
	v_mfma_f32_16x16x32_f16 v[62:65], v[164:167], v[188:191], v[62:65]
	v_mfma_f32_16x16x32_f16 v[58:61], v[172:175], v[188:191], v[58:61]
	v_mfma_f32_16x16x32_f16 v[54:57], v[164:167], v[196:199], v[54:57]
	v_mfma_f32_16x16x32_f16 v[50:53], v[172:175], v[196:199], v[50:53]
	v_mfma_f32_16x16x32_f16 v[46:49], v[164:167], v[204:207], v[46:49]
	v_mfma_f32_16x16x32_f16 v[42:45], v[172:175], v[204:207], v[42:45]
	v_mfma_f32_16x16x32_f16 v[38:41], v[164:167], v[212:215], v[38:41]
	v_mfma_f32_16x16x32_f16 v[34:37], v[172:175], v[212:215], v[34:37]
	s_setprio 2
	s_barrier
	v_mfma_f32_16x16x32_f16 v[62:65], v[168:171], v[192:195], v[62:65]
	v_mfma_f32_16x16x32_f16 v[58:61], v[180:183], v[192:195], v[58:61]
	v_mfma_f32_16x16x32_f16 v[54:57], v[168:171], v[200:203], v[54:57]
	v_mfma_f32_16x16x32_f16 v[50:53], v[180:183], v[200:203], v[50:53]
	v_mfma_f32_16x16x32_f16 v[46:49], v[168:171], v[208:211], v[46:49]
	v_mfma_f32_16x16x32_f16 v[42:45], v[180:183], v[208:211], v[42:45]
	v_mfma_f32_16x16x32_f16 v[38:41], v[168:171], v[216:219], v[38:41]
	v_mfma_f32_16x16x32_f16 v[34:37], v[180:183], v[216:219], v[34:37]
	s_setprio 0
	s_nop 0
	s_add_i32 s51, s43, s35
	v_lshl_add_u64 v[184:185], s[28:29], 0, v[148:149]
	s_mov_b32 m0, s51
	ds_read_b128 v[188:191], v179 offset:16384
	ds_read_b128 v[192:195], v179 offset:17408
	ds_read_b128 v[196:199], v179 offset:18432
	ds_read_b128 v[200:203], v179 offset:19456
	ds_read_b128 v[204:207], v179 offset:20480
	ds_read_b128 v[208:211], v179 offset:21504
	ds_read_b128 v[212:215], v179 offset:22528
	ds_read_b128 v[216:219], v179 offset:23552
	global_load_lds_dwordx4 v[184:185], off
	s_add_i32 m0, s51, 0x2000
	s_add_u32 s60, s28, 0x40000
	v_lshl_add_u64 v[220:221], s[28:29], 0, v[152:153]
	s_addc_u32 s61, s29, 0
	s_add_i32 s51, s44, s35
	global_load_lds_dwordx4 v[220:221], off
	v_lshl_add_u64 v[222:223], s[60:61], 0, v[148:149]
	s_mov_b32 m0, s51
	v_lshl_add_u64 v[224:225], s[30:31], 0, v[150:151]
	global_load_lds_dwordx4 v[222:223], off
	v_lshl_add_u64 v[222:223], s[60:61], 0, v[152:153]
	s_add_i32 m0, s51, 0x2000
	s_nop 0
	global_load_lds_dwordx4 v[222:223], off
	v_lshl_add_u64 v[222:223], s[30:31], 0, v[146:147]
	s_mov_b32 m0, s25
	s_nop 0
	global_load_lds_dwordx4 v[222:223], off
	s_mov_b32 m0, s36
	s_nop 0
	global_load_lds_dwordx4 v[224:225], off
	s_waitcnt vmcnt(8)
	s_waitcnt lgkmcnt(0)
	s_barrier
	s_setprio 1
	s_waitcnt lgkmcnt(0)
	v_mfma_f32_16x16x32_f16 v[94:97], v[130:133], v[188:191], v[94:97]
	v_mfma_f32_16x16x32_f16 v[90:93], v[138:141], v[188:191], v[90:93]
	v_mfma_f32_16x16x32_f16 v[86:89], v[130:133], v[196:199], v[86:89]
	v_mfma_f32_16x16x32_f16 v[82:85], v[138:141], v[196:199], v[82:85]
	v_mfma_f32_16x16x32_f16 v[78:81], v[130:133], v[204:207], v[78:81]
	v_mfma_f32_16x16x32_f16 v[74:77], v[138:141], v[204:207], v[74:77]
	v_mfma_f32_16x16x32_f16 v[70:73], v[130:133], v[212:215], v[70:73]
	v_mfma_f32_16x16x32_f16 v[66:69], v[138:141], v[212:215], v[66:69]
	v_mfma_f32_16x16x32_f16 v[94:97], v[134:137], v[192:195], v[94:97]
	v_mfma_f32_16x16x32_f16 v[90:93], v[142:145], v[192:195], v[90:93]
	v_mfma_f32_16x16x32_f16 v[86:89], v[134:137], v[200:203], v[86:89]
	v_mfma_f32_16x16x32_f16 v[82:85], v[142:145], v[200:203], v[82:85]
	v_mfma_f32_16x16x32_f16 v[78:81], v[134:137], v[208:211], v[78:81]
	v_mfma_f32_16x16x32_f16 v[74:77], v[142:145], v[208:211], v[74:77]
	v_mfma_f32_16x16x32_f16 v[70:73], v[134:137], v[216:219], v[70:73]
	v_mfma_f32_16x16x32_f16 v[66:69], v[142:145], v[216:219], v[66:69]
	s_setprio 0
	s_setprio 1
	v_mfma_f32_16x16x32_f16 v[30:33], v[164:167], v[188:191], v[30:33]
	v_mfma_f32_16x16x32_f16 v[26:29], v[172:175], v[188:191], v[26:29]
	v_mfma_f32_16x16x32_f16 v[22:25], v[164:167], v[196:199], v[22:25]
	v_mfma_f32_16x16x32_f16 v[18:21], v[172:175], v[196:199], v[18:21]
	v_mfma_f32_16x16x32_f16 v[14:17], v[164:167], v[204:207], v[14:17]
	v_mfma_f32_16x16x32_f16 v[10:13], v[172:175], v[204:207], v[10:13]
	v_mfma_f32_16x16x32_f16 v[6:9], v[164:167], v[212:215], v[6:9]
	v_mfma_f32_16x16x32_f16 v[2:5], v[172:175], v[212:215], v[2:5]
	s_setprio 2
	s_barrier
	v_mfma_f32_16x16x32_f16 v[30:33], v[168:171], v[192:195], v[30:33]
	v_mfma_f32_16x16x32_f16 v[26:29], v[180:183], v[192:195], v[26:29]
	v_mfma_f32_16x16x32_f16 v[22:25], v[168:171], v[200:203], v[22:25]
	v_mfma_f32_16x16x32_f16 v[18:21], v[180:183], v[200:203], v[18:21]
	v_mfma_f32_16x16x32_f16 v[14:17], v[168:171], v[208:211], v[14:17]
	v_mfma_f32_16x16x32_f16 v[10:13], v[180:183], v[208:211], v[10:13]
	v_mfma_f32_16x16x32_f16 v[6:9], v[168:171], v[216:219], v[6:9]
	v_mfma_f32_16x16x32_f16 v[2:5], v[180:183], v[216:219], v[2:5]
	s_setprio 0
	s_nop 0
	s_add_i32 s51, 0, 0x18000
	s_add_i32 s60, 0, 0x1c000
	v_add_u32_e32 v142, s51, v163
	v_add_u32_e32 v180, s60, v163
	ds_read_b128 v[130:133], v142
	ds_read_b128 v[134:137], v142 offset:1024
	ds_read_b128 v[138:141], v142 offset:2048
	ds_read_b128 v[142:145], v142 offset:3072
	ds_read_b128 v[164:167], v180
	ds_read_b128 v[168:171], v180 offset:1024
	ds_read_b128 v[172:175], v180 offset:2048
	ds_read_b128 v[180:183], v180 offset:3072
	s_add_u32 s30, s30, 0x40000
	s_addc_u32 s31, s31, 0
	s_mov_b32 m0, s37
	v_lshl_add_u64 v[226:227], s[30:31], 0, v[146:147]
	ds_read_b128 v[188:191], v179 offset:32768
	ds_read_b128 v[192:195], v179 offset:33792
	ds_read_b128 v[196:199], v179 offset:34816
	ds_read_b128 v[200:203], v179 offset:35840
	ds_read_b128 v[204:207], v179 offset:36864
	ds_read_b128 v[208:211], v179 offset:37888
	ds_read_b128 v[212:215], v179 offset:38912
	ds_read_b128 v[216:219], v179 offset:39936
	global_load_lds_dwordx4 v[226:227], off
	v_lshl_add_u64 v[226:227], s[30:31], 0, v[150:151]
	s_mov_b32 m0, s38
	s_nop 0
	global_load_lds_dwordx4 v[226:227], off
	s_waitcnt vmcnt(8)
	s_waitcnt lgkmcnt(0)
	s_barrier
	s_setprio 1
	s_waitcnt lgkmcnt(0)
	v_mfma_f32_16x16x32_f16 v[126:129], v[130:133], v[188:191], v[126:129]
	v_mfma_f32_16x16x32_f16 v[122:125], v[138:141], v[188:191], v[122:125]
	v_mfma_f32_16x16x32_f16 v[118:121], v[130:133], v[196:199], v[118:121]
	v_mfma_f32_16x16x32_f16 v[114:117], v[138:141], v[196:199], v[114:117]
	v_mfma_f32_16x16x32_f16 v[110:113], v[130:133], v[204:207], v[110:113]
	v_mfma_f32_16x16x32_f16 v[106:109], v[138:141], v[204:207], v[106:109]
	v_mfma_f32_16x16x32_f16 v[102:105], v[130:133], v[212:215], v[102:105]
	v_mfma_f32_16x16x32_f16 v[98:101], v[138:141], v[212:215], v[98:101]
	v_mfma_f32_16x16x32_f16 v[126:129], v[134:137], v[192:195], v[126:129]
	v_mfma_f32_16x16x32_f16 v[122:125], v[142:145], v[192:195], v[122:125]
	v_mfma_f32_16x16x32_f16 v[118:121], v[134:137], v[200:203], v[118:121]
	v_mfma_f32_16x16x32_f16 v[114:117], v[142:145], v[200:203], v[114:117]
	v_mfma_f32_16x16x32_f16 v[110:113], v[134:137], v[208:211], v[110:113]
	v_mfma_f32_16x16x32_f16 v[106:109], v[142:145], v[208:211], v[106:109]
	v_mfma_f32_16x16x32_f16 v[102:105], v[134:137], v[216:219], v[102:105]
	v_mfma_f32_16x16x32_f16 v[98:101], v[142:145], v[216:219], v[98:101]
	s_setprio 0
	s_setprio 1
	v_mfma_f32_16x16x32_f16 v[62:65], v[164:167], v[188:191], v[62:65]
	v_mfma_f32_16x16x32_f16 v[58:61], v[172:175], v[188:191], v[58:61]
	v_mfma_f32_16x16x32_f16 v[54:57], v[164:167], v[196:199], v[54:57]
	v_mfma_f32_16x16x32_f16 v[50:53], v[172:175], v[196:199], v[50:53]
	v_mfma_f32_16x16x32_f16 v[46:49], v[164:167], v[204:207], v[46:49]
	v_mfma_f32_16x16x32_f16 v[42:45], v[172:175], v[204:207], v[42:45]
	v_mfma_f32_16x16x32_f16 v[38:41], v[164:167], v[212:215], v[38:41]
	v_mfma_f32_16x16x32_f16 v[34:37], v[172:175], v[212:215], v[34:37]
	s_setprio 2
	s_barrier
	v_mfma_f32_16x16x32_f16 v[62:65], v[168:171], v[192:195], v[62:65]
	v_mfma_f32_16x16x32_f16 v[58:61], v[180:183], v[192:195], v[58:61]
	v_mfma_f32_16x16x32_f16 v[54:57], v[168:171], v[200:203], v[54:57]
	v_mfma_f32_16x16x32_f16 v[50:53], v[180:183], v[200:203], v[50:53]
	v_mfma_f32_16x16x32_f16 v[46:49], v[168:171], v[208:211], v[46:49]
	v_mfma_f32_16x16x32_f16 v[42:45], v[180:183], v[208:211], v[42:45]
	v_mfma_f32_16x16x32_f16 v[38:41], v[168:171], v[216:219], v[38:41]
	v_mfma_f32_16x16x32_f16 v[34:37], v[180:183], v[216:219], v[34:37]
	s_setprio 0
	s_nop 0
	s_add_i32 s30, s51, s35
	v_lshl_add_u64 v[184:185], v[184:185], 0, s[12:13]
	s_mov_b32 m0, s30
	ds_read_b128 v[188:191], v179 offset:49152
	ds_read_b128 v[192:195], v179 offset:50176
	ds_read_b128 v[196:199], v179 offset:51200
	ds_read_b128 v[200:203], v179 offset:52224
	ds_read_b128 v[204:207], v179 offset:53248
	ds_read_b128 v[208:211], v179 offset:54272
	ds_read_b128 v[212:215], v179 offset:55296
	ds_read_b128 v[216:219], v179 offset:56320
	global_load_lds_dwordx4 v[184:185], off
	s_add_i32 m0, s30, 0x2000
	s_add_u32 s28, s28, 0x40080
	v_lshl_add_u64 v[184:185], v[220:221], 0, s[12:13]
	s_addc_u32 s29, s29, 0
	s_add_i32 s30, s60, s35
	global_load_lds_dwordx4 v[184:185], off
	v_lshl_add_u64 v[184:185], s[28:29], 0, v[148:149]
	s_mov_b32 m0, s30
	s_nop 0
	global_load_lds_dwordx4 v[184:185], off
	v_lshl_add_u64 v[184:185], s[28:29], 0, v[152:153]
	s_add_i32 m0, s30, 0x2000
	s_nop 0
	global_load_lds_dwordx4 v[184:185], off
	v_lshl_add_u64 v[184:185], v[222:223], 0, s[12:13]
	s_mov_b32 m0, s40
	s_nop 0
	global_load_lds_dwordx4 v[184:185], off
	v_lshl_add_u64 v[184:185], v[224:225], 0, s[12:13]
	s_mov_b32 m0, s41
	s_nop 0
	global_load_lds_dwordx4 v[184:185], off
	s_waitcnt vmcnt(8)
	s_waitcnt lgkmcnt(0)
	s_barrier
	s_setprio 1
	s_waitcnt lgkmcnt(0)
	v_mfma_f32_16x16x32_f16 v[94:97], v[130:133], v[188:191], v[94:97]
	v_mfma_f32_16x16x32_f16 v[90:93], v[138:141], v[188:191], v[90:93]
	v_mfma_f32_16x16x32_f16 v[86:89], v[130:133], v[196:199], v[86:89]
	v_mfma_f32_16x16x32_f16 v[82:85], v[138:141], v[196:199], v[82:85]
	v_mfma_f32_16x16x32_f16 v[78:81], v[130:133], v[204:207], v[78:81]
	v_mfma_f32_16x16x32_f16 v[74:77], v[138:141], v[204:207], v[74:77]
	v_mfma_f32_16x16x32_f16 v[70:73], v[130:133], v[212:215], v[70:73]
	v_mfma_f32_16x16x32_f16 v[66:69], v[138:141], v[212:215], v[66:69]
	v_mfma_f32_16x16x32_f16 v[94:97], v[134:137], v[192:195], v[94:97]
	v_mfma_f32_16x16x32_f16 v[90:93], v[142:145], v[192:195], v[90:93]
	v_mfma_f32_16x16x32_f16 v[86:89], v[134:137], v[200:203], v[86:89]
	v_mfma_f32_16x16x32_f16 v[82:85], v[142:145], v[200:203], v[82:85]
	v_mfma_f32_16x16x32_f16 v[78:81], v[134:137], v[208:211], v[78:81]
	v_mfma_f32_16x16x32_f16 v[74:77], v[142:145], v[208:211], v[74:77]
	v_mfma_f32_16x16x32_f16 v[70:73], v[134:137], v[216:219], v[70:73]
	v_mfma_f32_16x16x32_f16 v[66:69], v[142:145], v[216:219], v[66:69]
	s_setprio 0
	s_setprio 1
	v_mfma_f32_16x16x32_f16 v[30:33], v[164:167], v[188:191], v[30:33]
	v_mfma_f32_16x16x32_f16 v[26:29], v[172:175], v[188:191], v[26:29]
	v_mfma_f32_16x16x32_f16 v[22:25], v[164:167], v[196:199], v[22:25]
	v_mfma_f32_16x16x32_f16 v[18:21], v[172:175], v[196:199], v[18:21]
	v_mfma_f32_16x16x32_f16 v[14:17], v[164:167], v[204:207], v[14:17]
	v_mfma_f32_16x16x32_f16 v[10:13], v[172:175], v[204:207], v[10:13]
	v_mfma_f32_16x16x32_f16 v[6:9], v[164:167], v[212:215], v[6:9]
	v_mfma_f32_16x16x32_f16 v[2:5], v[172:175], v[212:215], v[2:5]
	s_setprio 2
	s_barrier
	v_mfma_f32_16x16x32_f16 v[30:33], v[168:171], v[192:195], v[30:33]
	v_mfma_f32_16x16x32_f16 v[26:29], v[180:183], v[192:195], v[26:29]
	v_mfma_f32_16x16x32_f16 v[22:25], v[168:171], v[200:203], v[22:25]
	v_mfma_f32_16x16x32_f16 v[18:21], v[180:183], v[200:203], v[18:21]
	v_mfma_f32_16x16x32_f16 v[14:17], v[168:171], v[208:211], v[14:17]
	v_mfma_f32_16x16x32_f16 v[10:13], v[180:183], v[208:211], v[10:13]
	v_mfma_f32_16x16x32_f16 v[6:9], v[168:171], v[216:219], v[6:9]
	v_mfma_f32_16x16x32_f16 v[2:5], v[180:183], v[216:219], v[2:5]
	s_setprio 0
	s_nop 0
	s_add_i32 s50, s50, 2
	s_add_u32 s26, s26, 0x100
	s_addc_u32 s27, s27, 0
	s_add_u32 s48, s48, 0x100
	s_addc_u32 s49, s49, 0
	s_cmp_gt_u32 s50, 13
	s_cbranch_scc0 .LBB0_1734
	s_and_b64 vcc, exec, s[14:15]
	s_cbranch_vccz .LBB0_1737
	s_barrier

.LBB0_1813:
	ds_read_b128 v[146:149], v154
	ds_read_b128 v[158:161], v154 offset:1024
	ds_read_b128 v[164:167], v154 offset:2048
	ds_read_b128 v[168:171], v154 offset:3072
	ds_read_b128 v[172:175], v155
	ds_read_b128 v[176:179], v155 offset:1024
	ds_read_b128 v[180:183], v155 offset:2048
	ds_read_b128 v[188:191], v155 offset:3072
	s_add_u32 s36, s34, 0xfff80080
	s_addc_u32 s37, s35, -1
	s_cmp_eq_u32 s65, 28
	s_cselect_b32 s39, s25, s37
	s_cselect_b32 s38, s61, s36
	s_cselect_b32 s37, s23, s64
	s_cselect_b32 s36, s62, s63
	v_lshl_add_u64 v[150:151], s[34:35], 0, v[138:139]
	s_add_i32 m0, s31, 0xc000
	ds_read_b128 v[192:195], v156
	ds_read_b128 v[196:199], v156 offset:1024
	ds_read_b128 v[200:203], v156 offset:2048
	ds_read_b128 v[204:207], v156 offset:3072
	ds_read_b128 v[208:211], v156 offset:4096
	ds_read_b128 v[212:215], v156 offset:5120
	ds_read_b128 v[216:219], v156 offset:6144
	ds_read_b128 v[220:223], v156 offset:7168
	global_load_lds_dwordx4 v[150:151], off
	v_lshl_add_u64 v[150:151], s[34:35], 0, v[140:141]
	s_add_i32 m0, s31, 0xe000
	s_nop 0
	global_load_lds_dwordx4 v[150:151], off
	s_waitcnt vmcnt(8)
	s_waitcnt lgkmcnt(0)
	s_barrier
	s_setprio 1
	s_waitcnt lgkmcnt(0)
	v_mfma_f32_16x16x32_f16 v[126:129], v[146:149], v[192:195], v[126:129]
	v_mfma_f32_16x16x32_f16 v[122:125], v[164:167], v[192:195], v[122:125]
	v_mfma_f32_16x16x32_f16 v[110:113], v[146:149], v[200:203], v[110:113]
	v_mfma_f32_16x16x32_f16 v[106:109], v[164:167], v[200:203], v[106:109]
	v_mfma_f32_16x16x32_f16 v[94:97], v[146:149], v[208:211], v[94:97]
	v_mfma_f32_16x16x32_f16 v[90:93], v[164:167], v[208:211], v[90:93]
	v_mfma_f32_16x16x32_f16 v[78:81], v[146:149], v[216:219], v[78:81]
	v_mfma_f32_16x16x32_f16 v[74:77], v[164:167], v[216:219], v[74:77]
	v_mfma_f32_16x16x32_f16 v[126:129], v[158:161], v[196:199], v[126:129]
	v_mfma_f32_16x16x32_f16 v[122:125], v[168:171], v[196:199], v[122:125]
	v_mfma_f32_16x16x32_f16 v[110:113], v[158:161], v[204:207], v[110:113]
	v_mfma_f32_16x16x32_f16 v[106:109], v[168:171], v[204:207], v[106:109]
	v_mfma_f32_16x16x32_f16 v[94:97], v[158:161], v[212:215], v[94:97]
	v_mfma_f32_16x16x32_f16 v[90:93], v[168:171], v[212:215], v[90:93]
	v_mfma_f32_16x16x32_f16 v[78:81], v[158:161], v[220:223], v[78:81]
	v_mfma_f32_16x16x32_f16 v[74:77], v[168:171], v[220:223], v[74:77]
	s_setprio 0
	s_setprio 1
	v_mfma_f32_16x16x32_f16 v[118:121], v[172:175], v[192:195], v[118:121]
	v_mfma_f32_16x16x32_f16 v[114:117], v[180:183], v[192:195], v[114:117]
	v_mfma_f32_16x16x32_f16 v[102:105], v[172:175], v[200:203], v[102:105]
	v_mfma_f32_16x16x32_f16 v[98:101], v[180:183], v[200:203], v[98:101]
	v_mfma_f32_16x16x32_f16 v[86:89], v[172:175], v[208:211], v[86:89]
	v_mfma_f32_16x16x32_f16 v[82:85], v[180:183], v[208:211], v[82:85]
	v_mfma_f32_16x16x32_f16 v[70:73], v[172:175], v[216:219], v[70:73]
	v_mfma_f32_16x16x32_f16 v[66:69], v[180:183], v[216:219], v[66:69]
	s_setprio 2
	s_barrier
	v_mfma_f32_16x16x32_f16 v[118:121], v[176:179], v[196:199], v[118:121]
	v_mfma_f32_16x16x32_f16 v[114:117], v[188:191], v[196:199], v[114:117]
	v_mfma_f32_16x16x32_f16 v[102:105], v[176:179], v[204:207], v[102:105]
	v_mfma_f32_16x16x32_f16 v[98:101], v[188:191], v[204:207], v[98:101]
	v_mfma_f32_16x16x32_f16 v[86:89], v[176:179], v[212:215], v[86:89]
	v_mfma_f32_16x16x32_f16 v[82:85], v[188:191], v[212:215], v[82:85]
	v_mfma_f32_16x16x32_f16 v[70:73], v[176:179], v[220:223], v[70:73]
	v_mfma_f32_16x16x32_f16 v[66:69], v[188:191], v[220:223], v[66:69]
	s_setprio 0
	s_nop 0
	s_add_i32 s66, s50, s42
	v_lshl_add_u64 v[150:151], s[36:37], 0, v[132:133]
	s_mov_b32 m0, s66
	ds_read_b128 v[192:195], v156 offset:16384
	ds_read_b128 v[196:199], v156 offset:17408
	ds_read_b128 v[200:203], v156 offset:18432
	ds_read_b128 v[204:207], v156 offset:19456
	ds_read_b128 v[208:211], v156 offset:20480
	ds_read_b128 v[212:215], v156 offset:21504
	ds_read_b128 v[216:219], v156 offset:22528
	ds_read_b128 v[220:223], v156 offset:23552
	global_load_lds_dwordx4 v[150:151], off
	s_add_i32 m0, s66, 0x2000
	s_add_u32 s66, s36, 0x80000
	v_lshl_add_u64 v[184:185], s[36:37], 0, v[136:137]
	s_addc_u32 s67, s37, 0
	s_add_i32 s68, s51, s42
	global_load_lds_dwordx4 v[184:185], off
	v_lshl_add_u64 v[224:225], s[66:67], 0, v[132:133]
	s_mov_b32 m0, s68
	v_lshl_add_u64 v[226:227], s[38:39], 0, v[134:135]
	global_load_lds_dwordx4 v[224:225], off
	v_lshl_add_u64 v[224:225], s[66:67], 0, v[136:137]
	s_add_i32 m0, s68, 0x2000
	s_nop 0
	global_load_lds_dwordx4 v[224:225], off
	v_lshl_add_u64 v[224:225], s[38:39], 0, v[130:131]
	s_mov_b32 m0, s31
	s_nop 0
	global_load_lds_dwordx4 v[224:225], off
	s_mov_b32 m0, s43
	s_nop 0
	global_load_lds_dwordx4 v[226:227], off
	s_waitcnt vmcnt(8)
	s_waitcnt lgkmcnt(0)
	s_barrier
	s_setprio 1
	s_waitcnt lgkmcnt(0)
	v_mfma_f32_16x16x32_f16 v[62:65], v[146:149], v[192:195], v[62:65]
	v_mfma_f32_16x16x32_f16 v[58:61], v[164:167], v[192:195], v[58:61]
	v_mfma_f32_16x16x32_f16 v[46:49], v[146:149], v[200:203], v[46:49]
	v_mfma_f32_16x16x32_f16 v[42:45], v[164:167], v[200:203], v[42:45]
	v_mfma_f32_16x16x32_f16 v[30:33], v[146:149], v[208:211], v[30:33]
	v_mfma_f32_16x16x32_f16 v[26:29], v[164:167], v[208:211], v[26:29]
	v_mfma_f32_16x16x32_f16 v[14:17], v[146:149], v[216:219], v[14:17]
	v_mfma_f32_16x16x32_f16 v[10:13], v[164:167], v[216:219], v[10:13]
	v_mfma_f32_16x16x32_f16 v[62:65], v[158:161], v[196:199], v[62:65]
	v_mfma_f32_16x16x32_f16 v[58:61], v[168:171], v[196:199], v[58:61]
	v_mfma_f32_16x16x32_f16 v[46:49], v[158:161], v[204:207], v[46:49]
	v_mfma_f32_16x16x32_f16 v[42:45], v[168:171], v[204:207], v[42:45]
	v_mfma_f32_16x16x32_f16 v[30:33], v[158:161], v[212:215], v[30:33]
	v_mfma_f32_16x16x32_f16 v[26:29], v[168:171], v[212:215], v[26:29]
	v_mfma_f32_16x16x32_f16 v[14:17], v[158:161], v[220:223], v[14:17]
	v_mfma_f32_16x16x32_f16 v[10:13], v[168:171], v[220:223], v[10:13]
	s_setprio 0
	s_setprio 1
	v_mfma_f32_16x16x32_f16 v[54:57], v[172:175], v[192:195], v[54:57]
	v_mfma_f32_16x16x32_f16 v[50:53], v[180:183], v[192:195], v[50:53]
	v_mfma_f32_16x16x32_f16 v[38:41], v[172:175], v[200:203], v[38:41]
	v_mfma_f32_16x16x32_f16 v[34:37], v[180:183], v[200:203], v[34:37]
	v_mfma_f32_16x16x32_f16 v[22:25], v[172:175], v[208:211], v[22:25]
	v_mfma_f32_16x16x32_f16 v[18:21], v[180:183], v[208:211], v[18:21]
	v_mfma_f32_16x16x32_f16 v[6:9], v[172:175], v[216:219], v[6:9]
	v_mfma_f32_16x16x32_f16 v[2:5], v[180:183], v[216:219], v[2:5]
	s_setprio 2
	s_barrier
	v_mfma_f32_16x16x32_f16 v[54:57], v[176:179], v[196:199], v[54:57]
	v_mfma_f32_16x16x32_f16 v[50:53], v[188:191], v[196:199], v[50:53]
	v_mfma_f32_16x16x32_f16 v[38:41], v[176:179], v[204:207], v[38:41]
	v_mfma_f32_16x16x32_f16 v[34:37], v[188:191], v[204:207], v[34:37]
	v_mfma_f32_16x16x32_f16 v[22:25], v[176:179], v[212:215], v[22:25]
	v_mfma_f32_16x16x32_f16 v[18:21], v[188:191], v[212:215], v[18:21]
	v_mfma_f32_16x16x32_f16 v[6:9], v[176:179], v[220:223], v[6:9]
	v_mfma_f32_16x16x32_f16 v[2:5], v[188:191], v[220:223], v[2:5]
	s_setprio 0
	s_nop 0
	s_add_i32 s66, 0, 0x18000
	v_add_u32_e32 v157, s66, v152
	s_add_i32 s67, 0, 0x1c000
	ds_read_b128 v[146:149], v157
	ds_read_b128 v[158:161], v157 offset:1024
	ds_read_b128 v[164:167], v157 offset:2048
	ds_read_b128 v[168:171], v157 offset:3072
	v_add_u32_e32 v157, s67, v152
	ds_read_b128 v[172:175], v157
	ds_read_b128 v[176:179], v157 offset:1024
	ds_read_b128 v[180:183], v157 offset:2048
	ds_read_b128 v[188:191], v157 offset:3072
	s_add_u32 s38, s38, 0x80000
	s_addc_u32 s39, s39, 0
	s_mov_b32 m0, s44
	v_lshl_add_u64 v[228:229], s[38:39], 0, v[130:131]
	ds_read_b128 v[192:195], v156 offset:32768
	ds_read_b128 v[196:199], v156 offset:33792
	ds_read_b128 v[200:203], v156 offset:34816
	ds_read_b128 v[204:207], v156 offset:35840
	ds_read_b128 v[208:211], v156 offset:36864
	ds_read_b128 v[212:215], v156 offset:37888
	ds_read_b128 v[216:219], v156 offset:38912
	ds_read_b128 v[220:223], v156 offset:39936
	global_load_lds_dwordx4 v[228:229], off
	v_lshl_add_u64 v[228:229], s[38:39], 0, v[134:135]
	s_mov_b32 m0, s45
	s_nop 0
	global_load_lds_dwordx4 v[228:229], off
	s_waitcnt vmcnt(8)
	s_waitcnt lgkmcnt(0)
	s_barrier
	s_setprio 1
	s_waitcnt lgkmcnt(0)
	v_mfma_f32_16x16x32_f16 v[126:129], v[146:149], v[192:195], v[126:129]
	v_mfma_f32_16x16x32_f16 v[122:125], v[164:167], v[192:195], v[122:125]
	v_mfma_f32_16x16x32_f16 v[110:113], v[146:149], v[200:203], v[110:113]
	v_mfma_f32_16x16x32_f16 v[106:109], v[164:167], v[200:203], v[106:109]
	v_mfma_f32_16x16x32_f16 v[94:97], v[146:149], v[208:211], v[94:97]
	v_mfma_f32_16x16x32_f16 v[90:93], v[164:167], v[208:211], v[90:93]
	v_mfma_f32_16x16x32_f16 v[78:81], v[146:149], v[216:219], v[78:81]
	v_mfma_f32_16x16x32_f16 v[74:77], v[164:167], v[216:219], v[74:77]
	v_mfma_f32_16x16x32_f16 v[126:129], v[158:161], v[196:199], v[126:129]
	v_mfma_f32_16x16x32_f16 v[122:125], v[168:171], v[196:199], v[122:125]
	v_mfma_f32_16x16x32_f16 v[110:113], v[158:161], v[204:207], v[110:113]
	v_mfma_f32_16x16x32_f16 v[106:109], v[168:171], v[204:207], v[106:109]
	v_mfma_f32_16x16x32_f16 v[94:97], v[158:161], v[212:215], v[94:97]
	v_mfma_f32_16x16x32_f16 v[90:93], v[168:171], v[212:215], v[90:93]
	v_mfma_f32_16x16x32_f16 v[78:81], v[158:161], v[220:223], v[78:81]
	v_mfma_f32_16x16x32_f16 v[74:77], v[168:171], v[220:223], v[74:77]
	s_setprio 0
	s_setprio 1
	v_mfma_f32_16x16x32_f16 v[118:121], v[172:175], v[192:195], v[118:121]
	v_mfma_f32_16x16x32_f16 v[114:117], v[180:183], v[192:195], v[114:117]
	v_mfma_f32_16x16x32_f16 v[102:105], v[172:175], v[200:203], v[102:105]
	v_mfma_f32_16x16x32_f16 v[98:101], v[180:183], v[200:203], v[98:101]
	v_mfma_f32_16x16x32_f16 v[86:89], v[172:175], v[208:211], v[86:89]
	v_mfma_f32_16x16x32_f16 v[82:85], v[180:183], v[208:211], v[82:85]
	v_mfma_f32_16x16x32_f16 v[70:73], v[172:175], v[216:219], v[70:73]
	v_mfma_f32_16x16x32_f16 v[66:69], v[180:183], v[216:219], v[66:69]
	s_setprio 2
	s_barrier
	v_mfma_f32_16x16x32_f16 v[118:121], v[176:179], v[196:199], v[118:121]
	v_mfma_f32_16x16x32_f16 v[114:117], v[188:191], v[196:199], v[114:117]
	v_mfma_f32_16x16x32_f16 v[102:105], v[176:179], v[204:207], v[102:105]
	v_mfma_f32_16x16x32_f16 v[98:101], v[188:191], v[204:207], v[98:101]
	v_mfma_f32_16x16x32_f16 v[86:89], v[176:179], v[212:215], v[86:89]
	v_mfma_f32_16x16x32_f16 v[82:85], v[188:191], v[212:215], v[82:85]
	v_mfma_f32_16x16x32_f16 v[70:73], v[176:179], v[220:223], v[70:73]
	v_mfma_f32_16x16x32_f16 v[66:69], v[188:191], v[220:223], v[66:69]
	s_setprio 0
	s_nop 0
	s_add_i32 s38, s66, s42
	v_lshl_add_u64 v[150:151], v[150:151], 0, s[10:11]
	s_mov_b32 m0, s38
	ds_read_b128 v[192:195], v156 offset:49152
	ds_read_b128 v[196:199], v156 offset:50176
	ds_read_b128 v[200:203], v156 offset:51200
	ds_read_b128 v[204:207], v156 offset:52224
	ds_read_b128 v[208:211], v156 offset:53248
	ds_read_b128 v[212:215], v156 offset:54272
	ds_read_b128 v[216:219], v156 offset:55296
	ds_read_b128 v[220:223], v156 offset:56320
	global_load_lds_dwordx4 v[150:151], off
	s_add_i32 m0, s38, 0x2000
	s_add_u32 s36, s36, 0x80080
	v_lshl_add_u64 v[150:151], v[184:185], 0, s[10:11]
	s_addc_u32 s37, s37, 0
	s_add_i32 s38, s67, s42
	global_load_lds_dwordx4 v[150:151], off
	v_lshl_add_u64 v[150:151], s[36:37], 0, v[132:133]
	s_mov_b32 m0, s38
	s_nop 0
	global_load_lds_dwordx4 v[150:151], off
	v_lshl_add_u64 v[150:151], s[36:37], 0, v[136:137]
	s_add_i32 m0, s38, 0x2000
	s_nop 0
	global_load_lds_dwordx4 v[150:151], off
	v_lshl_add_u64 v[150:151], v[224:225], 0, s[10:11]
	s_mov_b32 m0, s47
	s_nop 0
	global_load_lds_dwordx4 v[150:151], off
	v_lshl_add_u64 v[150:151], v[226:227], 0, s[10:11]
	s_mov_b32 m0, s48
	s_nop 0
	global_load_lds_dwordx4 v[150:151], off
	s_waitcnt vmcnt(8)
	s_waitcnt lgkmcnt(0)
	s_barrier
	s_setprio 1
	s_waitcnt lgkmcnt(0)
	v_mfma_f32_16x16x32_f16 v[62:65], v[146:149], v[192:195], v[62:65]
	v_mfma_f32_16x16x32_f16 v[58:61], v[164:167], v[192:195], v[58:61]
	v_mfma_f32_16x16x32_f16 v[46:49], v[146:149], v[200:203], v[46:49]
	v_mfma_f32_16x16x32_f16 v[42:45], v[164:167], v[200:203], v[42:45]
	v_mfma_f32_16x16x32_f16 v[30:33], v[146:149], v[208:211], v[30:33]
	v_mfma_f32_16x16x32_f16 v[26:29], v[164:167], v[208:211], v[26:29]
	v_mfma_f32_16x16x32_f16 v[14:17], v[146:149], v[216:219], v[14:17]
	v_mfma_f32_16x16x32_f16 v[10:13], v[164:167], v[216:219], v[10:13]
	v_mfma_f32_16x16x32_f16 v[62:65], v[158:161], v[196:199], v[62:65]
	v_mfma_f32_16x16x32_f16 v[58:61], v[168:171], v[196:199], v[58:61]
	v_mfma_f32_16x16x32_f16 v[46:49], v[158:161], v[204:207], v[46:49]
	v_mfma_f32_16x16x32_f16 v[42:45], v[168:171], v[204:207], v[42:45]
	v_mfma_f32_16x16x32_f16 v[30:33], v[158:161], v[212:215], v[30:33]
	v_mfma_f32_16x16x32_f16 v[26:29], v[168:171], v[212:215], v[26:29]
	v_mfma_f32_16x16x32_f16 v[14:17], v[158:161], v[220:223], v[14:17]
	v_mfma_f32_16x16x32_f16 v[10:13], v[168:171], v[220:223], v[10:13]
	s_setprio 0
	s_setprio 1
	v_mfma_f32_16x16x32_f16 v[54:57], v[172:175], v[192:195], v[54:57]
	v_mfma_f32_16x16x32_f16 v[50:53], v[180:183], v[192:195], v[50:53]
	v_mfma_f32_16x16x32_f16 v[38:41], v[172:175], v[200:203], v[38:41]
	v_mfma_f32_16x16x32_f16 v[34:37], v[180:183], v[200:203], v[34:37]
	v_mfma_f32_16x16x32_f16 v[22:25], v[172:175], v[208:211], v[22:25]
	v_mfma_f32_16x16x32_f16 v[18:21], v[180:183], v[208:211], v[18:21]
	v_mfma_f32_16x16x32_f16 v[6:9], v[172:175], v[216:219], v[6:9]
	v_mfma_f32_16x16x32_f16 v[2:5], v[180:183], v[216:219], v[2:5]
	s_setprio 2
	s_barrier
	v_mfma_f32_16x16x32_f16 v[54:57], v[176:179], v[196:199], v[54:57]
	v_mfma_f32_16x16x32_f16 v[50:53], v[188:191], v[196:199], v[50:53]
	v_mfma_f32_16x16x32_f16 v[38:41], v[176:179], v[204:207], v[38:41]
	v_mfma_f32_16x16x32_f16 v[34:37], v[188:191], v[204:207], v[34:37]
	v_mfma_f32_16x16x32_f16 v[22:25], v[176:179], v[212:215], v[22:25]
	v_mfma_f32_16x16x32_f16 v[18:21], v[188:191], v[212:215], v[18:21]
	v_mfma_f32_16x16x32_f16 v[6:9], v[176:179], v[220:223], v[6:9]
	v_mfma_f32_16x16x32_f16 v[2:5], v[188:191], v[220:223], v[2:5]
	s_setprio 0
	s_nop 0
	s_add_i32 s65, s65, 2
	s_add_u32 s34, s34, 0x100
	s_addc_u32 s35, s35, 0
	s_add_u32 s63, s63, 0x100
	s_addc_u32 s64, s64, 0
	s_cmp_gt_u32 s65, 29
	s_cbranch_scc0 .LBB0_1813
	s_and_b64 vcc, exec, s[12:13]
	s_cbranch_vccz .LBB0_1816
	s_barrier

.LBB0_1957:
	ds_read_b128 v[26:29], v194
	ds_read_b128 v[30:33], v194 offset:1024
	ds_read_b128 v[18:21], v194 offset:2048
	ds_read_b128 v[22:25], v194 offset:3072
	ds_read_b128 v[10:13], v195
	ds_read_b128 v[14:17], v195 offset:1024
	ds_read_b128 v[2:5], v195 offset:2048
	ds_read_b128 v[6:9], v195 offset:3072
	s_add_u32 s24, s58, s22
	s_addc_u32 s25, s59, s23
	s_add_u32 s26, s24, 0x50a00100
	s_addc_u32 s27, s25, 0
	s_add_u32 s72, s69, s22
	s_addc_u32 s73, s70, s23
	s_cmpk_eq_i32 s22, 0x700
	s_cselect_b64 vcc, -1, 0
	s_and_b64 s[24:25], vcc, exec
	v_cndmask_b32_e32 v168, v202, v198, vcc
	v_cndmask_b32_e32 v186, v172, v199, vcc
	v_cndmask_b32_e32 v175, v174, v200, vcc
	v_cndmask_b32_e32 v177, v176, v201, vcc
	s_cselect_b32 s27, s1, s27
	s_cselect_b32 s26, s0, s26
	s_cselect_b32 s25, s19, s73
	s_cselect_b32 s24, s68, s72
	v_lshl_add_u64 v[182:183], v[180:181], 0, s[22:23]
	s_add_i32 m0, s36, 0xc000
	ds_read_b128 v[204:207], v196
	ds_read_b128 v[208:211], v196 offset:1024
	ds_read_b128 v[212:215], v196 offset:2048
	ds_read_b128 v[216:219], v196 offset:3072
	ds_read_b128 v[220:223], v196 offset:4096
	ds_read_b128 v[224:227], v196 offset:5120
	ds_read_b128 v[228:231], v196 offset:6144
	ds_read_b128 v[232:235], v196 offset:7168
	global_load_lds_dwordx4 v[182:183], off
	v_lshl_add_u64 v[182:183], v[178:179], 0, s[22:23]
	s_add_i32 m0, s36, 0xe000
	s_nop 0
	global_load_lds_dwordx4 v[182:183], off
	s_waitcnt vmcnt(8)
	s_waitcnt lgkmcnt(0)
	s_barrier
	s_setprio 1
	s_waitcnt lgkmcnt(0)
	v_mfma_scale_f32_16x16x128_f8f6f4 v[158:161], v[26:33], v[204:211], v[158:161], v1, v1 op_sel_hi:[0,0,0]
	v_mfma_scale_f32_16x16x128_f8f6f4 v[150:153], v[18:25], v[204:211], v[150:153], v1, v1 op_sel_hi:[0,0,0]
	v_mfma_scale_f32_16x16x128_f8f6f4 v[142:145], v[26:33], v[212:219], v[142:145], v1, v1 op_sel_hi:[0,0,0]
	v_mfma_scale_f32_16x16x128_f8f6f4 v[134:137], v[18:25], v[212:219], v[134:137], v1, v1 op_sel_hi:[0,0,0]
	v_mfma_scale_f32_16x16x128_f8f6f4 v[126:129], v[26:33], v[220:227], v[126:129], v1, v1 op_sel_hi:[0,0,0]
	v_mfma_scale_f32_16x16x128_f8f6f4 v[118:121], v[18:25], v[220:227], v[118:121], v1, v1 op_sel_hi:[0,0,0]
	v_mfma_scale_f32_16x16x128_f8f6f4 v[110:113], v[26:33], v[228:235], v[110:113], v1, v1 op_sel_hi:[0,0,0]
	v_mfma_scale_f32_16x16x128_f8f6f4 v[102:105], v[18:25], v[228:235], v[102:105], v1, v1 op_sel_hi:[0,0,0]
	s_setprio 0
	s_setprio 1
	v_mfma_scale_f32_16x16x128_f8f6f4 v[154:157], v[10:17], v[204:211], v[154:157], v1, v1 op_sel_hi:[0,0,0]
	v_mfma_scale_f32_16x16x128_f8f6f4 v[146:149], v[2:9], v[204:211], v[146:149], v1, v1 op_sel_hi:[0,0,0]
	v_mfma_scale_f32_16x16x128_f8f6f4 v[138:141], v[10:17], v[212:219], v[138:141], v1, v1 op_sel_hi:[0,0,0]
	v_mfma_scale_f32_16x16x128_f8f6f4 v[130:133], v[2:9], v[212:219], v[130:133], v1, v1 op_sel_hi:[0,0,0]
	s_setprio 2
	s_barrier
	v_mfma_scale_f32_16x16x128_f8f6f4 v[122:125], v[10:17], v[220:227], v[122:125], v1, v1 op_sel_hi:[0,0,0]
	v_mfma_scale_f32_16x16x128_f8f6f4 v[114:117], v[2:9], v[220:227], v[114:117], v1, v1 op_sel_hi:[0,0,0]
	v_mfma_scale_f32_16x16x128_f8f6f4 v[106:109], v[10:17], v[228:235], v[106:109], v1, v1 op_sel_hi:[0,0,0]
	v_mfma_scale_f32_16x16x128_f8f6f4 v[98:101], v[2:9], v[228:235], v[98:101], v1, v1 op_sel_hi:[0,0,0]
	s_setprio 0
	s_nop 0
	s_add_i32 s72, s44, s28
	v_lshl_add_u64 v[182:183], s[24:25], 0, v[166:167]
	s_mov_b32 m0, s72
	ds_read_b128 v[204:207], v196 offset:16384
	ds_read_b128 v[208:211], v196 offset:17408
	ds_read_b128 v[212:215], v196 offset:18432
	ds_read_b128 v[216:219], v196 offset:19456
	ds_read_b128 v[220:223], v196 offset:20480
	ds_read_b128 v[224:227], v196 offset:21504
	ds_read_b128 v[228:231], v196 offset:22528
	ds_read_b128 v[232:235], v196 offset:23552
	global_load_lds_dwordx4 v[182:183], off
	s_add_i32 m0, s72, 0x2000
	s_add_u32 s72, s24, 0x40000
	v_lshl_add_u64 v[184:185], s[24:25], 0, v[164:165]
	s_addc_u32 s73, s25, 0
	s_add_i32 s74, s45, s28
	global_load_lds_dwordx4 v[184:185], off
	v_lshl_add_u64 v[188:189], s[72:73], 0, v[166:167]
	s_mov_b32 m0, s74
	v_mov_b32_e32 v187, v169
	global_load_lds_dwordx4 v[188:189], off
	v_lshl_add_u64 v[188:189], s[72:73], 0, v[164:165]
	s_add_i32 m0, s74, 0x2000
	s_nop 0
	global_load_lds_dwordx4 v[188:189], off
	s_mov_b32 m0, s36
	v_lshl_add_u64 v[188:189], s[26:27], 0, v[168:169]
	global_load_lds_dwordx4 v168, s[26:27]
	s_mov_b32 m0, s37
	s_nop 0
	global_load_lds_dwordx4 v186, s[26:27]
	s_waitcnt vmcnt(8)
	s_waitcnt lgkmcnt(0)
	v_lshl_add_u64 v[186:187], s[26:27], 0, v[186:187]
	s_barrier
	s_setprio 1
	s_waitcnt lgkmcnt(0)
	v_mfma_scale_f32_16x16x128_f8f6f4 v[94:97], v[26:33], v[204:211], v[94:97], v1, v1 op_sel_hi:[0,0,0]
	v_mfma_scale_f32_16x16x128_f8f6f4 v[86:89], v[18:25], v[204:211], v[86:89], v1, v1 op_sel_hi:[0,0,0]
	v_mfma_scale_f32_16x16x128_f8f6f4 v[78:81], v[26:33], v[212:219], v[78:81], v1, v1 op_sel_hi:[0,0,0]
	v_mfma_scale_f32_16x16x128_f8f6f4 v[70:73], v[18:25], v[212:219], v[70:73], v1, v1 op_sel_hi:[0,0,0]
	v_mfma_scale_f32_16x16x128_f8f6f4 v[62:65], v[26:33], v[220:227], v[62:65], v1, v1 op_sel_hi:[0,0,0]
	v_mfma_scale_f32_16x16x128_f8f6f4 v[54:57], v[18:25], v[220:227], v[54:57], v1, v1 op_sel_hi:[0,0,0]
	v_mfma_scale_f32_16x16x128_f8f6f4 v[46:49], v[26:33], v[228:235], v[46:49], v1, v1 op_sel_hi:[0,0,0]
	v_mfma_scale_f32_16x16x128_f8f6f4 v[38:41], v[18:25], v[228:235], v[38:41], v1, v1 op_sel_hi:[0,0,0]
	s_setprio 0
	s_setprio 1
	v_mfma_scale_f32_16x16x128_f8f6f4 v[90:93], v[10:17], v[204:211], v[90:93], v1, v1 op_sel_hi:[0,0,0]
	v_mfma_scale_f32_16x16x128_f8f6f4 v[82:85], v[2:9], v[204:211], v[82:85], v1, v1 op_sel_hi:[0,0,0]
	v_mfma_scale_f32_16x16x128_f8f6f4 v[74:77], v[10:17], v[212:219], v[74:77], v1, v1 op_sel_hi:[0,0,0]
	v_mfma_scale_f32_16x16x128_f8f6f4 v[66:69], v[2:9], v[212:219], v[66:69], v1, v1 op_sel_hi:[0,0,0]
	s_setprio 2
	s_barrier
	v_mfma_scale_f32_16x16x128_f8f6f4 v[58:61], v[10:17], v[220:227], v[58:61], v1, v1 op_sel_hi:[0,0,0]
	v_mfma_scale_f32_16x16x128_f8f6f4 v[50:53], v[2:9], v[220:227], v[50:53], v1, v1 op_sel_hi:[0,0,0]
	v_mfma_scale_f32_16x16x128_f8f6f4 v[42:45], v[10:17], v[228:235], v[42:45], v1, v1 op_sel_hi:[0,0,0]
	v_mfma_scale_f32_16x16x128_f8f6f4 v[34:37], v[2:9], v[228:235], v[34:37], v1, v1 op_sel_hi:[0,0,0]
	s_setprio 0
	s_nop 0
	s_add_i32 s72, 0, 0x18000
	s_add_i32 s73, 0, 0x1c000
	v_add_u32_e32 v14, s72, v192
	v_add_u32_e32 v30, s73, v192
	ds_read_b128 v[2:5], v14
	ds_read_b128 v[6:9], v14 offset:1024
	ds_read_b128 v[10:13], v14 offset:2048
	ds_read_b128 v[14:17], v14 offset:3072
	ds_read_b128 v[18:21], v30
	ds_read_b128 v[22:25], v30 offset:1024
	ds_read_b128 v[26:29], v30 offset:2048
	ds_read_b128 v[30:33], v30 offset:3072
	s_mov_b32 m0, s38
	ds_read_b128 v[204:207], v196 offset:32768
	ds_read_b128 v[208:211], v196 offset:33792
	ds_read_b128 v[212:215], v196 offset:34816
	ds_read_b128 v[216:219], v196 offset:35840
	ds_read_b128 v[220:223], v196 offset:36864
	ds_read_b128 v[224:227], v196 offset:37888
	ds_read_b128 v[228:231], v196 offset:38912
	ds_read_b128 v[232:235], v196 offset:39936
	global_load_lds_dwordx4 v175, s[26:27]
	s_mov_b32 m0, s39
	s_nop 0
	global_load_lds_dwordx4 v177, s[26:27]
	s_waitcnt vmcnt(8)
	s_waitcnt lgkmcnt(0)
	s_barrier
	s_setprio 1
	s_waitcnt lgkmcnt(0)
	v_mfma_scale_f32_16x16x128_f8f6f4 v[158:161], v[2:9], v[204:211], v[158:161], v1, v1 op_sel_hi:[0,0,0]
	v_mfma_scale_f32_16x16x128_f8f6f4 v[150:153], v[10:17], v[204:211], v[150:153], v1, v1 op_sel_hi:[0,0,0]
	v_mfma_scale_f32_16x16x128_f8f6f4 v[142:145], v[2:9], v[212:219], v[142:145], v1, v1 op_sel_hi:[0,0,0]
	v_mfma_scale_f32_16x16x128_f8f6f4 v[134:137], v[10:17], v[212:219], v[134:137], v1, v1 op_sel_hi:[0,0,0]
	v_mfma_scale_f32_16x16x128_f8f6f4 v[126:129], v[2:9], v[220:227], v[126:129], v1, v1 op_sel_hi:[0,0,0]
	v_mfma_scale_f32_16x16x128_f8f6f4 v[118:121], v[10:17], v[220:227], v[118:121], v1, v1 op_sel_hi:[0,0,0]
	v_mfma_scale_f32_16x16x128_f8f6f4 v[110:113], v[2:9], v[228:235], v[110:113], v1, v1 op_sel_hi:[0,0,0]
	v_mfma_scale_f32_16x16x128_f8f6f4 v[102:105], v[10:17], v[228:235], v[102:105], v1, v1 op_sel_hi:[0,0,0]
	s_setprio 0
	s_setprio 1
	v_mfma_scale_f32_16x16x128_f8f6f4 v[154:157], v[18:25], v[204:211], v[154:157], v1, v1 op_sel_hi:[0,0,0]
	v_mfma_scale_f32_16x16x128_f8f6f4 v[146:149], v[26:33], v[204:211], v[146:149], v1, v1 op_sel_hi:[0,0,0]
	v_mfma_scale_f32_16x16x128_f8f6f4 v[138:141], v[18:25], v[212:219], v[138:141], v1, v1 op_sel_hi:[0,0,0]
	v_mfma_scale_f32_16x16x128_f8f6f4 v[130:133], v[26:33], v[212:219], v[130:133], v1, v1 op_sel_hi:[0,0,0]
	s_setprio 2
	s_barrier
	v_mfma_scale_f32_16x16x128_f8f6f4 v[122:125], v[18:25], v[220:227], v[122:125], v1, v1 op_sel_hi:[0,0,0]
	v_mfma_scale_f32_16x16x128_f8f6f4 v[114:117], v[26:33], v[220:227], v[114:117], v1, v1 op_sel_hi:[0,0,0]
	v_mfma_scale_f32_16x16x128_f8f6f4 v[106:109], v[18:25], v[228:235], v[106:109], v1, v1 op_sel_hi:[0,0,0]
	v_mfma_scale_f32_16x16x128_f8f6f4 v[98:101], v[26:33], v[228:235], v[98:101], v1, v1 op_sel_hi:[0,0,0]
	s_setprio 0
	s_nop 0
	s_add_i32 s26, s72, s28
	v_lshl_add_u64 v[182:183], v[182:183], 0, s[10:11]
	s_mov_b32 m0, s26
	ds_read_b128 v[204:207], v196 offset:49152
	ds_read_b128 v[208:211], v196 offset:50176
	ds_read_b128 v[212:215], v196 offset:51200
	ds_read_b128 v[216:219], v196 offset:52224
	ds_read_b128 v[220:223], v196 offset:53248
	ds_read_b128 v[224:227], v196 offset:54272
	ds_read_b128 v[228:231], v196 offset:55296
	ds_read_b128 v[232:235], v196 offset:56320
	global_load_lds_dwordx4 v[182:183], off
	s_add_i32 m0, s26, 0x2000
	s_add_u32 s24, s24, 0x40080
	v_lshl_add_u64 v[182:183], v[184:185], 0, s[10:11]
	s_addc_u32 s25, s25, 0
	s_add_i32 s26, s73, s28
	global_load_lds_dwordx4 v[182:183], off
	v_lshl_add_u64 v[182:183], s[24:25], 0, v[166:167]
	s_mov_b32 m0, s26
	s_nop 0
	global_load_lds_dwordx4 v[182:183], off
	v_lshl_add_u64 v[182:183], s[24:25], 0, v[164:165]
	s_add_i32 m0, s26, 0x2000
	s_nop 0
	global_load_lds_dwordx4 v[182:183], off
	v_lshl_add_u64 v[182:183], v[188:189], 0, s[10:11]
	s_mov_b32 m0, s40
	s_nop 0
	global_load_lds_dwordx4 v[182:183], off
	v_lshl_add_u64 v[182:183], v[186:187], 0, s[10:11]
	s_mov_b32 m0, s41
	s_nop 0
	global_load_lds_dwordx4 v[182:183], off
	s_waitcnt vmcnt(8)
	s_waitcnt lgkmcnt(0)
	s_barrier
	s_setprio 1
	s_waitcnt lgkmcnt(0)
	v_mfma_scale_f32_16x16x128_f8f6f4 v[94:97], v[2:9], v[204:211], v[94:97], v1, v1 op_sel_hi:[0,0,0]
	v_mfma_scale_f32_16x16x128_f8f6f4 v[86:89], v[10:17], v[204:211], v[86:89], v1, v1 op_sel_hi:[0,0,0]
	v_mfma_scale_f32_16x16x128_f8f6f4 v[78:81], v[2:9], v[212:219], v[78:81], v1, v1 op_sel_hi:[0,0,0]
	v_mfma_scale_f32_16x16x128_f8f6f4 v[70:73], v[10:17], v[212:219], v[70:73], v1, v1 op_sel_hi:[0,0,0]
	v_mfma_scale_f32_16x16x128_f8f6f4 v[62:65], v[2:9], v[220:227], v[62:65], v1, v1 op_sel_hi:[0,0,0]
	v_mfma_scale_f32_16x16x128_f8f6f4 v[54:57], v[10:17], v[220:227], v[54:57], v1, v1 op_sel_hi:[0,0,0]
	v_mfma_scale_f32_16x16x128_f8f6f4 v[46:49], v[2:9], v[228:235], v[46:49], v1, v1 op_sel_hi:[0,0,0]
	v_mfma_scale_f32_16x16x128_f8f6f4 v[38:41], v[10:17], v[228:235], v[38:41], v1, v1 op_sel_hi:[0,0,0]
	s_setprio 0
	s_setprio 1
	v_mfma_scale_f32_16x16x128_f8f6f4 v[90:93], v[18:25], v[204:211], v[90:93], v1, v1 op_sel_hi:[0,0,0]
	v_mfma_scale_f32_16x16x128_f8f6f4 v[82:85], v[26:33], v[204:211], v[82:85], v1, v1 op_sel_hi:[0,0,0]
	v_mfma_scale_f32_16x16x128_f8f6f4 v[74:77], v[18:25], v[212:219], v[74:77], v1, v1 op_sel_hi:[0,0,0]
	v_mfma_scale_f32_16x16x128_f8f6f4 v[66:69], v[26:33], v[212:219], v[66:69], v1, v1 op_sel_hi:[0,0,0]
	s_setprio 2
	s_barrier
	v_mfma_scale_f32_16x16x128_f8f6f4 v[58:61], v[18:25], v[220:227], v[58:61], v1, v1 op_sel_hi:[0,0,0]
	v_mfma_scale_f32_16x16x128_f8f6f4 v[50:53], v[26:33], v[220:227], v[50:53], v1, v1 op_sel_hi:[0,0,0]
	v_mfma_scale_f32_16x16x128_f8f6f4 v[42:45], v[18:25], v[228:235], v[42:45], v1, v1 op_sel_hi:[0,0,0]
	v_mfma_scale_f32_16x16x128_f8f6f4 v[34:37], v[26:33], v[228:235], v[34:37], v1, v1 op_sel_hi:[0,0,0]
	s_setprio 0
	s_nop 0
	s_add_i32 s71, s71, 2
	s_add_u32 s22, s22, 0x100
	s_addc_u32 s23, s23, 0
	s_cmp_gt_u32 s71, 13
	s_cbranch_scc0 .LBB0_1957
	s_and_b64 vcc, exec, s[14:15]
	s_cbranch_vccz .LBB0_1960
	s_barrier

.LBB0_2038:
	ds_read_b128 v[26:29], v200
	ds_read_b128 v[30:33], v200 offset:1024
	ds_read_b128 v[18:21], v200 offset:2048
	ds_read_b128 v[22:25], v200 offset:3072
	ds_read_b128 v[10:13], v201
	ds_read_b128 v[14:17], v201 offset:1024
	ds_read_b128 v[2:5], v201 offset:2048
	ds_read_b128 v[6:9], v201 offset:3072
	s_add_u32 s38, s36, 0xfff20080
	s_addc_u32 s39, s37, -1
	s_cmp_eq_u32 s79, 52
	s_cselect_b64 vcc, -1, 0
	s_cselect_b32 s39, s7, s39
	s_cselect_b32 s38, s6, s38
	v_cndmask_b32_e32 v183, v181, v179, vcc
	v_cndmask_b32_e32 v182, v180, v178, vcc
	v_lshl_add_u64 v[228:229], s[36:37], 0, v[172:173]
	s_add_i32 m0, s60, 0xc000
	ds_read_b128 v[184:187], v202
	ds_read_b128 v[188:191], v202 offset:1024
	ds_read_b128 v[204:207], v202 offset:2048
	ds_read_b128 v[208:211], v202 offset:3072
	ds_read_b128 v[212:215], v202 offset:4096
	ds_read_b128 v[216:219], v202 offset:5120
	ds_read_b128 v[220:223], v202 offset:6144
	ds_read_b128 v[224:227], v202 offset:7168
	global_load_lds_dwordx4 v[228:229], off
	v_lshl_add_u64 v[228:229], s[36:37], 0, v[174:175]
	s_add_i32 m0, s60, 0xe000
	s_nop 0
	global_load_lds_dwordx4 v[228:229], off
	s_waitcnt vmcnt(8)
	s_waitcnt lgkmcnt(0)
	s_barrier
	s_setprio 1
	s_waitcnt lgkmcnt(0)
	v_mfma_scale_f32_16x16x128_f8f6f4 v[158:161], v[26:33], v[184:191], v[158:161], v196, v196 op_sel_hi:[0,0,0]
	v_mfma_scale_f32_16x16x128_f8f6f4 v[154:157], v[18:25], v[184:191], v[154:157], v196, v196 op_sel_hi:[0,0,0]
	v_mfma_scale_f32_16x16x128_f8f6f4 v[150:153], v[26:33], v[204:211], v[150:153], v196, v196 op_sel_hi:[0,0,0]
	v_mfma_scale_f32_16x16x128_f8f6f4 v[142:145], v[18:25], v[204:211], v[142:145], v196, v196 op_sel_hi:[0,0,0]
	v_mfma_scale_f32_16x16x128_f8f6f4 v[134:137], v[26:33], v[212:219], v[134:137], v196, v196 op_sel_hi:[0,0,0]
	v_mfma_scale_f32_16x16x128_f8f6f4 v[126:129], v[18:25], v[212:219], v[126:129], v196, v196 op_sel_hi:[0,0,0]
	v_mfma_scale_f32_16x16x128_f8f6f4 v[118:121], v[26:33], v[220:227], v[118:121], v196, v196 op_sel_hi:[0,0,0]
	v_mfma_scale_f32_16x16x128_f8f6f4 v[110:113], v[18:25], v[220:227], v[110:113], v196, v196 op_sel_hi:[0,0,0]
	s_setprio 0
	s_setprio 1
	v_mfma_scale_f32_16x16x128_f8f6f4 v[146:149], v[10:17], v[184:191], v[146:149], v196, v196 op_sel_hi:[0,0,0]
	v_mfma_scale_f32_16x16x128_f8f6f4 v[138:141], v[2:9], v[184:191], v[138:141], v196, v196 op_sel_hi:[0,0,0]
	v_mfma_scale_f32_16x16x128_f8f6f4 v[130:133], v[10:17], v[204:211], v[130:133], v196, v196 op_sel_hi:[0,0,0]
	v_mfma_scale_f32_16x16x128_f8f6f4 v[122:125], v[2:9], v[204:211], v[122:125], v196, v196 op_sel_hi:[0,0,0]
	s_setprio 2
	s_barrier
	v_mfma_scale_f32_16x16x128_f8f6f4 v[114:117], v[10:17], v[212:219], v[114:117], v196, v196 op_sel_hi:[0,0,0]
	v_mfma_scale_f32_16x16x128_f8f6f4 v[106:109], v[2:9], v[212:219], v[106:109], v196, v196 op_sel_hi:[0,0,0]
	v_mfma_scale_f32_16x16x128_f8f6f4 v[102:105], v[10:17], v[220:227], v[102:105], v196, v196 op_sel_hi:[0,0,0]
	v_mfma_scale_f32_16x16x128_f8f6f4 v[98:101], v[2:9], v[220:227], v[98:101], v196, v196 op_sel_hi:[0,0,0]
	s_setprio 0
	s_nop 0
	s_add_i32 s80, s69, s25
	v_lshl_add_u64 v[184:185], v[182:183], 0, v[170:171]
	s_mov_b32 m0, s80
	ds_read_b128 v[204:207], v202 offset:16384
	ds_read_b128 v[208:211], v202 offset:17408
	ds_read_b128 v[212:215], v202 offset:18432
	ds_read_b128 v[216:219], v202 offset:19456
	ds_read_b128 v[220:223], v202 offset:20480
	ds_read_b128 v[224:227], v202 offset:21504
	ds_read_b128 v[228:231], v202 offset:22528
	ds_read_b128 v[232:235], v202 offset:23552
	global_load_lds_dwordx4 v[184:185], off
	v_lshl_add_u64 v[186:187], v[182:183], 0, v[168:169]
	s_add_i32 m0, s80, 0x2000
	v_lshl_add_u64 v[188:189], v[182:183], 0, s[10:11]
	s_add_i32 s80, s70, s25
	global_load_lds_dwordx4 v[186:187], off
	v_lshl_add_u64 v[190:191], v[188:189], 0, v[170:171]
	s_mov_b32 m0, s80
	v_lshl_add_u64 v[188:189], v[188:189], 0, v[168:169]
	global_load_lds_dwordx4 v[190:191], off
	s_add_i32 m0, s80, 0x2000
	v_lshl_add_u64 v[190:191], s[38:39], 0, v[166:167]
	global_load_lds_dwordx4 v[188:189], off
	v_lshl_add_u64 v[188:189], s[38:39], 0, v[164:165]
	s_mov_b32 m0, s60
	s_nop 0
	global_load_lds_dwordx4 v[188:189], off
	s_mov_b32 m0, s61
	s_nop 0
	global_load_lds_dwordx4 v[190:191], off
	s_waitcnt vmcnt(8)
	s_waitcnt lgkmcnt(0)
	s_barrier
	s_setprio 1
	s_waitcnt lgkmcnt(0)
	v_mfma_scale_f32_16x16x128_f8f6f4 v[94:97], v[26:33], v[204:211], v[94:97], v196, v196 op_sel_hi:[0,0,0]
	v_mfma_scale_f32_16x16x128_f8f6f4 v[90:93], v[18:25], v[204:211], v[90:93], v196, v196 op_sel_hi:[0,0,0]
	v_mfma_scale_f32_16x16x128_f8f6f4 v[86:89], v[26:33], v[212:219], v[86:89], v196, v196 op_sel_hi:[0,0,0]
	v_mfma_scale_f32_16x16x128_f8f6f4 v[78:81], v[18:25], v[212:219], v[78:81], v196, v196 op_sel_hi:[0,0,0]
	v_mfma_scale_f32_16x16x128_f8f6f4 v[70:73], v[26:33], v[220:227], v[70:73], v196, v196 op_sel_hi:[0,0,0]
	v_mfma_scale_f32_16x16x128_f8f6f4 v[62:65], v[18:25], v[220:227], v[62:65], v196, v196 op_sel_hi:[0,0,0]
	v_mfma_scale_f32_16x16x128_f8f6f4 v[54:57], v[26:33], v[228:235], v[54:57], v196, v196 op_sel_hi:[0,0,0]
	v_mfma_scale_f32_16x16x128_f8f6f4 v[46:49], v[18:25], v[228:235], v[46:49], v196, v196 op_sel_hi:[0,0,0]
	s_setprio 0
	s_setprio 1
	v_mfma_scale_f32_16x16x128_f8f6f4 v[82:85], v[10:17], v[204:211], v[82:85], v196, v196 op_sel_hi:[0,0,0]
	v_mfma_scale_f32_16x16x128_f8f6f4 v[74:77], v[2:9], v[204:211], v[74:77], v196, v196 op_sel_hi:[0,0,0]
	v_mfma_scale_f32_16x16x128_f8f6f4 v[66:69], v[10:17], v[212:219], v[66:69], v196, v196 op_sel_hi:[0,0,0]
	v_mfma_scale_f32_16x16x128_f8f6f4 v[58:61], v[2:9], v[212:219], v[58:61], v196, v196 op_sel_hi:[0,0,0]
	s_setprio 2
	s_barrier
	v_mfma_scale_f32_16x16x128_f8f6f4 v[50:53], v[10:17], v[220:227], v[50:53], v196, v196 op_sel_hi:[0,0,0]
	v_mfma_scale_f32_16x16x128_f8f6f4 v[42:45], v[2:9], v[220:227], v[42:45], v196, v196 op_sel_hi:[0,0,0]
	v_mfma_scale_f32_16x16x128_f8f6f4 v[38:41], v[10:17], v[228:235], v[38:41], v196, v196 op_sel_hi:[0,0,0]
	v_mfma_scale_f32_16x16x128_f8f6f4 v[34:37], v[2:9], v[228:235], v[34:37], v196, v196 op_sel_hi:[0,0,0]
	s_setprio 0
	s_nop 0
	s_add_i32 s80, 0, 0x18000
	s_add_i32 s81, 0, 0x1c000
	v_add_u32_e32 v14, s80, v198
	v_add_u32_e32 v30, s81, v198
	ds_read_b128 v[2:5], v14
	ds_read_b128 v[6:9], v14 offset:1024
	ds_read_b128 v[10:13], v14 offset:2048
	ds_read_b128 v[14:17], v14 offset:3072
	ds_read_b128 v[18:21], v30
	ds_read_b128 v[22:25], v30 offset:1024
	ds_read_b128 v[26:29], v30 offset:2048
	ds_read_b128 v[30:33], v30 offset:3072
	s_add_u32 s38, s38, 0xe0000
	s_addc_u32 s39, s39, 0
	s_mov_b32 m0, s62
	v_lshl_add_u64 v[236:237], s[38:39], 0, v[164:165]
	ds_read_b128 v[204:207], v202 offset:32768
	ds_read_b128 v[208:211], v202 offset:33792
	ds_read_b128 v[212:215], v202 offset:34816
	ds_read_b128 v[216:219], v202 offset:35840
	ds_read_b128 v[220:223], v202 offset:36864
	ds_read_b128 v[224:227], v202 offset:37888
	ds_read_b128 v[228:231], v202 offset:38912
	ds_read_b128 v[232:235], v202 offset:39936
	global_load_lds_dwordx4 v[236:237], off
	v_lshl_add_u64 v[236:237], s[38:39], 0, v[166:167]
	s_mov_b32 m0, s63
	s_nop 0
	global_load_lds_dwordx4 v[236:237], off
	s_waitcnt vmcnt(8)
	s_waitcnt lgkmcnt(0)
	s_barrier
	s_setprio 1
	s_waitcnt lgkmcnt(0)
	v_mfma_scale_f32_16x16x128_f8f6f4 v[158:161], v[2:9], v[204:211], v[158:161], v196, v196 op_sel_hi:[0,0,0]
	v_mfma_scale_f32_16x16x128_f8f6f4 v[154:157], v[10:17], v[204:211], v[154:157], v196, v196 op_sel_hi:[0,0,0]
	v_mfma_scale_f32_16x16x128_f8f6f4 v[150:153], v[2:9], v[212:219], v[150:153], v196, v196 op_sel_hi:[0,0,0]
	v_mfma_scale_f32_16x16x128_f8f6f4 v[142:145], v[10:17], v[212:219], v[142:145], v196, v196 op_sel_hi:[0,0,0]
	v_mfma_scale_f32_16x16x128_f8f6f4 v[134:137], v[2:9], v[220:227], v[134:137], v196, v196 op_sel_hi:[0,0,0]
	v_mfma_scale_f32_16x16x128_f8f6f4 v[126:129], v[10:17], v[220:227], v[126:129], v196, v196 op_sel_hi:[0,0,0]
	v_mfma_scale_f32_16x16x128_f8f6f4 v[118:121], v[2:9], v[228:235], v[118:121], v196, v196 op_sel_hi:[0,0,0]
	v_mfma_scale_f32_16x16x128_f8f6f4 v[110:113], v[10:17], v[228:235], v[110:113], v196, v196 op_sel_hi:[0,0,0]
	s_setprio 0
	s_setprio 1
	v_mfma_scale_f32_16x16x128_f8f6f4 v[146:149], v[18:25], v[204:211], v[146:149], v196, v196 op_sel_hi:[0,0,0]
	v_mfma_scale_f32_16x16x128_f8f6f4 v[138:141], v[26:33], v[204:211], v[138:141], v196, v196 op_sel_hi:[0,0,0]
	v_mfma_scale_f32_16x16x128_f8f6f4 v[130:133], v[18:25], v[212:219], v[130:133], v196, v196 op_sel_hi:[0,0,0]
	v_mfma_scale_f32_16x16x128_f8f6f4 v[122:125], v[26:33], v[212:219], v[122:125], v196, v196 op_sel_hi:[0,0,0]
	s_setprio 2
	s_barrier
	v_mfma_scale_f32_16x16x128_f8f6f4 v[114:117], v[18:25], v[220:227], v[114:117], v196, v196 op_sel_hi:[0,0,0]
	v_mfma_scale_f32_16x16x128_f8f6f4 v[106:109], v[26:33], v[220:227], v[106:109], v196, v196 op_sel_hi:[0,0,0]
	v_mfma_scale_f32_16x16x128_f8f6f4 v[102:105], v[18:25], v[228:235], v[102:105], v196, v196 op_sel_hi:[0,0,0]
	v_mfma_scale_f32_16x16x128_f8f6f4 v[98:101], v[26:33], v[228:235], v[98:101], v196, v196 op_sel_hi:[0,0,0]
	s_setprio 0
	s_nop 0
	s_add_i32 s38, s80, s25
	v_lshl_add_u64 v[184:185], v[184:185], 0, s[16:17]
	s_mov_b32 m0, s38
	ds_read_b128 v[204:207], v202 offset:49152
	ds_read_b128 v[208:211], v202 offset:50176
	ds_read_b128 v[212:215], v202 offset:51200
	ds_read_b128 v[216:219], v202 offset:52224
	ds_read_b128 v[220:223], v202 offset:53248
	ds_read_b128 v[224:227], v202 offset:54272
	ds_read_b128 v[228:231], v202 offset:55296
	ds_read_b128 v[232:235], v202 offset:56320
	global_load_lds_dwordx4 v[184:185], off
	v_lshl_add_u64 v[184:185], v[186:187], 0, s[16:17]
	s_add_i32 m0, s38, 0x2000
	v_lshl_add_u64 v[182:183], v[182:183], 0, s[18:19]
	s_add_i32 s38, s81, s25
	global_load_lds_dwordx4 v[184:185], off
	v_lshl_add_u64 v[184:185], v[182:183], 0, v[170:171]
	s_mov_b32 m0, s38
	v_lshl_add_u64 v[182:183], v[182:183], 0, v[168:169]
	global_load_lds_dwordx4 v[184:185], off
	s_add_i32 m0, s38, 0x2000
	s_nop 0
	global_load_lds_dwordx4 v[182:183], off
	v_lshl_add_u64 v[182:183], v[188:189], 0, s[16:17]
	s_mov_b32 m0, s66
	s_nop 0
	global_load_lds_dwordx4 v[182:183], off
	v_lshl_add_u64 v[182:183], v[190:191], 0, s[16:17]
	s_mov_b32 m0, s67
	s_nop 0
	global_load_lds_dwordx4 v[182:183], off
	s_waitcnt vmcnt(8)
	s_waitcnt lgkmcnt(0)
	s_barrier
	s_setprio 1
	s_waitcnt lgkmcnt(0)
	v_mfma_scale_f32_16x16x128_f8f6f4 v[94:97], v[2:9], v[204:211], v[94:97], v196, v196 op_sel_hi:[0,0,0]
	v_mfma_scale_f32_16x16x128_f8f6f4 v[90:93], v[10:17], v[204:211], v[90:93], v196, v196 op_sel_hi:[0,0,0]
	v_mfma_scale_f32_16x16x128_f8f6f4 v[86:89], v[2:9], v[212:219], v[86:89], v196, v196 op_sel_hi:[0,0,0]
	v_mfma_scale_f32_16x16x128_f8f6f4 v[78:81], v[10:17], v[212:219], v[78:81], v196, v196 op_sel_hi:[0,0,0]
	v_mfma_scale_f32_16x16x128_f8f6f4 v[70:73], v[2:9], v[220:227], v[70:73], v196, v196 op_sel_hi:[0,0,0]
	v_mfma_scale_f32_16x16x128_f8f6f4 v[62:65], v[10:17], v[220:227], v[62:65], v196, v196 op_sel_hi:[0,0,0]
	v_mfma_scale_f32_16x16x128_f8f6f4 v[54:57], v[2:9], v[228:235], v[54:57], v196, v196 op_sel_hi:[0,0,0]
	v_mfma_scale_f32_16x16x128_f8f6f4 v[46:49], v[10:17], v[228:235], v[46:49], v196, v196 op_sel_hi:[0,0,0]
	s_setprio 0
	s_setprio 1
	v_mfma_scale_f32_16x16x128_f8f6f4 v[82:85], v[18:25], v[204:211], v[82:85], v196, v196 op_sel_hi:[0,0,0]
	v_mfma_scale_f32_16x16x128_f8f6f4 v[74:77], v[26:33], v[204:211], v[74:77], v196, v196 op_sel_hi:[0,0,0]
	v_mfma_scale_f32_16x16x128_f8f6f4 v[66:69], v[18:25], v[212:219], v[66:69], v196, v196 op_sel_hi:[0,0,0]
	v_mfma_scale_f32_16x16x128_f8f6f4 v[58:61], v[26:33], v[212:219], v[58:61], v196, v196 op_sel_hi:[0,0,0]
	s_setprio 2
	s_barrier
	v_mfma_scale_f32_16x16x128_f8f6f4 v[50:53], v[18:25], v[220:227], v[50:53], v196, v196 op_sel_hi:[0,0,0]
	v_mfma_scale_f32_16x16x128_f8f6f4 v[42:45], v[26:33], v[220:227], v[42:45], v196, v196 op_sel_hi:[0,0,0]
	v_mfma_scale_f32_16x16x128_f8f6f4 v[38:41], v[18:25], v[228:235], v[38:41], v196, v196 op_sel_hi:[0,0,0]
	v_mfma_scale_f32_16x16x128_f8f6f4 v[34:37], v[26:33], v[228:235], v[34:37], v196, v196 op_sel_hi:[0,0,0]
	s_setprio 0
	s_nop 0
	s_add_i32 s79, s79, 2
	s_add_u32 s36, s36, 0x100
	s_addc_u32 s37, s37, 0
	s_cmp_gt_u32 s79, 53
	v_lshl_add_u64 v[180:181], v[180:181], 0, s[22:23]
	s_cbranch_scc0 .LBB0_2038
	s_and_b64 vcc, exec, s[20:21]
	s_cbranch_vccz .LBB0_2041
	s_barrier

.LBB0_2058:
	ds_read_b128 v[26:29], v1
	ds_read_b128 v[30:33], v1 offset:1024
	ds_read_b128 v[18:21], v1 offset:2048
	ds_read_b128 v[22:25], v1 offset:3072
	ds_read_b128 v[10:13], v190
	ds_read_b128 v[14:17], v190 offset:1024
	ds_read_b128 v[2:5], v190 offset:2048
	ds_read_b128 v[6:9], v190 offset:3072
	s_add_i32 s25, s28, 2
	s_add_u32 s80, s26, 0xfff20080
	s_addc_u32 s29, s27, -1
	s_cmp_eq_u32 s69, s28
	s_cselect_b32 s28, s6, s80
	s_cselect_b64 vcc, -1, 0
	s_cselect_b32 s29, s7, s29
	v_cndmask_b32_e32 v179, v177, v175, vcc
	v_cndmask_b32_e32 v178, v176, v174, vcc
	v_lshl_add_u64 v[218:219], s[26:27], 0, v[168:169]
	s_add_i32 m0, s60, 0xc000
	ds_read_b128 v[180:183], v191
	ds_read_b128 v[184:187], v191 offset:1024
	ds_read_b128 v[194:197], v191 offset:2048
	ds_read_b128 v[198:201], v191 offset:3072
	ds_read_b128 v[202:205], v191 offset:4096
	ds_read_b128 v[206:209], v191 offset:5120
	ds_read_b128 v[210:213], v191 offset:6144
	ds_read_b128 v[214:217], v191 offset:7168
	global_load_lds_dwordx4 v[218:219], off
	v_lshl_add_u64 v[218:219], s[26:27], 0, v[170:171]
	s_add_i32 m0, s60, 0xe000
	s_nop 0
	global_load_lds_dwordx4 v[218:219], off
	s_waitcnt vmcnt(8)
	s_waitcnt lgkmcnt(0)
	s_barrier
	s_setprio 1
	s_waitcnt lgkmcnt(0)
	v_mfma_scale_f32_16x16x128_f8f6f4 v[158:161], v[26:33], v[180:187], v[158:161], v188, v188 op_sel_hi:[0,0,0]
	v_mfma_scale_f32_16x16x128_f8f6f4 v[154:157], v[18:25], v[180:187], v[154:157], v188, v188 op_sel_hi:[0,0,0]
	v_mfma_scale_f32_16x16x128_f8f6f4 v[150:153], v[26:33], v[194:201], v[150:153], v188, v188 op_sel_hi:[0,0,0]
	v_mfma_scale_f32_16x16x128_f8f6f4 v[142:145], v[18:25], v[194:201], v[142:145], v188, v188 op_sel_hi:[0,0,0]
	v_mfma_scale_f32_16x16x128_f8f6f4 v[134:137], v[26:33], v[202:209], v[134:137], v188, v188 op_sel_hi:[0,0,0]
	v_mfma_scale_f32_16x16x128_f8f6f4 v[126:129], v[18:25], v[202:209], v[126:129], v188, v188 op_sel_hi:[0,0,0]
	v_mfma_scale_f32_16x16x128_f8f6f4 v[118:121], v[26:33], v[210:217], v[118:121], v188, v188 op_sel_hi:[0,0,0]
	v_mfma_scale_f32_16x16x128_f8f6f4 v[110:113], v[18:25], v[210:217], v[110:113], v188, v188 op_sel_hi:[0,0,0]
	s_setprio 0
	s_setprio 1
	v_mfma_scale_f32_16x16x128_f8f6f4 v[146:149], v[10:17], v[180:187], v[146:149], v188, v188 op_sel_hi:[0,0,0]
	v_mfma_scale_f32_16x16x128_f8f6f4 v[138:141], v[2:9], v[180:187], v[138:141], v188, v188 op_sel_hi:[0,0,0]
	v_mfma_scale_f32_16x16x128_f8f6f4 v[130:133], v[10:17], v[194:201], v[130:133], v188, v188 op_sel_hi:[0,0,0]
	v_mfma_scale_f32_16x16x128_f8f6f4 v[122:125], v[2:9], v[194:201], v[122:125], v188, v188 op_sel_hi:[0,0,0]
	s_setprio 2
	s_barrier
	v_mfma_scale_f32_16x16x128_f8f6f4 v[114:117], v[10:17], v[202:209], v[114:117], v188, v188 op_sel_hi:[0,0,0]
	v_mfma_scale_f32_16x16x128_f8f6f4 v[106:109], v[2:9], v[202:209], v[106:109], v188, v188 op_sel_hi:[0,0,0]
	v_mfma_scale_f32_16x16x128_f8f6f4 v[102:105], v[10:17], v[210:217], v[102:105], v188, v188 op_sel_hi:[0,0,0]
	v_mfma_scale_f32_16x16x128_f8f6f4 v[98:101], v[2:9], v[210:217], v[98:101], v188, v188 op_sel_hi:[0,0,0]
	s_setprio 0
	s_nop 0
	s_add_i32 s80, s71, s34
	v_lshl_add_u64 v[180:181], v[178:179], 0, v[164:165]
	s_mov_b32 m0, s80
	ds_read_b128 v[194:197], v191 offset:16384
	ds_read_b128 v[198:201], v191 offset:17408
	ds_read_b128 v[202:205], v191 offset:18432
	ds_read_b128 v[206:209], v191 offset:19456
	ds_read_b128 v[210:213], v191 offset:20480
	ds_read_b128 v[214:217], v191 offset:21504
	ds_read_b128 v[218:221], v191 offset:22528
	ds_read_b128 v[222:225], v191 offset:23552
	global_load_lds_dwordx4 v[180:181], off
	v_lshl_add_u64 v[182:183], v[178:179], 0, v[166:167]
	s_add_i32 m0, s80, 0x2000
	v_lshl_add_u64 v[184:185], v[178:179], 0, s[10:11]
	s_add_i32 s80, s72, s34
	global_load_lds_dwordx4 v[182:183], off
	v_lshl_add_u64 v[186:187], v[184:185], 0, v[164:165]
	s_mov_b32 m0, s80
	v_lshl_add_u64 v[184:185], v[184:185], 0, v[166:167]
	global_load_lds_dwordx4 v[186:187], off
	s_add_i32 m0, s80, 0x2000
	v_lshl_add_u64 v[186:187], s[28:29], 0, v[166:167]
	global_load_lds_dwordx4 v[184:185], off
	v_lshl_add_u64 v[184:185], s[28:29], 0, v[164:165]
	s_mov_b32 m0, s60
	s_nop 0
	global_load_lds_dwordx4 v[184:185], off
	s_mov_b32 m0, s61
	s_nop 0
	global_load_lds_dwordx4 v[186:187], off
	s_waitcnt vmcnt(8)
	s_waitcnt lgkmcnt(0)
	s_barrier
	s_setprio 1
	s_waitcnt lgkmcnt(0)
	v_mfma_scale_f32_16x16x128_f8f6f4 v[94:97], v[26:33], v[194:201], v[94:97], v188, v188 op_sel_hi:[0,0,0]
	v_mfma_scale_f32_16x16x128_f8f6f4 v[90:93], v[18:25], v[194:201], v[90:93], v188, v188 op_sel_hi:[0,0,0]
	v_mfma_scale_f32_16x16x128_f8f6f4 v[86:89], v[26:33], v[202:209], v[86:89], v188, v188 op_sel_hi:[0,0,0]
	v_mfma_scale_f32_16x16x128_f8f6f4 v[78:81], v[18:25], v[202:209], v[78:81], v188, v188 op_sel_hi:[0,0,0]
	v_mfma_scale_f32_16x16x128_f8f6f4 v[70:73], v[26:33], v[210:217], v[70:73], v188, v188 op_sel_hi:[0,0,0]
	v_mfma_scale_f32_16x16x128_f8f6f4 v[62:65], v[18:25], v[210:217], v[62:65], v188, v188 op_sel_hi:[0,0,0]
	v_mfma_scale_f32_16x16x128_f8f6f4 v[54:57], v[26:33], v[218:225], v[54:57], v188, v188 op_sel_hi:[0,0,0]
	v_mfma_scale_f32_16x16x128_f8f6f4 v[46:49], v[18:25], v[218:225], v[46:49], v188, v188 op_sel_hi:[0,0,0]
	s_setprio 0
	s_setprio 1
	v_mfma_scale_f32_16x16x128_f8f6f4 v[82:85], v[10:17], v[194:201], v[82:85], v188, v188 op_sel_hi:[0,0,0]
	v_mfma_scale_f32_16x16x128_f8f6f4 v[74:77], v[2:9], v[194:201], v[74:77], v188, v188 op_sel_hi:[0,0,0]
	v_mfma_scale_f32_16x16x128_f8f6f4 v[66:69], v[10:17], v[202:209], v[66:69], v188, v188 op_sel_hi:[0,0,0]
	v_mfma_scale_f32_16x16x128_f8f6f4 v[58:61], v[2:9], v[202:209], v[58:61], v188, v188 op_sel_hi:[0,0,0]
	s_setprio 2
	s_barrier
	v_mfma_scale_f32_16x16x128_f8f6f4 v[50:53], v[10:17], v[210:217], v[50:53], v188, v188 op_sel_hi:[0,0,0]
	v_mfma_scale_f32_16x16x128_f8f6f4 v[42:45], v[2:9], v[210:217], v[42:45], v188, v188 op_sel_hi:[0,0,0]
	v_mfma_scale_f32_16x16x128_f8f6f4 v[38:41], v[10:17], v[218:225], v[38:41], v188, v188 op_sel_hi:[0,0,0]
	v_mfma_scale_f32_16x16x128_f8f6f4 v[34:37], v[2:9], v[218:225], v[34:37], v188, v188 op_sel_hi:[0,0,0]
	s_setprio 0
	s_nop 0
	s_add_i32 s80, 0, 0x18000
	s_add_i32 s81, 0, 0x1c000
	v_add_u32_e32 v14, s80, v189
	v_add_u32_e32 v30, s81, v189
	ds_read_b128 v[2:5], v14
	ds_read_b128 v[6:9], v14 offset:1024
	ds_read_b128 v[10:13], v14 offset:2048
	ds_read_b128 v[14:17], v14 offset:3072
	ds_read_b128 v[18:21], v30
	ds_read_b128 v[22:25], v30 offset:1024
	ds_read_b128 v[26:29], v30 offset:2048
	ds_read_b128 v[30:33], v30 offset:3072
	s_add_u32 s28, s28, 0xe0000
	s_addc_u32 s29, s29, 0
	s_mov_b32 m0, s62
	v_lshl_add_u64 v[226:227], s[28:29], 0, v[164:165]
	ds_read_b128 v[194:197], v191 offset:32768
	ds_read_b128 v[198:201], v191 offset:33792
	ds_read_b128 v[202:205], v191 offset:34816
	ds_read_b128 v[206:209], v191 offset:35840
	ds_read_b128 v[210:213], v191 offset:36864
	ds_read_b128 v[214:217], v191 offset:37888
	ds_read_b128 v[218:221], v191 offset:38912
	ds_read_b128 v[222:225], v191 offset:39936
	global_load_lds_dwordx4 v[226:227], off
	v_lshl_add_u64 v[226:227], s[28:29], 0, v[166:167]
	s_mov_b32 m0, s63
	s_nop 0
	global_load_lds_dwordx4 v[226:227], off
	s_waitcnt vmcnt(8)
	s_waitcnt lgkmcnt(0)
	s_barrier
	s_setprio 1
	s_waitcnt lgkmcnt(0)
	v_mfma_scale_f32_16x16x128_f8f6f4 v[158:161], v[2:9], v[194:201], v[158:161], v188, v188 op_sel_hi:[0,0,0]
	v_mfma_scale_f32_16x16x128_f8f6f4 v[154:157], v[10:17], v[194:201], v[154:157], v188, v188 op_sel_hi:[0,0,0]
	v_mfma_scale_f32_16x16x128_f8f6f4 v[150:153], v[2:9], v[202:209], v[150:153], v188, v188 op_sel_hi:[0,0,0]
	v_mfma_scale_f32_16x16x128_f8f6f4 v[142:145], v[10:17], v[202:209], v[142:145], v188, v188 op_sel_hi:[0,0,0]
	v_mfma_scale_f32_16x16x128_f8f6f4 v[134:137], v[2:9], v[210:217], v[134:137], v188, v188 op_sel_hi:[0,0,0]
	v_mfma_scale_f32_16x16x128_f8f6f4 v[126:129], v[10:17], v[210:217], v[126:129], v188, v188 op_sel_hi:[0,0,0]
	v_mfma_scale_f32_16x16x128_f8f6f4 v[118:121], v[2:9], v[218:225], v[118:121], v188, v188 op_sel_hi:[0,0,0]
	v_mfma_scale_f32_16x16x128_f8f6f4 v[110:113], v[10:17], v[218:225], v[110:113], v188, v188 op_sel_hi:[0,0,0]
	s_setprio 0
	s_setprio 1
	v_mfma_scale_f32_16x16x128_f8f6f4 v[146:149], v[18:25], v[194:201], v[146:149], v188, v188 op_sel_hi:[0,0,0]
	v_mfma_scale_f32_16x16x128_f8f6f4 v[138:141], v[26:33], v[194:201], v[138:141], v188, v188 op_sel_hi:[0,0,0]
	v_mfma_scale_f32_16x16x128_f8f6f4 v[130:133], v[18:25], v[202:209], v[130:133], v188, v188 op_sel_hi:[0,0,0]
	v_mfma_scale_f32_16x16x128_f8f6f4 v[122:125], v[26:33], v[202:209], v[122:125], v188, v188 op_sel_hi:[0,0,0]
	s_setprio 2
	s_barrier
	v_mfma_scale_f32_16x16x128_f8f6f4 v[114:117], v[18:25], v[210:217], v[114:117], v188, v188 op_sel_hi:[0,0,0]
	v_mfma_scale_f32_16x16x128_f8f6f4 v[106:109], v[26:33], v[210:217], v[106:109], v188, v188 op_sel_hi:[0,0,0]
	v_mfma_scale_f32_16x16x128_f8f6f4 v[102:105], v[18:25], v[218:225], v[102:105], v188, v188 op_sel_hi:[0,0,0]
	v_mfma_scale_f32_16x16x128_f8f6f4 v[98:101], v[26:33], v[218:225], v[98:101], v188, v188 op_sel_hi:[0,0,0]
	s_setprio 0
	s_nop 0
	s_add_i32 s28, s80, s34
	v_lshl_add_u64 v[180:181], v[180:181], 0, s[14:15]
	s_mov_b32 m0, s28
	ds_read_b128 v[194:197], v191 offset:49152
	ds_read_b128 v[198:201], v191 offset:50176
	ds_read_b128 v[202:205], v191 offset:51200
	ds_read_b128 v[206:209], v191 offset:52224
	ds_read_b128 v[210:213], v191 offset:53248
	ds_read_b128 v[214:217], v191 offset:54272
	ds_read_b128 v[218:221], v191 offset:55296
	ds_read_b128 v[222:225], v191 offset:56320
	global_load_lds_dwordx4 v[180:181], off
	v_lshl_add_u64 v[180:181], v[182:183], 0, s[14:15]
	s_add_i32 m0, s28, 0x2000
	v_lshl_add_u64 v[178:179], v[178:179], 0, s[16:17]
	s_add_i32 s28, s81, s34
	global_load_lds_dwordx4 v[180:181], off
	v_lshl_add_u64 v[180:181], v[178:179], 0, v[164:165]
	s_mov_b32 m0, s28
	v_lshl_add_u64 v[178:179], v[178:179], 0, v[166:167]
	global_load_lds_dwordx4 v[180:181], off
	s_add_i32 m0, s28, 0x2000
	s_nop 0
	global_load_lds_dwordx4 v[178:179], off
	v_lshl_add_u64 v[178:179], v[184:185], 0, s[14:15]
	s_mov_b32 m0, s65
	s_nop 0
	global_load_lds_dwordx4 v[178:179], off
	v_lshl_add_u64 v[178:179], v[186:187], 0, s[14:15]
	s_mov_b32 m0, s66
	s_nop 0
	global_load_lds_dwordx4 v[178:179], off
	s_waitcnt vmcnt(8)
	s_waitcnt lgkmcnt(0)
	s_barrier
	s_setprio 1
	s_waitcnt lgkmcnt(0)
	v_mfma_scale_f32_16x16x128_f8f6f4 v[94:97], v[2:9], v[194:201], v[94:97], v188, v188 op_sel_hi:[0,0,0]
	v_mfma_scale_f32_16x16x128_f8f6f4 v[90:93], v[10:17], v[194:201], v[90:93], v188, v188 op_sel_hi:[0,0,0]
	v_mfma_scale_f32_16x16x128_f8f6f4 v[86:89], v[2:9], v[202:209], v[86:89], v188, v188 op_sel_hi:[0,0,0]
	v_mfma_scale_f32_16x16x128_f8f6f4 v[78:81], v[10:17], v[202:209], v[78:81], v188, v188 op_sel_hi:[0,0,0]
	v_mfma_scale_f32_16x16x128_f8f6f4 v[70:73], v[2:9], v[210:217], v[70:73], v188, v188 op_sel_hi:[0,0,0]
	v_mfma_scale_f32_16x16x128_f8f6f4 v[62:65], v[10:17], v[210:217], v[62:65], v188, v188 op_sel_hi:[0,0,0]
	v_mfma_scale_f32_16x16x128_f8f6f4 v[54:57], v[2:9], v[218:225], v[54:57], v188, v188 op_sel_hi:[0,0,0]
	v_mfma_scale_f32_16x16x128_f8f6f4 v[46:49], v[10:17], v[218:225], v[46:49], v188, v188 op_sel_hi:[0,0,0]
	s_setprio 0
	s_setprio 1
	v_mfma_scale_f32_16x16x128_f8f6f4 v[82:85], v[18:25], v[194:201], v[82:85], v188, v188 op_sel_hi:[0,0,0]
	v_mfma_scale_f32_16x16x128_f8f6f4 v[74:77], v[26:33], v[194:201], v[74:77], v188, v188 op_sel_hi:[0,0,0]
	v_mfma_scale_f32_16x16x128_f8f6f4 v[66:69], v[18:25], v[202:209], v[66:69], v188, v188 op_sel_hi:[0,0,0]
	v_mfma_scale_f32_16x16x128_f8f6f4 v[58:61], v[26:33], v[202:209], v[58:61], v188, v188 op_sel_hi:[0,0,0]
	s_setprio 2
	s_barrier
	v_mfma_scale_f32_16x16x128_f8f6f4 v[50:53], v[18:25], v[210:217], v[50:53], v188, v188 op_sel_hi:[0,0,0]
	v_mfma_scale_f32_16x16x128_f8f6f4 v[42:45], v[26:33], v[210:217], v[42:45], v188, v188 op_sel_hi:[0,0,0]
	v_mfma_scale_f32_16x16x128_f8f6f4 v[38:41], v[18:25], v[218:225], v[38:41], v188, v188 op_sel_hi:[0,0,0]
	v_mfma_scale_f32_16x16x128_f8f6f4 v[34:37], v[26:33], v[218:225], v[34:37], v188, v188 op_sel_hi:[0,0,0]
	s_setprio 0
	s_nop 0
	s_add_u32 s26, s26, 0x100
	s_addc_u32 s27, s27, 0
	v_lshl_add_u64 v[176:177], v[176:177], 0, s[22:23]
	s_cmp_ge_u32 s25, s67
	s_mov_b32 s28, s25
	s_cbranch_scc0 .LBB0_2058
	s_and_b64 vcc, exec, s[20:21]
	s_cbranch_vccz .LBB0_2061
	s_barrier
